# v37 + nt hint on the streaming stores of the norm, prep2 and layer-0 combine phases
# baseline (speedup 1.0000x reference)
.LBB0_171:
	global_load_dwordx4 v[44:47], v28, s[12:13]
	global_load_dwordx4 v[24:27], v28, s[12:13] offset:1024
	global_load_dwordx4 v[16:19], v28, s[12:13] offset:3072
	global_load_dwordx4 v[20:23], v28, s[12:13] offset:2048
	v_lshl_add_u64 v[0:1], s[12:13], 0, v[28:29]
	v_add_co_u32_e32 v34, vcc, s18, v0
	s_lshl_b64 s[12:13], s[10:11], 11
	s_nop 0
	v_addc_co_u32_e32 v35, vcc, 0, v1, vcc
	global_load_dwordx4 v[8:11], v[34:35], off offset:1024
	global_load_dwordx4 v[12:15], v[34:35], off
	global_load_dwordx4 v[0:3], v[34:35], off offset:3072
	global_load_dwordx4 v[4:7], v[34:35], off offset:2048
	s_lshl_b64 s[10:11], s[10:11], 12
	v_lshl_add_u64 v[34:35], v[32:33], 0, s[12:13]
	v_lshl_add_u64 v[36:37], v[30:31], 0, s[10:11]
	s_min_i32 s4, s0, 0x2000
	s_lshl_b32 s4, s4, 1
	s_and_b32 s4, s4, 0xffffe000
	v_add_u32_e32 v68, s4, v39
	v_mov_b32_e32 v43, 0
	s_add_u32 s0, s0, s2
	s_addc_u32 s1, s1, s3
	s_add_u32 s6, s6, s8
	s_addc_u32 s7, s7, s9
	s_cmpk_lt_i32 s0, 0x2200
	s_waitcnt vmcnt(7)
	v_mul_f32_e32 v69, v45, v45
	s_waitcnt vmcnt(6)
	v_mul_f32_e32 v70, v25, v25
	s_waitcnt vmcnt(5)
	v_mov_b32_e32 v50, v17
	s_waitcnt vmcnt(4)
	v_mov_b32_e32 v51, v21
	v_mov_b32_e32 v48, v16
	v_mov_b32_e32 v49, v20
	v_fmac_f32_e32 v69, v44, v44
	v_fmac_f32_e32 v70, v24, v24
	v_pk_mul_f32 v[50:51], v[50:51], v[50:51]
	v_mov_b32_e32 v52, v18
	v_mov_b32_e32 v53, v22
	v_fmac_f32_e32 v69, v46, v46
	v_fmac_f32_e32 v70, v26, v26
	v_pk_fma_f32 v[48:49], v[48:49], v[48:49], v[50:51]
	v_mov_b32_e32 v54, v19
	v_mov_b32_e32 v55, v23
	v_fmac_f32_e32 v69, v47, v47
	v_fmac_f32_e32 v70, v27, v27
	v_pk_fma_f32 v[48:49], v[52:53], v[52:53], v[48:49]
	s_waitcnt vmcnt(3)
	v_mov_b32_e32 v52, v9
	s_waitcnt vmcnt(2)
	v_mov_b32_e32 v53, v13
	v_mov_b32_e32 v50, v8
	v_mov_b32_e32 v51, v12
	s_waitcnt vmcnt(1)
	v_mov_b32_e32 v62, v1
	s_waitcnt vmcnt(0)
	v_mov_b32_e32 v63, v5
	v_add_f32_e32 v69, v69, v70
	v_pk_fma_f32 v[48:49], v[54:55], v[54:55], v[48:49]
	v_pk_mul_f32 v[52:53], v[52:53], v[52:53]
	v_mov_b32_e32 v56, v10
	v_mov_b32_e32 v57, v14
	v_mov_b32_e32 v60, v0
	v_mov_b32_e32 v61, v4
	v_pk_mul_f32 v[54:55], v[62:63], v[62:63]
	v_add_f32_e32 v49, v49, v69
	v_pk_fma_f32 v[50:51], v[50:51], v[50:51], v[52:53]
	v_mov_b32_e32 v58, v11
	v_mov_b32_e32 v59, v15
	v_pk_fma_f32 v[52:53], v[60:61], v[60:61], v[54:55]
	v_add_f32_e32 v54, v48, v49
	v_pk_fma_f32 v[48:49], v[56:57], v[56:57], v[50:51]
	v_mov_b32_e32 v64, v2
	v_mov_b32_e32 v65, v6
	v_pk_fma_f32 v[48:49], v[58:59], v[58:59], v[48:49]
	v_mov_b32_e32 v66, v3
	v_mov_b32_e32 v67, v7
	v_pk_fma_f32 v[50:51], v[64:65], v[64:65], v[52:53]
	v_add_f32_e32 v49, v49, v54
	v_pk_fma_f32 v[50:51], v[66:67], v[66:67], v[50:51]
	v_add_f32_e32 v48, v48, v49
	v_add_f32_e32 v48, v51, v48
	v_add_f32_e32 v48, v50, v48
	v_mov_b32_e32 v49, v48
	v_add_u32_e32 v57, s4, v40
	s_nop 0
	v_mov_b32_dpp v49, v49 quad_perm:[1,0,3,2] row_mask:0xf bank_mask:0xf
	v_add_f32_e32 v48, v48, v49
	v_mov_b32_e32 v49, v48
	s_nop 1
	v_mov_b32_dpp v49, v49 quad_perm:[2,3,0,1] row_mask:0xf bank_mask:0xf
	v_add_f32_e32 v48, v48, v49
	v_mov_b32_e32 v49, v48
	s_nop 1
	v_mov_b32_dpp v49, v49 row_half_mirror row_mask:0xf bank_mask:0xf
	v_add_f32_e32 v48, v48, v49
	v_mov_b32_e32 v49, v48
	s_nop 1
	v_mov_b32_dpp v49, v49 row_mirror row_mask:0xf bank_mask:0xf
	v_add_f32_e32 v48, v48, v49
	s_nop 0
	v_readlane_b32 s12, v48, 16
	v_readlane_b32 s13, v48, 48
	v_readlane_b32 s10, v48, 0
	v_readlane_b32 s11, v48, 32
	v_mov_b32_e32 v48, s12
	v_mov_b32_e32 v49, s13
	v_pk_add_f32 v[48:49], s[10:11], v[48:49]
	s_nop 0
	v_add_f32_e32 v48, v48, v49
	v_fmamk_f32 v48, v48, 0x3a000000, v41
	v_mul_f32_e32 v49, 0x4b800000, v48
	v_cmp_gt_f32_e32 vcc, s19, v48
	s_nop 1
	v_cndmask_b32_e32 v48, v48, v49, vcc
	v_rsq_f32_e32 v56, v48
	ds_read_b128 v[48:51], v68
	ds_read_b128 v[52:55], v57
	v_mul_f32_e32 v58, 0x45800000, v56
	v_cndmask_b32_e32 v56, v56, v58, vcc
	v_mul_f32_e32 v44, v44, v56
	v_mul_f32_e32 v45, v45, v56
	s_waitcnt lgkmcnt(0)
	v_fma_f32 v44, v48, v44, v52
	v_fma_f32 v45, v49, v45, v53
	v_mul_f32_e32 v58, v24, v56
	v_cvt_pk_bf16_f32 v24, v44, v45
	v_med3_f32 v44, v44, s20, v42
	v_med3_f32 v45, v45, s20, v42
	v_cvt_pk_fp8_f32 v43, v44, v45
	v_mul_f32_e32 v46, v46, v56
	v_mul_f32_e32 v47, v47, v56
	v_mul_f32_e32 v59, v25, v56
	v_fma_f32 v52, v50, v46, v54
	v_fmac_f32_e32 v55, v51, v47
	v_cvt_pk_bf16_f32 v25, v52, v55
	ds_read_b128 v[44:47], v68 offset:1024
	ds_read_b128 v[48:51], v57 offset:1024
	v_med3_f32 v52, v52, s20, v42
	v_med3_f32 v53, v55, s20, v42
	v_cvt_pk_fp8_f32 v43, v52, v53 op_sel:[0,0,1]
	global_store_dwordx2 v[36:37], v[24:25], off nt
	s_waitcnt lgkmcnt(0)
	v_fma_f32 v24, v44, v58, v48
	v_fma_f32 v25, v45, v59, v49
	global_store_dword v[34:35], v43, off nt
	v_cvt_pk_bf16_f32 v48, v24, v25
	v_med3_f32 v24, v24, s20, v42
	v_med3_f32 v25, v25, s20, v42
	v_mov_b32_e32 v43, 0
	v_cvt_pk_fp8_f32 v43, v24, v25
	v_mul_f32_e32 v26, v26, v56
	v_mul_f32_e32 v27, v27, v56
	v_fma_f32 v26, v46, v26, v50
	v_fmac_f32_e32 v51, v47, v27
	v_med3_f32 v24, v26, s20, v42
	v_med3_f32 v25, v51, s20, v42
	v_cvt_pk_bf16_f32 v49, v26, v51
	v_cvt_pk_fp8_f32 v43, v24, v25 op_sel:[0,0,1]
	ds_read_b128 v[24:27], v68 offset:2048
	ds_read_b128 v[44:47], v57 offset:2048
	v_mul_f32_e32 v20, v20, v56
	v_mul_f32_e32 v21, v21, v56
	global_store_dwordx2 v[36:37], v[48:49], off offset:512 nt
	global_store_dword v[34:35], v43, off offset:256 nt
	v_mov_b32_e32 v43, 0
	s_waitcnt lgkmcnt(0)
	v_fma_f32 v20, v20, v24, v44
	v_fma_f32 v21, v21, v25, v45
	v_cvt_pk_bf16_f32 v44, v20, v21
	v_med3_f32 v20, v20, s20, v42
	v_med3_f32 v21, v21, s20, v42
	v_cvt_pk_fp8_f32 v43, v20, v21
	v_mul_f32_e32 v22, v22, v56
	v_mul_f32_e32 v23, v23, v56
	v_fma_f32 v22, v22, v26, v46
	v_fmac_f32_e32 v47, v23, v27
	v_med3_f32 v20, v22, s20, v42
	v_med3_f32 v21, v47, s20, v42
	v_cvt_pk_bf16_f32 v45, v22, v47
	v_cvt_pk_fp8_f32 v43, v20, v21 op_sel:[0,0,1]
	ds_read_b128 v[20:23], v68 offset:3072
	ds_read_b128 v[24:27], v57 offset:3072
	v_mul_f32_e32 v16, v16, v56
	v_mul_f32_e32 v17, v17, v56
	v_mul_f32_e32 v18, v18, v56
	global_store_dwordx2 v[36:37], v[44:45], off offset:1024 nt
	global_store_dword v[34:35], v43, off offset:512 nt
	s_waitcnt lgkmcnt(0)
	v_fma_f32 v16, v16, v20, v24
	v_fma_f32 v17, v17, v21, v25
	v_fma_f32 v18, v18, v22, v26
	v_cvt_pk_bf16_f32 v24, v16, v17
	v_med3_f32 v16, v16, s20, v42
	v_med3_f32 v17, v17, s20, v42
	v_mov_b32_e32 v26, 0
	v_cvt_pk_fp8_f32 v26, v16, v17
	v_mul_f32_e32 v19, v19, v56
	v_fmac_f32_e32 v27, v19, v23
	v_med3_f32 v16, v18, s20, v42
	v_med3_f32 v17, v27, s20, v42
	v_cvt_pk_bf16_f32 v25, v18, v27
	v_cvt_pk_fp8_f32 v26, v16, v17 op_sel:[0,0,1]
	ds_read_b128 v[16:19], v68 offset:4096
	ds_read_b128 v[20:23], v57 offset:4096
	v_mul_f32_e32 v12, v12, v56
	v_mul_f32_e32 v13, v13, v56
	v_mul_f32_e32 v14, v14, v56
	global_store_dwordx2 v[36:37], v[24:25], off offset:1536 nt
	global_store_dword v[34:35], v26, off offset:768 nt
	s_waitcnt lgkmcnt(0)
	v_fma_f32 v12, v12, v16, v20
	v_fma_f32 v13, v13, v17, v21
	v_fma_f32 v14, v14, v18, v22
	v_cvt_pk_bf16_f32 v20, v12, v13
	v_med3_f32 v12, v12, s20, v42
	v_med3_f32 v13, v13, s20, v42
	v_mov_b32_e32 v22, 0
	v_cvt_pk_fp8_f32 v22, v12, v13
	v_mul_f32_e32 v15, v15, v56
	v_fmac_f32_e32 v23, v15, v19
	v_med3_f32 v12, v14, s20, v42
	v_med3_f32 v13, v23, s20, v42
	v_cvt_pk_bf16_f32 v21, v14, v23
	v_cvt_pk_fp8_f32 v22, v12, v13 op_sel:[0,0,1]
	ds_read_b128 v[12:15], v68 offset:5120
	ds_read_b128 v[16:19], v57 offset:5120
	v_mul_f32_e32 v8, v8, v56
	v_mul_f32_e32 v9, v9, v56
	v_mul_f32_e32 v10, v10, v56
	global_store_dwordx2 v[36:37], v[20:21], off offset:2048 nt
	global_store_dword v[34:35], v22, off offset:1024 nt
	s_waitcnt lgkmcnt(0)
	v_fma_f32 v8, v8, v12, v16
	v_fma_f32 v9, v9, v13, v17
	v_fma_f32 v10, v10, v14, v18
	v_cvt_pk_bf16_f32 v16, v8, v9
	v_med3_f32 v8, v8, s20, v42
	v_med3_f32 v9, v9, s20, v42
	v_mov_b32_e32 v18, 0
	v_cvt_pk_fp8_f32 v18, v8, v9
	v_mul_f32_e32 v11, v11, v56
	v_fmac_f32_e32 v19, v11, v15
	v_med3_f32 v8, v10, s20, v42
	v_med3_f32 v9, v19, s20, v42
	v_cvt_pk_bf16_f32 v17, v10, v19
	v_cvt_pk_fp8_f32 v18, v8, v9 op_sel:[0,0,1]
	ds_read_b128 v[8:11], v68 offset:6144
	ds_read_b128 v[12:15], v57 offset:6144
	v_mul_f32_e32 v4, v4, v56
	v_mul_f32_e32 v5, v5, v56
	v_mul_f32_e32 v6, v6, v56
	global_store_dwordx2 v[36:37], v[16:17], off offset:2560 nt
	global_store_dword v[34:35], v18, off offset:1280 nt
	s_waitcnt lgkmcnt(0)
	v_fma_f32 v4, v4, v8, v12
	v_fma_f32 v5, v5, v9, v13
	v_fma_f32 v6, v6, v10, v14
	v_cvt_pk_bf16_f32 v12, v4, v5
	v_med3_f32 v4, v4, s20, v42
	v_med3_f32 v5, v5, s20, v42
	v_mov_b32_e32 v14, 0
	v_cvt_pk_fp8_f32 v14, v4, v5
	v_mul_f32_e32 v7, v7, v56
	v_fmac_f32_e32 v15, v7, v11
	v_med3_f32 v4, v6, s20, v42
	v_med3_f32 v5, v15, s20, v42
	v_cvt_pk_bf16_f32 v13, v6, v15
	v_cvt_pk_fp8_f32 v14, v4, v5 op_sel:[0,0,1]
	ds_read_b128 v[4:7], v68 offset:7168
	ds_read_b128 v[8:11], v57 offset:7168
	v_mul_f32_e32 v0, v0, v56
	global_store_dwordx2 v[36:37], v[12:13], off offset:3072 nt
	global_store_dword v[34:35], v14, off offset:1536 nt
	s_waitcnt lgkmcnt(0)
	v_fma_f32 v4, v0, v4, v8
	v_mul_f32_e32 v0, v1, v56
	v_fma_f32 v5, v0, v5, v9
	v_mul_f32_e32 v0, v2, v56
	v_fma_f32 v2, v0, v6, v10
	v_mul_f32_e32 v0, v3, v56
	v_fmac_f32_e32 v11, v0, v7
	v_cvt_pk_bf16_f32 v0, v4, v5
	v_med3_f32 v3, v4, s20, v42
	v_med3_f32 v4, v5, s20, v42
	v_mov_b32_e32 v5, 0
	v_cvt_pk_fp8_f32 v5, v3, v4
	v_cvt_pk_bf16_f32 v1, v2, v11
	global_store_dwordx2 v[36:37], v[0:1], off offset:3584 nt
	v_med3_f32 v0, v2, s20, v42
	v_med3_f32 v1, v11, s20, v42
	v_cvt_pk_fp8_f32 v5, v0, v1 op_sel:[0,0,1]
	global_store_dword v[34:35], v5, off offset:1792 nt
	s_cbranch_scc0 .LBB0_174

.LBB0_468:
	s_waitcnt vmcnt(2)
	v_mul_f32_e32 v60, v60, v106
	v_mul_f32_e32 v48, v48, v106
	v_mul_f32_e32 v60, v60, v92
	v_mul_f32_e32 v92, v48, v102
	v_mul_f32_e32 v48, v52, v106
	v_mul_f32_e32 v52, v48, v104
	v_mul_f32_e32 v48, v49, v106
	v_mul_f32_e32 v49, v48, v103
	v_mul_f32_e32 v48, v53, v106
	v_mul_f32_e32 v53, v48, v105
	v_mul_f32_e32 v48, v50, v106
	v_mul_f32_e32 v50, v48, v85
	v_mul_f32_e32 v48, v106, v54
	v_mul_f32_e32 v56, v56, v106
	v_mul_f32_e32 v57, v57, v106
	v_mul_f32_e32 v54, v48, v83
	v_mul_f32_e32 v48, v106, v51
	v_mul_f32_e32 v56, v56, v94
	v_mul_f32_e32 v57, v57, v95
	v_mul_f32_e32 v51, v48, v84
	v_mul_f32_e32 v48, v106, v55
	v_mul_f32_e32 v55, v48, v82
	v_med3_f32 v56, v56, s58, v112
	v_med3_f32 v57, v57, s58, v112
	v_mov_b32_e32 v48, 0
	v_cvt_pk_fp8_f32 v48, v56, v57
	v_med3_f32 v56, v92, s58, v112
	v_med3_f32 v57, v49, s58, v112
	v_mov_b32_e32 v49, 0
	v_cvt_pk_fp8_f32 v49, v56, v57
	v_mul_f32_e32 v61, v61, v106
	v_mul_f32_e32 v61, v61, v93
	v_med3_f32 v50, v50, s58, v112
	v_med3_f32 v51, v51, s58, v112
	v_cvt_pk_fp8_f32 v49, v50, v51 op_sel:[0,0,1]
	v_med3_f32 v51, v60, s58, v112
	v_med3_f32 v56, v61, s58, v112
	v_mov_b32_e32 v50, 0
	v_cvt_pk_fp8_f32 v50, v51, v56
	v_med3_f32 v52, v52, s58, v112
	v_med3_f32 v53, v53, s58, v112
	v_mov_b32_e32 v51, 0
	v_cvt_pk_fp8_f32 v51, v52, v53
	v_med3_f32 v52, v54, s58, v112
	v_med3_f32 v53, v55, s58, v112
	v_max_f32_e32 v55, v90, v90
	v_cvt_pk_fp8_f32 v51, v52, v53 op_sel:[0,0,1]
	v_max_f32_e32 v52, v96, v96
	v_med3_f32 v53, v52, s58, v112
	v_max_f32_e32 v52, v97, v97
	v_med3_f32 v54, v52, s58, v112
	v_mov_b32_e32 v52, 0
	v_cvt_pk_fp8_f32 v52, v53, v54
	v_max_f32_e32 v54, v91, v91
	v_med3_f32 v53, v55, s58, v112
	v_med3_f32 v54, v54, s58, v112
	v_cvt_pk_fp8_f32 v52, v53, v54 op_sel:[0,0,1]
	v_max_f32_e32 v53, v88, v88
	v_med3_f32 v54, v53, s58, v112
	v_max_f32_e32 v53, v89, v89
	v_mul_f32_e32 v58, v58, v106
	v_mul_f32_e32 v59, v59, v106
	v_med3_f32 v55, v53, s58, v112
	v_mov_b32_e32 v53, 0
	v_mul_f32_e32 v58, v58, v98
	v_mul_f32_e32 v62, v62, v106
	v_mul_f32_e32 v59, v59, v99
	v_mul_f32_e32 v63, v63, v106
	v_cvt_pk_fp8_f32 v53, v54, v55
	v_mul_f32_e32 v62, v62, v100
	v_mul_f32_e32 v63, v63, v101
	v_med3_f32 v58, v58, s58, v112
	v_med3_f32 v59, v59, s58, v112
	v_cvt_pk_fp8_f32 v48, v58, v59 op_sel:[0,0,1]
	v_med3_f32 v57, v62, s58, v112
	v_med3_f32 v58, v63, s58, v112
	v_max_f32_e32 v56, v86, v86
	v_max_f32_e32 v55, v87, v87
	v_cvt_pk_fp8_f32 v50, v57, v58 op_sel:[0,0,1]
	v_med3_f32 v54, v56, s58, v112
	v_med3_f32 v55, v55, s58, v112
	v_cvt_pk_fp8_f32 v53, v54, v55 op_sel:[0,0,1]
	v_lshl_add_u64 v[54:55], s[8:9], 0, v[74:75]
	global_store_dwordx2 v[54:55], v[48:49], off offset:-64 nt
	global_store_dwordx2 v[54:55], v[50:51], off nt
	global_store_dwordx2 v[54:55], v[52:53], off offset:64 nt
	s_andn2_b64 vcc, exec, s[30:31]
	s_cbranch_vccnz .LBB0_472

.LBB0_475:
	s_and_b64 vcc, exec, s[2:3]
	s_cbranch_vccnz .LBB0_478
	s_waitcnt vmcnt(2)
	v_mul_f32_e32 v45, v45, v82
	v_mul_f32_e32 v47, v82, v47
	v_mul_f32_e32 v36, v82, v36
	v_mul_f32_e32 v37, v82, v37
	v_mul_f32_e32 v45, v45, v59
	v_mul_f32_e32 v33, v47, v33
	v_mul_f32_e32 v34, v36, v34
	v_mul_f32_e32 v35, v37, v35
	s_waitcnt vmcnt(1)
	v_mul_f32_e32 v37, v82, v41
	v_mul_f32_e32 v41, v82, v43
	v_med3_f32 v43, v45, s58, v112
	v_med3_f32 v45, v33, s58, v112
	v_med3_f32 v34, v34, s58, v112
	v_med3_f32 v35, v35, s58, v112
	v_mov_b32_e32 v33, 0
	v_cvt_pk_fp8_f32 v33, v34, v35
	v_mul_f32_e32 v38, v82, v38
	v_mul_f32_e32 v39, v82, v39
	s_waitcnt vmcnt(0)
	v_mul_f32_e32 v48, v48, v82
	v_mul_f32_e32 v49, v49, v82
	v_mul_f32_e32 v38, v38, v55
	v_mul_f32_e32 v39, v39, v54
	v_mul_f32_e32 v48, v48, v56
	v_mul_f32_e32 v49, v49, v57
	v_mul_f32_e32 v36, v82, v40
	v_med3_f32 v34, v38, s58, v112
	v_med3_f32 v35, v39, s58, v112
	v_mul_f32_e32 v36, v36, v62
	v_mul_f32_e32 v37, v37, v63
	v_cvt_pk_fp8_f32 v33, v34, v35 op_sel:[0,0,1]
	v_med3_f32 v35, v48, s58, v112
	v_med3_f32 v38, v49, s58, v112
	v_mov_b32_e32 v34, 0
	v_cvt_pk_fp8_f32 v34, v35, v38
	v_med3_f32 v36, v36, s58, v112
	v_med3_f32 v37, v37, s58, v112
	v_mov_b32_e32 v35, 0
	v_cvt_pk_fp8_f32 v35, v36, v37
	v_mul_f32_e32 v40, v82, v42
	v_mul_f32_e32 v40, v40, v53
	v_mul_f32_e32 v41, v41, v52
	v_med3_f32 v36, v40, s58, v112
	v_med3_f32 v37, v41, s58, v112
	v_max_f32_e32 v30, v30, v30
	v_max_f32_e32 v31, v31, v31
	v_cvt_pk_fp8_f32 v35, v36, v37 op_sel:[0,0,1]
	v_med3_f32 v30, v30, s58, v112
	v_med3_f32 v31, v31, s58, v112
	v_max_f32_e32 v36, v28, v28
	v_mov_b32_e32 v28, 0
	v_mul_f32_e32 v44, v44, v82
	v_mul_f32_e32 v46, v46, v82
	v_cvt_pk_fp8_f32 v28, v30, v31
	v_mul_f32_e32 v44, v44, v58
	v_mul_f32_e32 v32, v46, v32
	v_med3_f32 v42, v44, s58, v112
	v_med3_f32 v44, v32, s58, v112
	v_mov_b32_e32 v32, 0
	v_max_f32_e32 v29, v29, v29
	v_cvt_pk_fp8_f32 v32, v42, v43
	v_med3_f32 v30, v36, s58, v112
	v_med3_f32 v29, v29, s58, v112
	v_max_f32_e32 v26, v26, v26
	v_max_f32_e32 v27, v27, v27
	v_cvt_pk_fp8_f32 v28, v30, v29 op_sel:[0,0,1]
	v_med3_f32 v26, v26, s58, v112
	v_med3_f32 v27, v27, s58, v112
	v_mov_b32_e32 v29, 0
	v_mul_f32_e32 v46, v50, v82
	v_mul_f32_e32 v47, v82, v51
	v_cvt_pk_fp8_f32 v29, v26, v27
	v_mul_f32_e32 v46, v46, v60
	v_mul_f32_e32 v47, v47, v61
	v_cvt_pk_fp8_f32 v32, v44, v45 op_sel:[0,0,1]
	v_med3_f32 v39, v46, s58, v112
	v_med3_f32 v42, v47, s58, v112
	v_max_f32_e32 v24, v24, v24
	v_max_f32_e32 v25, v25, v25
	v_cvt_pk_fp8_f32 v34, v39, v42 op_sel:[0,0,1]
	v_med3_f32 v24, v24, s58, v112
	v_med3_f32 v25, v25, s58, v112
	v_cvt_pk_fp8_f32 v29, v24, v25 op_sel:[0,0,1]
	v_mad_i64_i32 v[24:25], s[28:29], s62, v113, v[68:69]
	global_store_dwordx2 v[24:25], v[32:33], off nt
	global_store_dwordx2 v[24:25], v[34:35], off offset:64 nt
	global_store_dwordx2 v[24:25], v[28:29], off offset:128 nt
	s_branch .LBB0_478
.LBB0_477:
	s_waitcnt vmcnt(2)
	v_mul_f32_e32 v57, v57, v94
	v_mul_f32_e32 v59, v94, v59
	v_mul_f32_e32 v48, v94, v48
	v_mul_f32_e32 v49, v94, v49
	v_mul_f32_e32 v57, v57, v89
	v_mul_f32_e32 v45, v59, v45
	v_mul_f32_e32 v46, v48, v46
	v_mul_f32_e32 v47, v49, v47
	s_waitcnt vmcnt(1)
	v_mul_f32_e32 v49, v94, v53
	v_mul_f32_e32 v53, v94, v55
	v_med3_f32 v55, v57, s58, v112
	v_med3_f32 v57, v45, s58, v112
	v_med3_f32 v46, v46, s58, v112
	v_med3_f32 v47, v47, s58, v112
	v_mov_b32_e32 v45, 0
	v_cvt_pk_fp8_f32 v45, v46, v47
	v_mul_f32_e32 v50, v94, v50
	v_mul_f32_e32 v51, v94, v51
	s_waitcnt vmcnt(0)
	v_mul_f32_e32 v60, v60, v94
	v_mul_f32_e32 v61, v61, v94
	v_mul_f32_e32 v50, v50, v85
	v_mul_f32_e32 v51, v51, v84
	v_mul_f32_e32 v60, v60, v86
	v_mul_f32_e32 v61, v61, v87
	v_mul_f32_e32 v48, v94, v52
	v_med3_f32 v46, v50, s58, v112
	v_med3_f32 v47, v51, s58, v112
	v_mul_f32_e32 v48, v48, v92
	v_mul_f32_e32 v49, v49, v93
	v_cvt_pk_fp8_f32 v45, v46, v47 op_sel:[0,0,1]
	v_med3_f32 v47, v60, s58, v112
	v_med3_f32 v50, v61, s58, v112
	v_mov_b32_e32 v46, 0
	v_cvt_pk_fp8_f32 v46, v47, v50
	v_med3_f32 v48, v48, s58, v112
	v_med3_f32 v49, v49, s58, v112
	v_mov_b32_e32 v47, 0
	v_cvt_pk_fp8_f32 v47, v48, v49
	v_mul_f32_e32 v52, v94, v54
	v_mul_f32_e32 v52, v52, v83
	v_mul_f32_e32 v53, v53, v82
	v_med3_f32 v48, v52, s58, v112
	v_med3_f32 v49, v53, s58, v112
	v_max_f32_e32 v42, v42, v42
	v_max_f32_e32 v43, v43, v43
	v_cvt_pk_fp8_f32 v47, v48, v49 op_sel:[0,0,1]
	v_med3_f32 v42, v42, s58, v112
	v_med3_f32 v43, v43, s58, v112
	v_max_f32_e32 v48, v40, v40
	v_mov_b32_e32 v40, 0
	v_mul_f32_e32 v56, v56, v94
	v_mul_f32_e32 v58, v58, v94
	v_cvt_pk_fp8_f32 v40, v42, v43
	v_mul_f32_e32 v56, v56, v88
	v_mul_f32_e32 v44, v58, v44
	v_med3_f32 v54, v56, s58, v112
	v_med3_f32 v56, v44, s58, v112
	v_mov_b32_e32 v44, 0
	v_max_f32_e32 v41, v41, v41
	v_cvt_pk_fp8_f32 v44, v54, v55
	v_med3_f32 v42, v48, s58, v112
	v_med3_f32 v41, v41, s58, v112
	v_max_f32_e32 v38, v38, v38
	v_max_f32_e32 v39, v39, v39
	v_cvt_pk_fp8_f32 v40, v42, v41 op_sel:[0,0,1]
	v_med3_f32 v38, v38, s58, v112
	v_med3_f32 v39, v39, s58, v112
	v_mov_b32_e32 v41, 0
	v_mul_f32_e32 v58, v62, v94
	v_mul_f32_e32 v59, v94, v63
	v_cvt_pk_fp8_f32 v41, v38, v39
	v_mul_f32_e32 v58, v58, v90
	v_mul_f32_e32 v59, v59, v91
	v_cvt_pk_fp8_f32 v44, v56, v57 op_sel:[0,0,1]
	v_med3_f32 v51, v58, s58, v112
	v_med3_f32 v54, v59, s58, v112
	v_max_f32_e32 v36, v36, v36
	v_max_f32_e32 v37, v37, v37
	v_cvt_pk_fp8_f32 v46, v51, v54 op_sel:[0,0,1]
	v_med3_f32 v36, v36, s58, v112
	v_med3_f32 v37, v37, s58, v112
	v_cvt_pk_fp8_f32 v41, v36, v37 op_sel:[0,0,1]
	v_lshl_add_u64 v[36:37], s[8:9], 0, v[76:77]
	global_store_dwordx2 v[36:37], v[44:45], off offset:-64 nt
	global_store_dwordx2 v[36:37], v[46:47], off nt
	global_store_dwordx2 v[36:37], v[40:41], off offset:64 nt
	s_andn2_b64 vcc, exec, s[28:29]
	s_cbranch_vccz .LBB0_473

.LBB0_485:
	s_and_b64 vcc, exec, s[2:3]
	s_cbranch_vccnz .LBB0_463
	s_waitcnt vmcnt(0)
	v_mul_f32_e32 v26, v26, v40
	v_mul_f32_e32 v26, v26, v8
	v_mul_f32_e32 v8, v40, v23
	v_mul_f32_e32 v23, v40, v27
	v_mul_f32_e32 v23, v23, v9
	v_mul_f32_e32 v9, v40, v12
	v_mul_f32_e32 v20, v20, v40
	v_mul_f32_e32 v21, v21, v40
	v_mul_f32_e32 v9, v9, v10
	v_mul_f32_e32 v10, v40, v16
	v_mul_f32_e32 v20, v20, v34
	v_mul_f32_e32 v21, v21, v35
	v_mul_f32_e32 v8, v8, v37
	v_mul_f32_e32 v12, v10, v38
	v_mul_f32_e32 v10, v40, v13
	v_mul_f32_e32 v10, v10, v11
	v_mul_f32_e32 v11, v40, v17
	v_mul_f32_e32 v13, v40, v14
	v_mul_f32_e32 v14, v40, v18
	v_med3_f32 v17, v20, s58, v112
	v_med3_f32 v18, v21, s58, v112
	v_med3_f32 v20, v8, s58, v112
	v_mov_b32_e32 v8, 0
	v_cvt_pk_fp8_f32 v8, v17, v18
	v_med3_f32 v17, v9, s58, v112
	v_med3_f32 v10, v10, s58, v112
	v_mov_b32_e32 v9, 0
	v_cvt_pk_fp8_f32 v9, v17, v10
	v_mul_f32_e32 v15, v40, v15
	v_mul_f32_e32 v24, v24, v40
	v_mul_f32_e32 v25, v25, v40
	v_mul_f32_e32 v13, v13, v31
	v_mul_f32_e32 v15, v15, v30
	v_mul_f32_e32 v24, v24, v32
	v_mul_f32_e32 v25, v25, v33
	v_med3_f32 v10, v13, s58, v112
	v_med3_f32 v13, v15, s58, v112
	v_mul_f32_e32 v11, v11, v39
	v_cvt_pk_fp8_f32 v9, v10, v13 op_sel:[0,0,1]
	v_med3_f32 v13, v24, s58, v112
	v_med3_f32 v15, v25, s58, v112
	v_mov_b32_e32 v10, 0
	v_cvt_pk_fp8_f32 v10, v13, v15
	v_med3_f32 v12, v12, s58, v112
	v_med3_f32 v13, v11, s58, v112
	v_mov_b32_e32 v11, 0
	v_cvt_pk_fp8_f32 v11, v12, v13
	v_mul_f32_e32 v16, v40, v19
	v_mul_f32_e32 v14, v14, v29
	v_mul_f32_e32 v16, v16, v28
	v_med3_f32 v12, v14, s58, v112
	v_med3_f32 v13, v16, s58, v112
	v_max_f32_e32 v6, v6, v6
	v_max_f32_e32 v7, v7, v7
	v_cvt_pk_fp8_f32 v11, v12, v13 op_sel:[0,0,1]
	v_med3_f32 v6, v6, s58, v112
	v_med3_f32 v7, v7, s58, v112
	v_max_f32_e32 v12, v4, v4
	v_mov_b32_e32 v4, 0
	v_cvt_pk_fp8_f32 v4, v6, v7
	v_max_f32_e32 v5, v5, v5
	v_med3_f32 v6, v12, s58, v112
	v_med3_f32 v5, v5, s58, v112
	v_max_f32_e32 v2, v2, v2
	v_max_f32_e32 v3, v3, v3
	v_mul_f32_e32 v22, v22, v40
	v_cvt_pk_fp8_f32 v4, v6, v5 op_sel:[0,0,1]
	v_med3_f32 v2, v2, s58, v112
	v_med3_f32 v3, v3, s58, v112
	v_mov_b32_e32 v5, 0
	v_mul_f32_e32 v22, v22, v36
	v_cvt_pk_fp8_f32 v5, v2, v3
	v_med3_f32 v19, v22, s58, v112
	v_cvt_pk_fp8_f32 v8, v19, v20 op_sel:[0,0,1]
	v_med3_f32 v17, v26, s58, v112
	v_med3_f32 v18, v23, s58, v112
	v_max_f32_e32 v0, v0, v0
	v_max_f32_e32 v1, v1, v1
	v_cvt_pk_fp8_f32 v10, v17, v18 op_sel:[0,0,1]
	v_med3_f32 v0, v0, s58, v112
	v_med3_f32 v1, v1, s58, v112
	v_cvt_pk_fp8_f32 v5, v0, v1 op_sel:[0,0,1]
	v_mad_i64_i32 v[0:1], s[2:3], s60, v113, v[68:69]
	global_store_dwordx2 v[0:1], v[8:9], off nt
	global_store_dwordx2 v[0:1], v[10:11], off offset:64 nt
	global_store_dwordx2 v[0:1], v[4:5], off offset:128 nt
	s_branch .LBB0_463
.LBB0_487:
	s_waitcnt vmcnt(2)
	v_mul_f32_e32 v33, v33, v52
	v_mul_f32_e32 v35, v52, v35
	v_mul_f32_e32 v24, v52, v24
	v_mul_f32_e32 v25, v52, v25
	v_mul_f32_e32 v33, v33, v47
	v_mul_f32_e32 v21, v35, v21
	v_mul_f32_e32 v22, v24, v22
	v_mul_f32_e32 v23, v25, v23
	s_waitcnt vmcnt(1)
	v_mul_f32_e32 v25, v52, v29
	v_mul_f32_e32 v29, v52, v31
	v_med3_f32 v31, v33, s58, v112
	v_med3_f32 v33, v21, s58, v112
	v_med3_f32 v22, v22, s58, v112
	v_med3_f32 v23, v23, s58, v112
	v_mov_b32_e32 v21, 0
	v_cvt_pk_fp8_f32 v21, v22, v23
	v_mul_f32_e32 v26, v52, v26
	v_mul_f32_e32 v27, v52, v27
	s_waitcnt vmcnt(0)
	v_mul_f32_e32 v36, v36, v52
	v_mul_f32_e32 v37, v37, v52
	v_mul_f32_e32 v26, v26, v43
	v_mul_f32_e32 v27, v27, v42
	v_mul_f32_e32 v36, v36, v44
	v_mul_f32_e32 v37, v37, v45
	v_mul_f32_e32 v24, v52, v28
	v_med3_f32 v22, v26, s58, v112
	v_med3_f32 v23, v27, s58, v112
	v_mul_f32_e32 v24, v24, v50
	v_mul_f32_e32 v25, v25, v51
	v_cvt_pk_fp8_f32 v21, v22, v23 op_sel:[0,0,1]
	v_med3_f32 v23, v36, s58, v112
	v_med3_f32 v26, v37, s58, v112
	v_mov_b32_e32 v22, 0
	v_cvt_pk_fp8_f32 v22, v23, v26
	v_med3_f32 v24, v24, s58, v112
	v_med3_f32 v25, v25, s58, v112
	v_mov_b32_e32 v23, 0
	v_cvt_pk_fp8_f32 v23, v24, v25
	v_mul_f32_e32 v28, v52, v30
	v_mul_f32_e32 v28, v28, v41
	v_mul_f32_e32 v29, v29, v40
	v_med3_f32 v24, v28, s58, v112
	v_med3_f32 v25, v29, s58, v112
	v_max_f32_e32 v18, v18, v18
	v_max_f32_e32 v19, v19, v19
	v_cvt_pk_fp8_f32 v23, v24, v25 op_sel:[0,0,1]
	v_med3_f32 v18, v18, s58, v112
	v_med3_f32 v19, v19, s58, v112
	v_max_f32_e32 v24, v16, v16
	v_mov_b32_e32 v16, 0
	v_mul_f32_e32 v32, v32, v52
	v_mul_f32_e32 v34, v34, v52
	v_cvt_pk_fp8_f32 v16, v18, v19
	v_mul_f32_e32 v32, v32, v46
	v_mul_f32_e32 v20, v34, v20
	v_med3_f32 v30, v32, s58, v112
	v_med3_f32 v32, v20, s58, v112
	v_mov_b32_e32 v20, 0
	v_max_f32_e32 v17, v17, v17
	v_cvt_pk_fp8_f32 v20, v30, v31
	v_med3_f32 v18, v24, s58, v112
	v_med3_f32 v17, v17, s58, v112
	v_max_f32_e32 v14, v14, v14
	v_max_f32_e32 v15, v15, v15
	v_cvt_pk_fp8_f32 v16, v18, v17 op_sel:[0,0,1]
	v_med3_f32 v14, v14, s58, v112
	v_med3_f32 v15, v15, s58, v112
	v_mov_b32_e32 v17, 0
	v_mul_f32_e32 v34, v38, v52
	v_mul_f32_e32 v35, v52, v39
	v_cvt_pk_fp8_f32 v17, v14, v15
	v_mul_f32_e32 v34, v34, v48
	v_mul_f32_e32 v35, v35, v49
	v_cvt_pk_fp8_f32 v20, v32, v33 op_sel:[0,0,1]
	v_med3_f32 v27, v34, s58, v112
	v_med3_f32 v30, v35, s58, v112
	v_max_f32_e32 v12, v12, v12
	v_max_f32_e32 v13, v13, v13
	v_cvt_pk_fp8_f32 v22, v27, v30 op_sel:[0,0,1]
	v_med3_f32 v12, v12, s58, v112
	v_med3_f32 v13, v13, s58, v112
	v_cvt_pk_fp8_f32 v17, v12, v13 op_sel:[0,0,1]
	v_mad_i64_i32 v[12:13], s[26:27], s61, v113, v[68:69]
	global_store_dwordx2 v[12:13], v[20:21], off nt
	global_store_dwordx2 v[12:13], v[22:23], off offset:64 nt
	global_store_dwordx2 v[12:13], v[16:17], off offset:128 nt
	s_andn2_b64 vcc, exec, s[24:25]
	s_cbranch_vccnz .LBB0_463
	s_branch .LBB0_483

.LBB0_492:
	s_and_b32 s2, s11, 0xffffffc0
	v_or_b32_e32 v0, s2, v108
	v_ashrrev_i32_e32 v1, 31, v0
	v_lshlrev_b64 v[0:1], 12, v[0:1]
	s_and_b32 s2, s13, 0x700
	v_lshl_add_u64 v[0:1], s[4:5], 0, v[0:1]
	s_lshl_b32 s2, s2, 1
	v_lshl_add_u64 v[70:71], v[0:1], 0, s[2:3]
	global_load_dwordx4 v[50:53], v[70:71], off offset:256
	global_load_dwordx4 v[54:57], v[70:71], off offset:272
	global_load_dwordx4 v[58:61], v[70:71], off offset:304
	global_load_dwordx4 v[62:65], v[70:71], off offset:288
	global_load_dwordx4 v[32:35], v[70:71], off offset:368
	global_load_dwordx4 v[36:39], v[70:71], off offset:352
	global_load_dwordx4 v[40:43], v[70:71], off offset:336
	global_load_dwordx4 v[66:69], v[70:71], off offset:320
	global_load_dwordx4 v[16:19], v[70:71], off offset:432
	global_load_dwordx4 v[20:23], v[70:71], off offset:416
	global_load_dwordx4 v[24:27], v[70:71], off offset:400
	global_load_dwordx4 v[28:31], v[70:71], off offset:384
	global_load_dwordx4 v[0:3], v[70:71], off offset:496
	global_load_dwordx4 v[4:7], v[70:71], off offset:480
	global_load_dwordx4 v[8:11], v[70:71], off offset:464
	global_load_dwordx4 v[12:15], v[70:71], off offset:448
	v_mov_b32_e32 v49, 0
	v_mov_b32_e32 v72, 0
	v_mov_b32_e32 v73, 0
	v_mov_b32_e32 v74, 0
	s_and_b64 vcc, exec, s[0:1]
	s_waitcnt vmcnt(15)
	v_lshlrev_b32_e32 v70, 16, v50
	v_and_b32_e32 v50, 0xffff0000, v50
	v_lshlrev_b32_e32 v75, 16, v52
	v_and_b32_e32 v52, 0xffff0000, v52
	s_waitcnt vmcnt(14)
	v_lshlrev_b32_e32 v77, 16, v54
	v_and_b32_e32 v54, 0xffff0000, v54
	v_lshlrev_b32_e32 v79, 16, v56
	v_and_b32_e32 v56, 0xffff0000, v56
	v_max_f32_e32 v70, v70, v70
	v_max_f32_e32 v50, v50, v50
	v_max_f32_e32 v75, v75, v75
	v_max_f32_e32 v52, v52, v52
	v_max_f32_e32 v77, v77, v77
	v_max_f32_e32 v54, v54, v54
	v_max_f32_e32 v79, v79, v79
	v_max_f32_e32 v56, v56, v56
	v_med3_f32 v70, v70, s7, v45
	v_med3_f32 v50, v50, s7, v45
	v_med3_f32 v75, v75, s7, v45
	v_med3_f32 v52, v52, s7, v45
	v_med3_f32 v77, v77, s7, v45
	v_med3_f32 v54, v54, s7, v45
	v_med3_f32 v79, v79, s7, v45
	v_med3_f32 v56, v56, s7, v45
	v_cvt_pk_fp8_f32 v49, v70, v50
	v_lshlrev_b32_e32 v71, 16, v51
	v_and_b32_e32 v51, 0xffff0000, v51
	v_cvt_pk_fp8_f32 v72, v75, v52
	v_cvt_pk_fp8_f32 v73, v77, v54
	v_cvt_pk_fp8_f32 v74, v79, v56
	v_lshlrev_b32_e32 v76, 16, v53
	v_and_b32_e32 v53, 0xffff0000, v53
	v_lshlrev_b32_e32 v78, 16, v55
	v_and_b32_e32 v55, 0xffff0000, v55
	v_lshlrev_b32_e32 v80, 16, v57
	v_and_b32_e32 v57, 0xffff0000, v57
	v_max_f32_e32 v71, v71, v71
	v_max_f32_e32 v51, v51, v51
	v_max_f32_e32 v76, v76, v76
	v_max_f32_e32 v53, v53, v53
	v_max_f32_e32 v78, v78, v78
	v_max_f32_e32 v55, v55, v55
	v_max_f32_e32 v80, v80, v80
	v_max_f32_e32 v57, v57, v57
	v_med3_f32 v71, v71, s7, v45
	v_med3_f32 v51, v51, s7, v45
	v_med3_f32 v76, v76, s7, v45
	v_med3_f32 v53, v53, s7, v45
	v_med3_f32 v78, v78, s7, v45
	v_med3_f32 v55, v55, s7, v45
	v_med3_f32 v80, v80, s7, v45
	v_med3_f32 v57, v57, s7, v45
	v_cvt_pk_fp8_f32 v49, v71, v51 op_sel:[0,0,1]
	v_cvt_pk_fp8_f32 v72, v76, v53 op_sel:[0,0,1]
	v_cvt_pk_fp8_f32 v73, v78, v55 op_sel:[0,0,1]
	v_cvt_pk_fp8_f32 v74, v80, v57 op_sel:[0,0,1]
	ds_write_b8 v48, v49
	ds_write_b8 v48, v72 offset:256
	v_lshrrev_b32_e32 v50, 8, v49
	ds_write_b8_d16_hi v48, v49 offset:128
	ds_write_b8_d16_hi v48, v72 offset:384
	v_lshrrev_b32_e32 v49, 24, v49
	v_lshrrev_b32_e32 v51, 8, v72
	v_lshrrev_b32_e32 v52, 24, v72
	ds_write_b8 v48, v73 offset:512
	ds_write_b8 v48, v74 offset:768
	v_lshrrev_b32_e32 v53, 8, v73
	ds_write_b8 v48, v50 offset:64
	ds_write_b8 v48, v51 offset:320
	ds_write_b8 v48, v49 offset:192
	ds_write_b8 v48, v52 offset:448
	ds_write_b8 v48, v53 offset:576
	v_lshrrev_b32_e32 v49, 8, v74
	ds_write_b8 v48, v49 offset:832
	ds_write_b8_d16_hi v48, v73 offset:640
	ds_write_b8_d16_hi v48, v74 offset:896
	v_lshrrev_b32_e32 v49, 24, v73
	ds_write_b8 v48, v49 offset:704
	s_waitcnt vmcnt(12)
	v_lshlrev_b32_e32 v49, 16, v62
	v_and_b32_e32 v50, 0xffff0000, v62
	v_max_f32_e32 v49, v49, v49
	v_max_f32_e32 v50, v50, v50
	v_med3_f32 v49, v49, s7, v45
	v_med3_f32 v50, v50, s7, v45
	v_mov_b32_e32 v57, 0
	v_cvt_pk_fp8_f32 v57, v49, v50
	v_lshlrev_b32_e32 v51, 16, v63
	v_and_b32_e32 v52, 0xffff0000, v63
	v_max_f32_e32 v51, v51, v51
	v_max_f32_e32 v50, v52, v52
	v_lshlrev_b32_e32 v53, 16, v64
	v_and_b32_e32 v54, 0xffff0000, v64
	v_med3_f32 v49, v51, s7, v45
	v_med3_f32 v50, v50, s7, v45
	v_cvt_pk_fp8_f32 v57, v49, v50 op_sel:[0,0,1]
	v_max_f32_e32 v49, v53, v53
	v_max_f32_e32 v50, v54, v54
	v_med3_f32 v49, v49, s7, v45
	v_med3_f32 v50, v50, s7, v45
	v_mov_b32_e32 v52, 0
	v_cvt_pk_fp8_f32 v52, v49, v50
	v_lshlrev_b32_e32 v55, 16, v65
	v_and_b32_e32 v56, 0xffff0000, v65
	v_max_f32_e32 v51, v55, v55
	v_max_f32_e32 v50, v56, v56
	v_med3_f32 v49, v51, s7, v45
	v_med3_f32 v50, v50, s7, v45
	v_cvt_pk_fp8_f32 v52, v49, v50 op_sel:[0,0,1]
	v_lshrrev_b32_e32 v49, 24, v74
	ds_write_b8 v48, v49 offset:960
	ds_write_b8 v48, v57 offset:1024
	ds_write_b8 v48, v52 offset:1280
	v_lshrrev_b32_e32 v49, 8, v57
	ds_write_b8 v48, v49 offset:1088
	v_lshrrev_b32_e32 v49, 8, v52
	ds_write_b8 v48, v49 offset:1344
	ds_write_b8_d16_hi v48, v57 offset:1152
	ds_write_b8_d16_hi v48, v52 offset:1408
	v_lshrrev_b32_e32 v49, 24, v57
	ds_write_b8 v48, v49 offset:1216
	v_lshlrev_b32_e32 v49, 16, v58
	v_and_b32_e32 v50, 0xffff0000, v58
	v_max_f32_e32 v49, v49, v49
	v_max_f32_e32 v50, v50, v50
	v_med3_f32 v49, v49, s7, v45
	v_med3_f32 v50, v50, s7, v45
	v_mov_b32_e32 v58, 0
	v_cvt_pk_fp8_f32 v58, v49, v50
	v_lshlrev_b32_e32 v51, 16, v59
	v_and_b32_e32 v53, 0xffff0000, v59
	v_max_f32_e32 v51, v51, v51
	v_max_f32_e32 v50, v53, v53
	v_lshlrev_b32_e32 v54, 16, v60
	v_and_b32_e32 v55, 0xffff0000, v60
	v_med3_f32 v49, v51, s7, v45
	v_med3_f32 v50, v50, s7, v45
	v_cvt_pk_fp8_f32 v58, v49, v50 op_sel:[0,0,1]
	v_max_f32_e32 v49, v54, v54
	v_max_f32_e32 v50, v55, v55
	v_med3_f32 v49, v49, s7, v45
	v_med3_f32 v50, v50, s7, v45
	v_mov_b32_e32 v53, 0
	v_cvt_pk_fp8_f32 v53, v49, v50
	v_lshlrev_b32_e32 v56, 16, v61
	v_and_b32_e32 v57, 0xffff0000, v61
	v_max_f32_e32 v51, v56, v56
	v_max_f32_e32 v50, v57, v57
	v_med3_f32 v49, v51, s7, v45
	v_med3_f32 v50, v50, s7, v45
	v_cvt_pk_fp8_f32 v53, v49, v50 op_sel:[0,0,1]
	v_lshrrev_b32_e32 v49, 24, v52
	ds_write_b8 v48, v49 offset:1472
	ds_write_b8 v48, v58 offset:1536
	ds_write_b8 v48, v53 offset:1792
	v_lshrrev_b32_e32 v49, 8, v58
	ds_write_b8 v48, v49 offset:1600
	v_lshrrev_b32_e32 v49, 8, v53
	ds_write_b8 v48, v49 offset:1856
	ds_write_b8_d16_hi v48, v58 offset:1664
	ds_write_b8_d16_hi v48, v53 offset:1920
	v_lshrrev_b32_e32 v49, 24, v58
	ds_write_b8 v48, v49 offset:1728
	s_waitcnt vmcnt(8)
	v_lshlrev_b32_e32 v49, 16, v66
	v_and_b32_e32 v50, 0xffff0000, v66
	v_max_f32_e32 v49, v49, v49
	v_max_f32_e32 v50, v50, v50
	v_med3_f32 v49, v49, s7, v45
	v_med3_f32 v50, v50, s7, v45
	v_mov_b32_e32 v58, 0
	v_cvt_pk_fp8_f32 v58, v49, v50
	v_lshlrev_b32_e32 v51, 16, v67
	v_and_b32_e32 v52, 0xffff0000, v67
	v_max_f32_e32 v51, v51, v51
	v_max_f32_e32 v50, v52, v52
	v_lshlrev_b32_e32 v54, 16, v68
	v_and_b32_e32 v55, 0xffff0000, v68
	v_med3_f32 v49, v51, s7, v45
	v_med3_f32 v50, v50, s7, v45
	v_cvt_pk_fp8_f32 v58, v49, v50 op_sel:[0,0,1]
	v_max_f32_e32 v49, v54, v54
	v_max_f32_e32 v50, v55, v55
	v_med3_f32 v49, v49, s7, v45
	v_med3_f32 v50, v50, s7, v45
	v_mov_b32_e32 v52, 0
	v_cvt_pk_fp8_f32 v52, v49, v50
	v_lshlrev_b32_e32 v56, 16, v69
	v_and_b32_e32 v57, 0xffff0000, v69
	v_max_f32_e32 v51, v56, v56
	v_max_f32_e32 v50, v57, v57
	v_med3_f32 v49, v51, s7, v45
	v_med3_f32 v50, v50, s7, v45
	v_cvt_pk_fp8_f32 v52, v49, v50 op_sel:[0,0,1]
	v_lshrrev_b32_e32 v49, 24, v53
	ds_write_b8 v48, v49 offset:1984
	ds_write_b8 v48, v58 offset:2048
	ds_write_b8 v48, v52 offset:2304
	v_lshrrev_b32_e32 v49, 8, v58
	ds_write_b8 v48, v49 offset:2112
	v_lshrrev_b32_e32 v49, 8, v52
	ds_write_b8 v48, v49 offset:2368
	ds_write_b8_d16_hi v48, v58 offset:2176
	ds_write_b8_d16_hi v48, v52 offset:2432
	v_lshrrev_b32_e32 v49, 24, v58
	ds_write_b8 v48, v49 offset:2240
	v_lshlrev_b32_e32 v49, 16, v40
	v_and_b32_e32 v40, 0xffff0000, v40
	v_max_f32_e32 v49, v49, v49
	v_max_f32_e32 v40, v40, v40
	v_med3_f32 v49, v49, s7, v45
	v_med3_f32 v40, v40, s7, v45
	v_mov_b32_e32 v54, 0
	v_cvt_pk_fp8_f32 v54, v49, v40
	v_lshlrev_b32_e32 v50, 16, v41
	v_and_b32_e32 v41, 0xffff0000, v41
	v_max_f32_e32 v50, v50, v50
	v_max_f32_e32 v41, v41, v41
	v_lshlrev_b32_e32 v51, 16, v42
	v_and_b32_e32 v42, 0xffff0000, v42
	v_med3_f32 v40, v50, s7, v45
	v_med3_f32 v41, v41, s7, v45
	v_cvt_pk_fp8_f32 v54, v40, v41 op_sel:[0,0,1]
	v_max_f32_e32 v40, v51, v51
	v_max_f32_e32 v41, v42, v42
	v_med3_f32 v40, v40, s7, v45
	v_med3_f32 v41, v41, s7, v45
	v_mov_b32_e32 v49, 0
	v_cvt_pk_fp8_f32 v49, v40, v41
	v_lshlrev_b32_e32 v53, 16, v43
	v_and_b32_e32 v43, 0xffff0000, v43
	v_max_f32_e32 v42, v53, v53
	v_max_f32_e32 v41, v43, v43
	v_med3_f32 v40, v42, s7, v45
	v_med3_f32 v41, v41, s7, v45
	v_cvt_pk_fp8_f32 v49, v40, v41 op_sel:[0,0,1]
	v_lshrrev_b32_e32 v40, 24, v52
	ds_write_b8 v48, v40 offset:2496
	ds_write_b8 v48, v54 offset:2560
	ds_write_b8 v48, v49 offset:2816
	v_lshrrev_b32_e32 v40, 8, v54
	ds_write_b8 v48, v40 offset:2624
	v_lshrrev_b32_e32 v40, 8, v49
	ds_write_b8 v48, v40 offset:2880
	ds_write_b8_d16_hi v48, v54 offset:2688
	ds_write_b8_d16_hi v48, v49 offset:2944
	v_lshrrev_b32_e32 v40, 24, v54
	ds_write_b8 v48, v40 offset:2752
	v_lshlrev_b32_e32 v40, 16, v36
	v_and_b32_e32 v36, 0xffff0000, v36
	v_max_f32_e32 v40, v40, v40
	v_max_f32_e32 v36, v36, v36
	v_med3_f32 v40, v40, s7, v45
	v_med3_f32 v36, v36, s7, v45
	v_mov_b32_e32 v50, 0
	v_cvt_pk_fp8_f32 v50, v40, v36
	v_lshlrev_b32_e32 v41, 16, v37
	v_and_b32_e32 v37, 0xffff0000, v37
	v_max_f32_e32 v41, v41, v41
	v_max_f32_e32 v37, v37, v37
	v_lshlrev_b32_e32 v42, 16, v38
	v_and_b32_e32 v38, 0xffff0000, v38
	v_med3_f32 v36, v41, s7, v45
	v_med3_f32 v37, v37, s7, v45
	v_cvt_pk_fp8_f32 v50, v36, v37 op_sel:[0,0,1]
	v_max_f32_e32 v36, v42, v42
	v_max_f32_e32 v37, v38, v38
	v_med3_f32 v36, v36, s7, v45
	v_med3_f32 v37, v37, s7, v45
	v_mov_b32_e32 v40, 0
	v_cvt_pk_fp8_f32 v40, v36, v37
	v_lshlrev_b32_e32 v43, 16, v39
	v_and_b32_e32 v39, 0xffff0000, v39
	v_max_f32_e32 v38, v43, v43
	v_max_f32_e32 v37, v39, v39
	v_med3_f32 v36, v38, s7, v45
	v_med3_f32 v37, v37, s7, v45
	v_cvt_pk_fp8_f32 v40, v36, v37 op_sel:[0,0,1]
	v_lshrrev_b32_e32 v36, 24, v49
	ds_write_b8 v48, v36 offset:3008
	ds_write_b8 v48, v50 offset:3072
	ds_write_b8 v48, v40 offset:3328
	v_lshrrev_b32_e32 v36, 8, v50
	ds_write_b8 v48, v36 offset:3136
	v_lshrrev_b32_e32 v36, 8, v40
	ds_write_b8 v48, v36 offset:3392
	ds_write_b8_d16_hi v48, v50 offset:3200
	ds_write_b8_d16_hi v48, v40 offset:3456
	v_lshrrev_b32_e32 v36, 24, v50
	ds_write_b8 v48, v36 offset:3264
	v_lshlrev_b32_e32 v36, 16, v32
	v_and_b32_e32 v32, 0xffff0000, v32
	v_max_f32_e32 v36, v36, v36
	v_max_f32_e32 v32, v32, v32
	v_med3_f32 v36, v36, s7, v45
	v_med3_f32 v32, v32, s7, v45
	v_mov_b32_e32 v41, 0
	v_cvt_pk_fp8_f32 v41, v36, v32
	v_lshlrev_b32_e32 v37, 16, v33
	v_and_b32_e32 v33, 0xffff0000, v33
	v_max_f32_e32 v37, v37, v37
	v_max_f32_e32 v33, v33, v33
	v_lshlrev_b32_e32 v38, 16, v34
	v_and_b32_e32 v34, 0xffff0000, v34
	v_med3_f32 v32, v37, s7, v45
	v_med3_f32 v33, v33, s7, v45
	v_cvt_pk_fp8_f32 v41, v32, v33 op_sel:[0,0,1]
	v_max_f32_e32 v32, v38, v38
	v_max_f32_e32 v33, v34, v34
	v_med3_f32 v32, v32, s7, v45
	v_med3_f32 v33, v33, s7, v45
	v_mov_b32_e32 v36, 0
	v_cvt_pk_fp8_f32 v36, v32, v33
	v_lshlrev_b32_e32 v39, 16, v35
	v_and_b32_e32 v35, 0xffff0000, v35
	v_max_f32_e32 v34, v39, v39
	v_max_f32_e32 v33, v35, v35
	v_med3_f32 v32, v34, s7, v45
	v_med3_f32 v33, v33, s7, v45
	v_cvt_pk_fp8_f32 v36, v32, v33 op_sel:[0,0,1]
	v_lshrrev_b32_e32 v32, 24, v40
	ds_write_b8 v48, v32 offset:3520
	ds_write_b8 v48, v41 offset:3584
	ds_write_b8 v48, v36 offset:3840
	v_lshrrev_b32_e32 v32, 8, v41
	ds_write_b8 v48, v32 offset:3648
	v_lshrrev_b32_e32 v32, 8, v36
	ds_write_b8 v48, v32 offset:3904
	ds_write_b8_d16_hi v48, v41 offset:3712
	ds_write_b8_d16_hi v48, v36 offset:3968
	v_lshrrev_b32_e32 v32, 24, v41
	ds_write_b8 v48, v32 offset:3776
	s_waitcnt vmcnt(4)
	v_lshlrev_b32_e32 v32, 16, v28
	v_and_b32_e32 v28, 0xffff0000, v28
	v_max_f32_e32 v32, v32, v32
	v_max_f32_e32 v28, v28, v28
	v_med3_f32 v32, v32, s7, v45
	v_med3_f32 v28, v28, s7, v45
	v_mov_b32_e32 v37, 0
	v_cvt_pk_fp8_f32 v37, v32, v28
	v_lshlrev_b32_e32 v33, 16, v29
	v_and_b32_e32 v29, 0xffff0000, v29
	v_max_f32_e32 v33, v33, v33
	v_max_f32_e32 v29, v29, v29
	v_lshlrev_b32_e32 v34, 16, v30
	v_and_b32_e32 v30, 0xffff0000, v30
	v_med3_f32 v28, v33, s7, v45
	v_med3_f32 v29, v29, s7, v45
	v_cvt_pk_fp8_f32 v37, v28, v29 op_sel:[0,0,1]
	v_max_f32_e32 v28, v34, v34
	v_max_f32_e32 v29, v30, v30
	v_med3_f32 v28, v28, s7, v45
	v_med3_f32 v29, v29, s7, v45
	v_mov_b32_e32 v32, 0
	v_cvt_pk_fp8_f32 v32, v28, v29
	v_lshlrev_b32_e32 v35, 16, v31
	v_and_b32_e32 v31, 0xffff0000, v31
	v_max_f32_e32 v30, v35, v35
	v_max_f32_e32 v29, v31, v31
	v_med3_f32 v28, v30, s7, v45
	v_med3_f32 v29, v29, s7, v45
	v_cvt_pk_fp8_f32 v32, v28, v29 op_sel:[0,0,1]
	v_lshrrev_b32_e32 v28, 24, v36
	ds_write_b8 v48, v28 offset:4032
	ds_write_b8 v48, v37 offset:4096
	ds_write_b8 v48, v32 offset:4352
	v_lshrrev_b32_e32 v28, 8, v37
	ds_write_b8 v48, v28 offset:4160
	v_lshrrev_b32_e32 v28, 8, v32
	ds_write_b8 v48, v28 offset:4416
	ds_write_b8_d16_hi v48, v37 offset:4224
	ds_write_b8_d16_hi v48, v32 offset:4480
	v_lshrrev_b32_e32 v28, 24, v37
	ds_write_b8 v48, v28 offset:4288
	v_lshlrev_b32_e32 v28, 16, v24
	v_and_b32_e32 v24, 0xffff0000, v24
	v_max_f32_e32 v28, v28, v28
	v_max_f32_e32 v24, v24, v24
	v_med3_f32 v28, v28, s7, v45
	v_med3_f32 v24, v24, s7, v45
	v_mov_b32_e32 v33, 0
	v_cvt_pk_fp8_f32 v33, v28, v24
	v_lshlrev_b32_e32 v29, 16, v25
	v_and_b32_e32 v25, 0xffff0000, v25
	v_max_f32_e32 v29, v29, v29
	v_max_f32_e32 v25, v25, v25
	v_lshlrev_b32_e32 v30, 16, v26
	v_and_b32_e32 v26, 0xffff0000, v26
	v_med3_f32 v24, v29, s7, v45
	v_med3_f32 v25, v25, s7, v45
	v_cvt_pk_fp8_f32 v33, v24, v25 op_sel:[0,0,1]
	v_max_f32_e32 v24, v30, v30
	v_max_f32_e32 v25, v26, v26
	v_med3_f32 v24, v24, s7, v45
	v_med3_f32 v25, v25, s7, v45
	v_mov_b32_e32 v28, 0
	v_cvt_pk_fp8_f32 v28, v24, v25
	v_lshlrev_b32_e32 v31, 16, v27
	v_and_b32_e32 v27, 0xffff0000, v27
	v_max_f32_e32 v26, v31, v31
	v_max_f32_e32 v25, v27, v27
	v_med3_f32 v24, v26, s7, v45
	v_med3_f32 v25, v25, s7, v45
	v_cvt_pk_fp8_f32 v28, v24, v25 op_sel:[0,0,1]
	v_lshrrev_b32_e32 v24, 24, v32
	ds_write_b8 v48, v24 offset:4544
	ds_write_b8 v48, v33 offset:4608
	ds_write_b8 v48, v28 offset:4864
	v_lshrrev_b32_e32 v24, 8, v33
	ds_write_b8 v48, v24 offset:4672
	v_lshrrev_b32_e32 v24, 8, v28
	ds_write_b8 v48, v24 offset:4928
	ds_write_b8_d16_hi v48, v33 offset:4736
	ds_write_b8_d16_hi v48, v28 offset:4992
	v_lshrrev_b32_e32 v24, 24, v33
	ds_write_b8 v48, v24 offset:4800
	v_lshlrev_b32_e32 v24, 16, v20
	v_and_b32_e32 v20, 0xffff0000, v20
	v_max_f32_e32 v24, v24, v24
	v_max_f32_e32 v20, v20, v20
	v_med3_f32 v24, v24, s7, v45
	v_med3_f32 v20, v20, s7, v45
	v_mov_b32_e32 v29, 0
	v_cvt_pk_fp8_f32 v29, v24, v20
	v_lshlrev_b32_e32 v25, 16, v21
	v_and_b32_e32 v21, 0xffff0000, v21
	v_max_f32_e32 v25, v25, v25
	v_max_f32_e32 v21, v21, v21
	v_lshlrev_b32_e32 v26, 16, v22
	v_and_b32_e32 v22, 0xffff0000, v22
	v_med3_f32 v20, v25, s7, v45
	v_med3_f32 v21, v21, s7, v45
	v_cvt_pk_fp8_f32 v29, v20, v21 op_sel:[0,0,1]
	v_max_f32_e32 v20, v26, v26
	v_max_f32_e32 v21, v22, v22
	v_med3_f32 v20, v20, s7, v45
	v_med3_f32 v21, v21, s7, v45
	v_mov_b32_e32 v24, 0
	v_cvt_pk_fp8_f32 v24, v20, v21
	v_lshlrev_b32_e32 v27, 16, v23
	v_and_b32_e32 v23, 0xffff0000, v23
	v_max_f32_e32 v22, v27, v27
	v_max_f32_e32 v21, v23, v23
	v_med3_f32 v20, v22, s7, v45
	v_med3_f32 v21, v21, s7, v45
	v_cvt_pk_fp8_f32 v24, v20, v21 op_sel:[0,0,1]
	v_lshrrev_b32_e32 v20, 24, v28
	ds_write_b8 v48, v20 offset:5056
	ds_write_b8 v48, v29 offset:5120
	ds_write_b8 v48, v24 offset:5376
	v_lshrrev_b32_e32 v20, 8, v29
	ds_write_b8 v48, v20 offset:5184
	v_lshrrev_b32_e32 v20, 8, v24
	ds_write_b8 v48, v20 offset:5440
	ds_write_b8_d16_hi v48, v29 offset:5248
	ds_write_b8_d16_hi v48, v24 offset:5504
	v_lshrrev_b32_e32 v20, 24, v29
	ds_write_b8 v48, v20 offset:5312
	v_lshlrev_b32_e32 v20, 16, v16
	v_and_b32_e32 v16, 0xffff0000, v16
	v_max_f32_e32 v20, v20, v20
	v_max_f32_e32 v16, v16, v16
	v_med3_f32 v20, v20, s7, v45
	v_med3_f32 v16, v16, s7, v45
	v_mov_b32_e32 v25, 0
	v_cvt_pk_fp8_f32 v25, v20, v16
	v_lshlrev_b32_e32 v21, 16, v17
	v_and_b32_e32 v17, 0xffff0000, v17
	v_max_f32_e32 v21, v21, v21
	v_max_f32_e32 v17, v17, v17
	v_lshlrev_b32_e32 v22, 16, v18
	v_and_b32_e32 v18, 0xffff0000, v18
	v_med3_f32 v16, v21, s7, v45
	v_med3_f32 v17, v17, s7, v45
	v_cvt_pk_fp8_f32 v25, v16, v17 op_sel:[0,0,1]
	v_max_f32_e32 v16, v22, v22
	v_max_f32_e32 v17, v18, v18
	v_med3_f32 v16, v16, s7, v45
	v_med3_f32 v17, v17, s7, v45
	v_mov_b32_e32 v20, 0
	v_cvt_pk_fp8_f32 v20, v16, v17
	v_lshlrev_b32_e32 v23, 16, v19
	v_and_b32_e32 v19, 0xffff0000, v19
	v_max_f32_e32 v18, v23, v23
	v_max_f32_e32 v17, v19, v19
	v_med3_f32 v16, v18, s7, v45
	v_med3_f32 v17, v17, s7, v45
	v_cvt_pk_fp8_f32 v20, v16, v17 op_sel:[0,0,1]
	v_lshrrev_b32_e32 v16, 24, v24
	ds_write_b8 v48, v16 offset:5568
	ds_write_b8 v48, v25 offset:5632
	ds_write_b8 v48, v20 offset:5888
	v_lshrrev_b32_e32 v16, 8, v25
	ds_write_b8 v48, v16 offset:5696
	v_lshrrev_b32_e32 v16, 8, v20
	ds_write_b8 v48, v16 offset:5952
	ds_write_b8_d16_hi v48, v25 offset:5760
	ds_write_b8_d16_hi v48, v20 offset:6016
	v_lshrrev_b32_e32 v16, 24, v25
	ds_write_b8 v48, v16 offset:5824
	s_waitcnt vmcnt(0)
	v_lshlrev_b32_e32 v16, 16, v12
	v_and_b32_e32 v12, 0xffff0000, v12
	v_max_f32_e32 v16, v16, v16
	v_max_f32_e32 v12, v12, v12
	v_med3_f32 v16, v16, s7, v45
	v_med3_f32 v12, v12, s7, v45
	v_mov_b32_e32 v21, 0
	v_cvt_pk_fp8_f32 v21, v16, v12
	v_lshlrev_b32_e32 v17, 16, v13
	v_and_b32_e32 v13, 0xffff0000, v13
	v_max_f32_e32 v17, v17, v17
	v_max_f32_e32 v13, v13, v13
	v_lshlrev_b32_e32 v18, 16, v14
	v_and_b32_e32 v14, 0xffff0000, v14
	v_med3_f32 v12, v17, s7, v45
	v_med3_f32 v13, v13, s7, v45
	v_cvt_pk_fp8_f32 v21, v12, v13 op_sel:[0,0,1]
	v_max_f32_e32 v12, v18, v18
	v_max_f32_e32 v13, v14, v14
	v_med3_f32 v12, v12, s7, v45
	v_med3_f32 v13, v13, s7, v45
	v_mov_b32_e32 v16, 0
	v_cvt_pk_fp8_f32 v16, v12, v13
	v_lshlrev_b32_e32 v19, 16, v15
	v_and_b32_e32 v15, 0xffff0000, v15
	v_max_f32_e32 v14, v19, v19
	v_max_f32_e32 v13, v15, v15
	v_med3_f32 v12, v14, s7, v45
	v_med3_f32 v13, v13, s7, v45
	v_cvt_pk_fp8_f32 v16, v12, v13 op_sel:[0,0,1]
	v_lshrrev_b32_e32 v12, 24, v20
	ds_write_b8 v48, v12 offset:6080
	ds_write_b8 v48, v21 offset:6144
	ds_write_b8 v48, v16 offset:6400
	v_lshrrev_b32_e32 v12, 8, v21
	ds_write_b8 v48, v12 offset:6208
	v_lshrrev_b32_e32 v12, 8, v16
	ds_write_b8 v48, v12 offset:6464
	ds_write_b8_d16_hi v48, v21 offset:6272
	ds_write_b8_d16_hi v48, v16 offset:6528
	v_lshrrev_b32_e32 v12, 24, v21
	ds_write_b8 v48, v12 offset:6336
	v_lshlrev_b32_e32 v12, 16, v8
	v_and_b32_e32 v8, 0xffff0000, v8
	v_max_f32_e32 v12, v12, v12
	v_max_f32_e32 v8, v8, v8
	v_med3_f32 v12, v12, s7, v45
	v_med3_f32 v8, v8, s7, v45
	v_mov_b32_e32 v17, 0
	v_cvt_pk_fp8_f32 v17, v12, v8
	v_lshlrev_b32_e32 v13, 16, v9
	v_and_b32_e32 v9, 0xffff0000, v9
	v_max_f32_e32 v13, v13, v13
	v_max_f32_e32 v9, v9, v9
	v_lshlrev_b32_e32 v14, 16, v10
	v_and_b32_e32 v10, 0xffff0000, v10
	v_med3_f32 v8, v13, s7, v45
	v_med3_f32 v9, v9, s7, v45
	v_cvt_pk_fp8_f32 v17, v8, v9 op_sel:[0,0,1]
	v_max_f32_e32 v8, v14, v14
	v_max_f32_e32 v9, v10, v10
	v_med3_f32 v8, v8, s7, v45
	v_med3_f32 v9, v9, s7, v45
	v_mov_b32_e32 v12, 0
	v_cvt_pk_fp8_f32 v12, v8, v9
	v_lshlrev_b32_e32 v15, 16, v11
	v_and_b32_e32 v11, 0xffff0000, v11
	v_max_f32_e32 v10, v15, v15
	v_max_f32_e32 v9, v11, v11
	v_med3_f32 v8, v10, s7, v45
	v_med3_f32 v9, v9, s7, v45
	v_cvt_pk_fp8_f32 v12, v8, v9 op_sel:[0,0,1]
	v_lshrrev_b32_e32 v8, 24, v16
	ds_write_b8 v48, v8 offset:6592
	ds_write_b8 v48, v17 offset:6656
	ds_write_b8 v48, v12 offset:6912
	v_lshrrev_b32_e32 v8, 8, v17
	ds_write_b8 v48, v8 offset:6720
	v_lshrrev_b32_e32 v8, 8, v12
	ds_write_b8 v48, v8 offset:6976
	ds_write_b8_d16_hi v48, v17 offset:6784
	ds_write_b8_d16_hi v48, v12 offset:7040
	v_lshrrev_b32_e32 v8, 24, v17
	ds_write_b8 v48, v8 offset:6848
	v_lshlrev_b32_e32 v8, 16, v4
	v_and_b32_e32 v4, 0xffff0000, v4
	v_max_f32_e32 v8, v8, v8
	v_max_f32_e32 v4, v4, v4
	v_med3_f32 v8, v8, s7, v45
	v_med3_f32 v4, v4, s7, v45
	v_mov_b32_e32 v13, 0
	v_cvt_pk_fp8_f32 v13, v8, v4
	v_lshlrev_b32_e32 v9, 16, v5
	v_and_b32_e32 v5, 0xffff0000, v5
	v_max_f32_e32 v9, v9, v9
	v_max_f32_e32 v5, v5, v5
	v_lshlrev_b32_e32 v10, 16, v6
	v_and_b32_e32 v6, 0xffff0000, v6
	v_med3_f32 v4, v9, s7, v45
	v_med3_f32 v5, v5, s7, v45
	v_cvt_pk_fp8_f32 v13, v4, v5 op_sel:[0,0,1]
	v_max_f32_e32 v4, v10, v10
	v_max_f32_e32 v5, v6, v6
	v_med3_f32 v4, v4, s7, v45
	v_med3_f32 v5, v5, s7, v45
	v_mov_b32_e32 v8, 0
	v_cvt_pk_fp8_f32 v8, v4, v5
	v_lshlrev_b32_e32 v11, 16, v7
	v_and_b32_e32 v7, 0xffff0000, v7
	v_max_f32_e32 v6, v11, v11
	v_max_f32_e32 v5, v7, v7
	v_med3_f32 v4, v6, s7, v45
	v_med3_f32 v5, v5, s7, v45
	v_cvt_pk_fp8_f32 v8, v4, v5 op_sel:[0,0,1]
	v_lshrrev_b32_e32 v4, 24, v12
	ds_write_b8 v48, v4 offset:7104
	ds_write_b8 v48, v13 offset:7168
	ds_write_b8 v48, v8 offset:7424
	v_lshrrev_b32_e32 v4, 8, v13
	ds_write_b8 v48, v4 offset:7232
	v_lshrrev_b32_e32 v4, 8, v8
	ds_write_b8 v48, v4 offset:7488
	ds_write_b8_d16_hi v48, v13 offset:7296
	ds_write_b8_d16_hi v48, v8 offset:7552
	v_lshrrev_b32_e32 v4, 24, v13
	ds_write_b8 v48, v4 offset:7360
	v_lshlrev_b32_e32 v4, 16, v0
	v_and_b32_e32 v0, 0xffff0000, v0
	v_max_f32_e32 v4, v4, v4
	v_max_f32_e32 v0, v0, v0
	v_med3_f32 v4, v4, s7, v45
	v_med3_f32 v0, v0, s7, v45
	v_mov_b32_e32 v9, 0
	v_cvt_pk_fp8_f32 v9, v4, v0
	v_lshlrev_b32_e32 v5, 16, v1
	v_and_b32_e32 v1, 0xffff0000, v1
	v_max_f32_e32 v5, v5, v5
	v_max_f32_e32 v1, v1, v1
	v_lshlrev_b32_e32 v6, 16, v2
	v_and_b32_e32 v2, 0xffff0000, v2
	v_med3_f32 v0, v5, s7, v45
	v_med3_f32 v1, v1, s7, v45
	v_cvt_pk_fp8_f32 v9, v0, v1 op_sel:[0,0,1]
	v_max_f32_e32 v0, v6, v6
	v_max_f32_e32 v1, v2, v2
	v_med3_f32 v0, v0, s7, v45
	v_med3_f32 v1, v1, s7, v45
	v_mov_b32_e32 v4, 0
	v_cvt_pk_fp8_f32 v4, v0, v1
	v_lshlrev_b32_e32 v7, 16, v3
	v_and_b32_e32 v3, 0xffff0000, v3
	v_max_f32_e32 v2, v7, v7
	v_max_f32_e32 v1, v3, v3
	v_med3_f32 v0, v2, s7, v45
	v_med3_f32 v1, v1, s7, v45
	v_cvt_pk_fp8_f32 v4, v0, v1 op_sel:[0,0,1]
	v_lshrrev_b32_e32 v0, 24, v8
	ds_write_b8 v48, v0 offset:7616
	ds_write_b8 v48, v9 offset:7680
	ds_write_b8 v48, v4 offset:7936
	v_lshrrev_b32_e32 v0, 8, v9
	ds_write_b8 v48, v0 offset:7744
	v_lshrrev_b32_e32 v0, 8, v4
	ds_write_b8 v48, v0 offset:8000
	ds_write_b8_d16_hi v48, v9 offset:7808
	ds_write_b8_d16_hi v48, v4 offset:8064
	v_lshrrev_b32_e32 v0, 24, v9
	ds_write_b8 v48, v0 offset:7872
	v_lshrrev_b32_e32 v0, 24, v4
	ds_write_b8 v48, v0 offset:8128
	s_waitcnt lgkmcnt(0)
	s_cbranch_vccnz .LBB0_491
	v_add_u32_e32 v16, s10, v44
	ds_read_b128 v[0:3], v16
	ds_read_b128 v[4:7], v16 offset:1024
	ds_read_b128 v[8:11], v16 offset:2048
	v_add_co_u32_e32 v12, vcc, 0xfffff000, v46
	s_nop 1
	v_addc_co_u32_e32 v13, vcc, -1, v47, vcc
	s_waitcnt lgkmcnt(2)
	global_store_dwordx4 v[12:13], v[0:3], off offset:-3072 nt
	s_waitcnt lgkmcnt(1)
	global_store_dwordx4 v[12:13], v[4:7], off offset:-2048 nt
	s_waitcnt lgkmcnt(0)
	global_store_dwordx4 v[12:13], v[8:11], off offset:-1024 nt
	ds_read_b128 v[0:3], v16 offset:3072
	ds_read_b128 v[4:7], v16 offset:4096
	ds_read_b128 v[8:11], v16 offset:5120
	ds_read_b128 v[12:15], v16 offset:6144
	ds_read_b128 v[16:19], v16 offset:7168
	s_waitcnt lgkmcnt(4)
	global_store_dwordx4 v[46:47], v[0:3], off offset:-4096 nt
	s_waitcnt lgkmcnt(3)
	global_store_dwordx4 v[46:47], v[4:7], off offset:-3072 nt
	s_waitcnt lgkmcnt(2)
	global_store_dwordx4 v[46:47], v[8:11], off offset:-2048 nt
	s_waitcnt lgkmcnt(1)
	global_store_dwordx4 v[46:47], v[12:15], off offset:-1024 nt
	s_waitcnt lgkmcnt(0)
	global_store_dwordx4 v[46:47], v[16:19], off nt
	s_branch .LBB0_491

.LBB0_1411:
	s_ashr_i32 s11, s10, 31
	v_lshl_add_u64 v[12:13], s[0:1], 0, v[10:11]
	s_lshl_b64 s[30:31], s[10:11], 2
	v_add_co_u32_e32 v34, vcc, s23, v12
	s_add_u32 s38, s13, s30
	s_nop 0
	v_addc_co_u32_e32 v35, vcc, 0, v13, vcc
	s_addc_u32 s39, s16, s31
	global_load_dwordx2 v[66:67], v[34:35], off nt
	global_load_dwordx2 v[68:69], v[34:35], off offset:512 nt
	global_load_dwordx2 v[70:71], v[34:35], off offset:1024 nt
	global_load_dwordx2 v[72:73], v[34:35], off offset:1536 nt
	global_load_dwordx2 v[76:77], v[34:35], off offset:2048 nt
	global_load_dwordx2 v[78:79], v[34:35], off offset:2560 nt
	global_load_dwordx2 v[80:81], v[34:35], off offset:3072 nt
	global_load_dwordx2 v[82:83], v[34:35], off offset:3584 nt
	global_load_dwordx2 v[84:85], v5, s[38:39]
	s_add_u32 s38, s17, s30
	s_addc_u32 s39, s18, s31
	s_add_i32 s40, s10, 1
	s_ashr_i32 s41, s40, 31
	global_load_dword v75, v5, s[38:39]
	s_lshl_b64 s[38:39], s[40:41], 2
	s_add_u32 s40, s17, s38
	s_addc_u32 s41, s18, s39
	global_load_dword v87, v5, s[40:41]
	s_add_u32 s30, s19, s30
	s_addc_u32 s31, s20, s31
	global_load_dword v86, v5, s[30:31]
	s_add_u32 s30, s19, s38
	s_addc_u32 s31, s20, s39
	s_min_i32 s11, s29, 0x2000
	global_load_dword v88, v5, s[30:31]
	s_ashr_i32 s30, s11, 12
	s_mul_i32 s30, s30, 6
	s_ashr_i32 s31, s30, 31
	s_lshl_b64 s[30:31], s[30:31], 13
	s_add_u32 s30, s21, s30
	s_addc_u32 s31, s22, s31
	s_add_u32 s30, s30, 0xa000
	s_addc_u32 s31, s31, 0
	global_load_dwordx4 v[34:37], v19, s[30:31]
	global_load_dwordx4 v[38:41], v19, s[30:31] offset:1024
	global_load_dwordx4 v[42:45], v19, s[30:31] offset:2048
	global_load_dwordx4 v[46:49], v19, s[30:31] offset:3072
	global_load_dwordx4 v[50:53], v20, s[30:31]
	global_load_dwordx4 v[54:57], v21, s[30:31]
	global_load_dwordx4 v[58:61], v22, s[30:31]
	global_load_dwordx4 v[62:65], v23, s[30:31]
	v_add_co_u32_e32 v16, vcc, s24, v12
	s_lshl_b32 s11, s11, 1
	s_nop 0
	v_addc_co_u32_e32 v17, vcc, 0, v13, vcc
	s_and_b32 s11, s11, 0xffffe000
	v_add_u32_e32 v168, s11, v4
	v_add_u32_e32 v169, s11, v18
	v_add_co_u32_e32 v12, vcc, s26, v12
	v_lshl_add_u64 v[14:15], s[0:1], 0, v[8:9]
	s_nop 0
	v_addc_co_u32_e32 v13, vcc, 0, v13, vcc
	v_add_co_u32_e32 v14, vcc, s28, v14
	v_mov_b32_e32 v26, 0
	s_nop 0
	v_addc_co_u32_e32 v15, vcc, 0, v15, vcc
	v_mov_b32_e32 v27, 0
	v_mov_b32_e32 v28, 0
	v_mov_b32_e32 v29, 0
	v_mov_b32_e32 v30, 0
	v_mov_b32_e32 v31, 0
	v_mov_b32_e32 v32, 0
	v_mov_b32_e32 v33, 0
	s_add_i32 s29, s29, s2
	s_add_i32 s10, s10, s3
	v_lshl_add_u64 v[8:9], v[8:9], 0, s[6:7]
	v_lshl_add_u64 v[10:11], v[10:11], 0, s[8:9]
	s_cmpk_gt_i32 s29, 0x21ff
	s_waitcnt vmcnt(20)
	v_lshlrev_b32_e32 v90, 16, v66
	v_and_b32_e32 v91, 0xffff0000, v66
	s_waitcnt vmcnt(19)
	v_lshlrev_b32_e32 v92, 16, v68
	v_and_b32_e32 v93, 0xffff0000, v68
	s_waitcnt vmcnt(18)
	v_lshlrev_b32_e32 v94, 16, v70
	v_and_b32_e32 v95, 0xffff0000, v70
	s_waitcnt vmcnt(17)
	v_lshlrev_b32_e32 v96, 16, v72
	v_and_b32_e32 v97, 0xffff0000, v72
	s_waitcnt vmcnt(12)
	v_lshlrev_b32_e32 v84, 2, v84
	v_lshlrev_b32_e32 v85, 2, v85
	v_add_u32_e32 v84, s5, v84
	v_add_u32_e32 v85, s5, v85
	ds_read_b32 v84, v84
	ds_read_b32 v85, v85
	v_lshlrev_b32_e32 v66, 16, v67
	v_and_b32_e32 v67, 0xffff0000, v67
	v_lshlrev_b32_e32 v68, 16, v69
	s_waitcnt vmcnt(11) lgkmcnt(1)
	v_add_u32_e32 v84, v75, v84
	s_waitcnt vmcnt(10) lgkmcnt(0)
	v_add_u32_e32 v106, v87, v85
	v_ashrrev_i32_e32 v85, 31, v84
	v_ashrrev_i32_e32 v107, 31, v106
	v_lshlrev_b64 v[84:85], 12, v[84:85]
	v_lshlrev_b64 v[106:107], 12, v[106:107]
	v_lshl_add_u64 v[84:85], v[6:7], 0, v[84:85]
	v_lshl_add_u64 v[106:107], v[6:7], 0, v[106:107]
	global_load_dwordx2 v[108:109], v[84:85], off nt
	global_load_dwordx2 v[110:111], v[106:107], off nt
	global_load_dwordx2 v[112:113], v[84:85], off offset:512 nt
	global_load_dwordx2 v[114:115], v[106:107], off offset:512 nt
	global_load_dwordx2 v[116:117], v[84:85], off offset:1024 nt
	global_load_dwordx2 v[118:119], v[106:107], off offset:1024 nt
	global_load_dwordx2 v[120:121], v[84:85], off offset:1536 nt
	global_load_dwordx2 v[122:123], v[106:107], off offset:1536 nt
	global_load_dwordx2 v[124:125], v[84:85], off offset:2048 nt
	global_load_dwordx2 v[126:127], v[106:107], off offset:2048 nt
	global_load_dwordx2 v[128:129], v[84:85], off offset:2560 nt
	global_load_dwordx2 v[130:131], v[106:107], off offset:2560 nt
	global_load_dwordx2 v[132:133], v[84:85], off offset:3072 nt
	global_load_dwordx2 v[134:135], v[106:107], off offset:3072 nt
	s_nop 0
	global_load_dwordx2 v[84:85], v[84:85], off offset:3584 nt
	s_nop 0
	global_load_dwordx2 v[106:107], v[106:107], off offset:3584 nt
	v_and_b32_e32 v69, 0xffff0000, v69
	v_lshlrev_b32_e32 v70, 16, v71
	v_and_b32_e32 v71, 0xffff0000, v71
	v_lshlrev_b32_e32 v72, 16, v73
	v_and_b32_e32 v73, 0xffff0000, v73
	v_lshlrev_b32_e32 v98, 16, v76
	v_and_b32_e32 v99, 0xffff0000, v76
	v_lshlrev_b32_e32 v100, 16, v78
	v_and_b32_e32 v101, 0xffff0000, v78
	v_lshlrev_b32_e32 v76, 16, v77
	v_and_b32_e32 v77, 0xffff0000, v77
	v_lshlrev_b32_e32 v78, 16, v79
	v_and_b32_e32 v79, 0xffff0000, v79
	v_lshlrev_b32_e32 v102, 16, v80
	v_and_b32_e32 v103, 0xffff0000, v80
	v_lshlrev_b32_e32 v104, 16, v82
	v_and_b32_e32 v105, 0xffff0000, v82
	v_lshlrev_b32_e32 v82, 16, v83
	v_and_b32_e32 v83, 0xffff0000, v83
	v_lshlrev_b32_e32 v80, 16, v81
	v_and_b32_e32 v81, 0xffff0000, v81
	s_waitcnt vmcnt(15)
	v_lshlrev_b32_e32 v136, 16, v108
	s_waitcnt vmcnt(14)
	v_lshlrev_b32_e32 v138, 16, v110
	v_and_b32_e32 v139, 0xffff0000, v110
	v_lshlrev_b32_e32 v110, 16, v111
	v_and_b32_e32 v111, 0xffff0000, v111
	s_waitcnt vmcnt(12)
	v_lshlrev_b32_e32 v142, 16, v114
	v_and_b32_e32 v143, 0xffff0000, v114
	v_lshlrev_b32_e32 v114, 16, v115
	v_and_b32_e32 v115, 0xffff0000, v115
	s_waitcnt vmcnt(10)
	v_lshlrev_b32_e32 v146, 16, v118
	v_and_b32_e32 v147, 0xffff0000, v118
	v_lshlrev_b32_e32 v118, 16, v119
	v_and_b32_e32 v119, 0xffff0000, v119
	s_waitcnt vmcnt(8)
	v_lshlrev_b32_e32 v150, 16, v122
	v_and_b32_e32 v151, 0xffff0000, v122
	v_and_b32_e32 v137, 0xffff0000, v108
	v_lshlrev_b32_e32 v108, 16, v109
	v_and_b32_e32 v109, 0xffff0000, v109
	v_lshlrev_b32_e32 v140, 16, v112
	v_and_b32_e32 v141, 0xffff0000, v112
	v_lshlrev_b32_e32 v112, 16, v113
	v_and_b32_e32 v113, 0xffff0000, v113
	v_lshlrev_b32_e32 v144, 16, v116
	v_and_b32_e32 v145, 0xffff0000, v116
	v_lshlrev_b32_e32 v116, 16, v117
	v_and_b32_e32 v117, 0xffff0000, v117
	v_lshlrev_b32_e32 v148, 16, v120
	v_and_b32_e32 v149, 0xffff0000, v120
	v_lshlrev_b32_e32 v122, 16, v123
	v_and_b32_e32 v123, 0xffff0000, v123
	s_waitcnt vmcnt(6)
	v_lshlrev_b32_e32 v154, 16, v126
	v_and_b32_e32 v155, 0xffff0000, v126
	v_lshlrev_b32_e32 v126, 16, v127
	v_and_b32_e32 v127, 0xffff0000, v127
	s_waitcnt vmcnt(4)
	v_lshlrev_b32_e32 v158, 16, v130
	v_and_b32_e32 v159, 0xffff0000, v130
	v_lshlrev_b32_e32 v130, 16, v131
	v_and_b32_e32 v131, 0xffff0000, v131
	s_waitcnt vmcnt(2)
	v_lshlrev_b32_e32 v162, 16, v134
	v_and_b32_e32 v163, 0xffff0000, v134
	v_lshlrev_b32_e32 v134, 16, v135
	v_and_b32_e32 v135, 0xffff0000, v135
	s_waitcnt vmcnt(0)
	v_lshlrev_b32_e32 v166, 16, v106
	v_and_b32_e32 v167, 0xffff0000, v106
	v_lshlrev_b32_e32 v106, 16, v107
	v_and_b32_e32 v107, 0xffff0000, v107
	v_pk_mul_f32 v[138:139], v[88:89], v[138:139] op_sel_hi:[0,1]
	v_pk_mul_f32 v[110:111], v[88:89], v[110:111] op_sel_hi:[0,1]
	v_pk_mul_f32 v[142:143], v[88:89], v[142:143] op_sel_hi:[0,1]
	v_pk_mul_f32 v[114:115], v[88:89], v[114:115] op_sel_hi:[0,1]
	v_pk_mul_f32 v[146:147], v[88:89], v[146:147] op_sel_hi:[0,1]
	v_pk_mul_f32 v[118:119], v[88:89], v[118:119] op_sel_hi:[0,1]
	v_pk_mul_f32 v[150:151], v[88:89], v[150:151] op_sel_hi:[0,1]
	v_lshlrev_b32_e32 v120, 16, v121
	v_and_b32_e32 v121, 0xffff0000, v121
	v_lshlrev_b32_e32 v152, 16, v124
	v_and_b32_e32 v153, 0xffff0000, v124
	v_lshlrev_b32_e32 v124, 16, v125
	v_and_b32_e32 v125, 0xffff0000, v125
	v_lshlrev_b32_e32 v156, 16, v128
	v_and_b32_e32 v157, 0xffff0000, v128
	v_lshlrev_b32_e32 v128, 16, v129
	v_and_b32_e32 v129, 0xffff0000, v129
	v_lshlrev_b32_e32 v160, 16, v132
	v_and_b32_e32 v161, 0xffff0000, v132
	v_lshlrev_b32_e32 v132, 16, v133
	v_and_b32_e32 v133, 0xffff0000, v133
	v_lshlrev_b32_e32 v164, 16, v84
	v_and_b32_e32 v165, 0xffff0000, v84
	v_lshlrev_b32_e32 v84, 16, v85
	v_and_b32_e32 v85, 0xffff0000, v85
	v_pk_mul_f32 v[122:123], v[88:89], v[122:123] op_sel_hi:[0,1]
	v_pk_mul_f32 v[154:155], v[88:89], v[154:155] op_sel_hi:[0,1]
	v_pk_mul_f32 v[126:127], v[88:89], v[126:127] op_sel_hi:[0,1]
	v_pk_mul_f32 v[158:159], v[88:89], v[158:159] op_sel_hi:[0,1]
	v_pk_mul_f32 v[130:131], v[88:89], v[130:131] op_sel_hi:[0,1]
	v_pk_mul_f32 v[162:163], v[88:89], v[162:163] op_sel_hi:[0,1]
	v_pk_mul_f32 v[134:135], v[88:89], v[134:135] op_sel_hi:[0,1]
	v_pk_mul_f32 v[166:167], v[88:89], v[166:167] op_sel_hi:[0,1]
	v_pk_mul_f32 v[88:89], v[88:89], v[106:107] op_sel_hi:[0,1]
	v_pk_fma_f32 v[106:107], v[86:87], v[136:137], v[138:139] op_sel_hi:[0,1,1]
	v_pk_fma_f32 v[108:109], v[86:87], v[108:109], v[110:111] op_sel_hi:[0,1,1]
	v_pk_fma_f32 v[110:111], v[86:87], v[140:141], v[142:143] op_sel_hi:[0,1,1]
	v_pk_fma_f32 v[112:113], v[86:87], v[112:113], v[114:115] op_sel_hi:[0,1,1]
	v_pk_fma_f32 v[114:115], v[86:87], v[144:145], v[146:147] op_sel_hi:[0,1,1]
	v_pk_fma_f32 v[116:117], v[86:87], v[116:117], v[118:119] op_sel_hi:[0,1,1]
	v_pk_fma_f32 v[118:119], v[86:87], v[148:149], v[150:151] op_sel_hi:[0,1,1]
	v_pk_fma_f32 v[120:121], v[86:87], v[120:121], v[122:123] op_sel_hi:[0,1,1]
	v_pk_fma_f32 v[122:123], v[86:87], v[152:153], v[154:155] op_sel_hi:[0,1,1]
	v_pk_fma_f32 v[124:125], v[86:87], v[124:125], v[126:127] op_sel_hi:[0,1,1]
	v_pk_fma_f32 v[126:127], v[86:87], v[156:157], v[158:159] op_sel_hi:[0,1,1]
	v_pk_fma_f32 v[128:129], v[86:87], v[128:129], v[130:131] op_sel_hi:[0,1,1]
	v_pk_fma_f32 v[130:131], v[86:87], v[160:161], v[162:163] op_sel_hi:[0,1,1]
	v_pk_fma_f32 v[132:133], v[86:87], v[132:133], v[134:135] op_sel_hi:[0,1,1]
	v_pk_fma_f32 v[134:135], v[86:87], v[164:165], v[166:167] op_sel_hi:[0,1,1]
	v_pk_fma_f32 v[84:85], v[86:87], v[84:85], v[88:89] op_sel_hi:[0,1,1]
	v_pk_fma_f32 v[86:87], v[34:35], v[106:107], v[90:91]
	v_pk_fma_f32 v[88:89], v[38:39], v[110:111], v[92:93]
	v_pk_fma_f32 v[42:43], v[42:43], v[114:115], v[94:95]
	v_pk_fma_f32 v[46:47], v[46:47], v[118:119], v[96:97]
	v_mul_f32_e32 v75, v87, v87
	v_mul_f32_e32 v94, v89, v89
	v_mov_b32_e32 v38, v43
	v_mov_b32_e32 v39, v47
	v_pk_fma_f32 v[66:67], v[36:37], v[108:109], v[66:67]
	v_pk_fma_f32 v[68:69], v[40:41], v[112:113], v[68:69]
	v_pk_fma_f32 v[44:45], v[44:45], v[116:117], v[70:71]
	v_pk_fma_f32 v[48:49], v[48:49], v[120:121], v[72:73]
	v_pk_fma_f32 v[50:51], v[50:51], v[122:123], v[98:99]
	v_pk_fma_f32 v[54:55], v[54:55], v[126:127], v[100:101]
	v_cvt_pk_bf16_f32 v34, v86, v87
	v_cvt_pk_bf16_f32 v35, v66, v67
	v_mov_b32_e32 v36, v42
	v_mov_b32_e32 v37, v46
	v_fmac_f32_e32 v75, v86, v86
	v_fmac_f32_e32 v94, v88, v88
	v_pk_mul_f32 v[38:39], v[38:39], v[38:39]
	v_pk_fma_f32 v[52:53], v[52:53], v[124:125], v[76:77]
	v_mov_b32_e32 v40, v44
	v_mov_b32_e32 v41, v48
	v_mov_b32_e32 v76, v51
	v_mov_b32_e32 v77, v55
	global_store_dwordx2 v[16:17], v[34:35], off nt
	v_cvt_pk_bf16_f32 v34, v88, v89
	v_cvt_pk_bf16_f32 v35, v68, v69
	v_fmac_f32_e32 v75, v66, v66
	v_fmac_f32_e32 v94, v68, v68
	v_pk_fma_f32 v[36:37], v[36:37], v[36:37], v[38:39]
	v_pk_fma_f32 v[56:57], v[56:57], v[128:129], v[78:79]
	v_pk_fma_f32 v[58:59], v[58:59], v[130:131], v[102:103]
	v_pk_fma_f32 v[62:63], v[62:63], v[134:135], v[104:105]
	v_mov_b32_e32 v70, v45
	v_mov_b32_e32 v71, v49
	v_mov_b32_e32 v72, v50
	v_mov_b32_e32 v73, v54
	v_pk_mul_f32 v[76:77], v[76:77], v[76:77]
	global_store_dwordx2 v[16:17], v[34:35], off offset:512 nt
	v_cvt_pk_bf16_f32 v34, v42, v43
	v_cvt_pk_bf16_f32 v35, v44, v45
	v_fmac_f32_e32 v75, v67, v67
	v_fmac_f32_e32 v94, v69, v69
	v_pk_fma_f32 v[36:37], v[40:41], v[40:41], v[36:37]
	v_pk_fma_f32 v[64:65], v[64:65], v[84:85], v[82:83]
	v_mov_b32_e32 v78, v52
	v_mov_b32_e32 v79, v56
	v_mov_b32_e32 v84, v59
	v_mov_b32_e32 v85, v63
	v_pk_fma_f32 v[38:39], v[72:73], v[72:73], v[76:77]
	global_store_dwordx2 v[16:17], v[34:35], off offset:1024 nt
	v_cvt_pk_bf16_f32 v34, v46, v47
	v_cvt_pk_bf16_f32 v35, v48, v49
	v_add_f32_e32 v75, v75, v94
	v_pk_fma_f32 v[36:37], v[70:71], v[70:71], v[36:37]
	v_pk_fma_f32 v[60:61], v[60:61], v[132:133], v[80:81]
	v_mov_b32_e32 v80, v53
	v_mov_b32_e32 v81, v57
	v_mov_b32_e32 v82, v58
	v_mov_b32_e32 v83, v62
	v_pk_mul_f32 v[84:85], v[84:85], v[84:85]
	v_pk_fma_f32 v[38:39], v[78:79], v[78:79], v[38:39]
	global_store_dwordx2 v[16:17], v[34:35], off offset:1536 nt
	v_cvt_pk_bf16_f32 v34, v50, v51
	v_cvt_pk_bf16_f32 v35, v52, v53
	v_add_f32_e32 v36, v75, v36
	v_mov_b32_e32 v90, v60
	v_mov_b32_e32 v91, v64
	v_pk_fma_f32 v[72:73], v[82:83], v[82:83], v[84:85]
	v_pk_fma_f32 v[70:71], v[80:81], v[80:81], v[38:39]
	global_store_dwordx2 v[16:17], v[34:35], off offset:2048 nt
	v_cvt_pk_bf16_f32 v34, v54, v55
	v_cvt_pk_bf16_f32 v35, v56, v57
	v_add_f32_e32 v36, v36, v37
	v_mov_b32_e32 v92, v61
	v_mov_b32_e32 v93, v65
	v_pk_fma_f32 v[40:41], v[90:91], v[90:91], v[72:73]
	global_store_dwordx2 v[16:17], v[34:35], off offset:2560 nt
	v_cvt_pk_bf16_f32 v34, v58, v59
	v_cvt_pk_bf16_f32 v35, v60, v61
	v_add_f32_e32 v70, v36, v70
	v_pk_fma_f32 v[72:73], v[92:93], v[92:93], v[40:41]
	global_store_dwordx2 v[16:17], v[34:35], off offset:3072 nt
	v_cvt_pk_bf16_f32 v76, v62, v63
	v_cvt_pk_bf16_f32 v77, v64, v65
	ds_read_b128 v[34:37], v168
	ds_read_b128 v[38:41], v169
	global_store_dwordx2 v[16:17], v[76:77], off offset:3584 nt
	v_add_f32_e32 v16, v70, v71
	v_add_f32_e32 v16, v16, v72
	v_add_f32_e32 v16, v16, v73
	v_mov_b32_e32 v17, v16
	s_nop 1
	v_mov_b32_dpp v17, v17 quad_perm:[1,0,3,2] row_mask:0xf bank_mask:0xf
	v_add_f32_e32 v16, v16, v17
	v_mov_b32_e32 v17, v16
	s_nop 1
	v_mov_b32_dpp v17, v17 quad_perm:[2,3,0,1] row_mask:0xf bank_mask:0xf
	v_add_f32_e32 v16, v16, v17
	v_mov_b32_e32 v17, v16
	s_nop 1
	v_mov_b32_dpp v17, v17 row_half_mirror row_mask:0xf bank_mask:0xf
	v_add_f32_e32 v16, v16, v17
	v_mov_b32_e32 v17, v16
	s_nop 1
	v_mov_b32_dpp v17, v17 row_mirror row_mask:0xf bank_mask:0xf
	v_add_f32_e32 v16, v16, v17
	s_nop 0
	v_readlane_b32 s11, v16, 16
	v_readlane_b32 s38, v16, 48
	v_readlane_b32 s30, v16, 0
	v_readlane_b32 s31, v16, 32
	v_mov_b32_e32 v16, s11
	v_mov_b32_e32 v17, s38
	v_pk_add_f32 v[16:17], s[30:31], v[16:17]
	s_nop 0
	v_add_f32_e32 v16, v16, v17
	v_fmamk_f32 v16, v16, 0x3a000000, v24
	v_mul_f32_e32 v17, 0x4b800000, v16
	v_cmp_gt_f32_e32 vcc, s25, v16
	s_nop 1
	v_cndmask_b32_e32 v16, v16, v17, vcc
	v_rsq_f32_e32 v16, v16
	s_nop 0
	v_mul_f32_e32 v17, 0x45800000, v16
	v_cndmask_b32_e32 v16, v16, v17, vcc
	v_mul_f32_e32 v17, v86, v16
	v_mul_f32_e32 v70, v87, v16
	v_mul_f32_e32 v66, v66, v16
	v_mul_f32_e32 v67, v67, v16
	s_waitcnt lgkmcnt(0)
	v_fma_f32 v34, v34, v17, v38
	v_fma_f32 v35, v35, v70, v39
	v_fma_f32 v36, v36, v66, v40
	v_fmac_f32_e32 v41, v37, v67
	v_mul_f32_e32 v71, v88, v16
	v_mul_f32_e32 v72, v89, v16
	v_mul_f32_e32 v68, v68, v16
	v_mul_f32_e32 v69, v69, v16
	v_mul_f32_e32 v42, v42, v16
	v_mul_f32_e32 v43, v43, v16
	v_mul_f32_e32 v44, v44, v16
	v_mul_f32_e32 v45, v45, v16
	v_mul_f32_e32 v46, v46, v16
	v_mul_f32_e32 v47, v47, v16
	v_mul_f32_e32 v48, v48, v16
	v_mul_f32_e32 v49, v49, v16
	v_mul_f32_e32 v50, v50, v16
	v_mul_f32_e32 v51, v51, v16
	v_mul_f32_e32 v52, v52, v16
	v_mul_f32_e32 v53, v53, v16
	v_mul_f32_e32 v54, v54, v16
	v_mul_f32_e32 v55, v55, v16
	v_mul_f32_e32 v56, v56, v16
	v_mul_f32_e32 v57, v57, v16
	v_mul_f32_e32 v58, v58, v16
	v_mul_f32_e32 v59, v59, v16
	v_mul_f32_e32 v60, v60, v16
	v_mul_f32_e32 v61, v61, v16
	v_mul_f32_e32 v62, v62, v16
	v_mul_f32_e32 v63, v63, v16
	v_mul_f32_e32 v64, v64, v16
	v_mul_f32_e32 v65, v65, v16
	v_cvt_pk_bf16_f32 v16, v34, v35
	v_cvt_pk_bf16_f32 v17, v36, v41
	v_med3_f32 v66, v34, s27, v25
	v_med3_f32 v67, v35, s27, v25
	v_med3_f32 v70, v36, s27, v25
	v_med3_f32 v73, v41, s27, v25
	ds_read_b128 v[34:37], v168 offset:1024
	ds_read_b128 v[38:41], v169 offset:1024
	v_cvt_pk_fp8_f32 v26, v66, v67
	global_store_dwordx2 v[12:13], v[16:17], off nt
	v_cvt_pk_fp8_f32 v26, v70, v73 op_sel:[0,0,1]
	s_waitcnt lgkmcnt(0)
	v_fma_f32 v16, v34, v71, v38
	v_fma_f32 v17, v35, v72, v39
	v_fma_f32 v34, v36, v68, v40
	v_med3_f32 v35, v16, s27, v25
	v_med3_f32 v36, v17, s27, v25
	v_cvt_pk_fp8_f32 v27, v35, v36
	v_fmac_f32_e32 v41, v37, v69
	v_med3_f32 v66, v34, s27, v25
	v_med3_f32 v67, v41, s27, v25
	global_store_dword v[14:15], v26, off nt
	v_cvt_pk_bf16_f32 v16, v16, v17
	v_cvt_pk_bf16_f32 v17, v34, v41
	ds_read_b128 v[34:37], v168 offset:2048
	ds_read_b128 v[38:41], v169 offset:2048
	v_cvt_pk_fp8_f32 v27, v66, v67 op_sel:[0,0,1]
	global_store_dwordx2 v[12:13], v[16:17], off offset:512 nt
	s_waitcnt lgkmcnt(0)
	v_fma_f32 v26, v42, v34, v38
	v_fma_f32 v34, v43, v35, v39
	v_fma_f32 v35, v44, v36, v40
	v_fmac_f32_e32 v41, v45, v37
	global_store_dword v[14:15], v27, off offset:256 nt
	v_cvt_pk_bf16_f32 v16, v26, v34
	v_cvt_pk_bf16_f32 v17, v35, v41
	v_med3_f32 v26, v26, s27, v25
	v_med3_f32 v27, v34, s27, v25
	v_med3_f32 v42, v35, s27, v25
	v_med3_f32 v43, v41, s27, v25
	ds_read_b128 v[34:37], v168 offset:3072
	ds_read_b128 v[38:41], v169 offset:3072
	v_cvt_pk_fp8_f32 v28, v26, v27
	global_store_dwordx2 v[12:13], v[16:17], off offset:1024 nt
	v_cvt_pk_fp8_f32 v28, v42, v43 op_sel:[0,0,1]
	s_waitcnt lgkmcnt(0)
	v_fma_f32 v16, v46, v34, v38
	v_fma_f32 v17, v47, v35, v39
	v_med3_f32 v27, v16, s27, v25
	v_med3_f32 v34, v17, s27, v25
	v_cvt_pk_fp8_f32 v29, v27, v34
	v_fmac_f32_e32 v41, v49, v37
	v_fma_f32 v26, v48, v36, v40
	v_med3_f32 v43, v41, s27, v25
	global_store_dword v[14:15], v28, off offset:512 nt
	v_cvt_pk_bf16_f32 v16, v16, v17
	v_cvt_pk_bf16_f32 v17, v26, v41
	ds_read_b128 v[34:37], v168 offset:4096
	ds_read_b128 v[38:41], v169 offset:4096
	v_med3_f32 v42, v26, s27, v25
	v_cvt_pk_fp8_f32 v29, v42, v43 op_sel:[0,0,1]
	global_store_dwordx2 v[12:13], v[16:17], off offset:1536 nt
	s_waitcnt lgkmcnt(0)
	v_fma_f32 v26, v50, v34, v38
	v_fma_f32 v27, v51, v35, v39
	v_fma_f32 v28, v52, v36, v40
	v_fmac_f32_e32 v41, v53, v37
	global_store_dword v[14:15], v29, off offset:768 nt
	v_cvt_pk_bf16_f32 v16, v26, v27
	v_cvt_pk_bf16_f32 v17, v28, v41
	v_med3_f32 v38, v26, s27, v25
	v_med3_f32 v39, v27, s27, v25
	v_med3_f32 v40, v28, s27, v25
	ds_read_b128 v[26:29], v168 offset:5120
	ds_read_b128 v[34:37], v169 offset:5120
	v_cvt_pk_fp8_f32 v30, v38, v39
	v_med3_f32 v41, v41, s27, v25
	global_store_dwordx2 v[12:13], v[16:17], off offset:2048 nt
	v_cvt_pk_fp8_f32 v30, v40, v41 op_sel:[0,0,1]
	s_waitcnt lgkmcnt(0)
	v_fma_f32 v16, v54, v26, v34
	v_fma_f32 v17, v55, v27, v35
	v_fma_f32 v26, v56, v28, v36
	v_med3_f32 v27, v16, s27, v25
	v_med3_f32 v28, v17, s27, v25
	v_cvt_pk_fp8_f32 v31, v27, v28
	v_fmac_f32_e32 v37, v57, v29
	v_med3_f32 v38, v26, s27, v25
	v_med3_f32 v39, v37, s27, v25
	global_store_dword v[14:15], v30, off offset:1024 nt
	v_cvt_pk_bf16_f32 v16, v16, v17
	v_cvt_pk_bf16_f32 v17, v26, v37
	ds_read_b128 v[26:29], v168 offset:6144
	ds_read_b128 v[34:37], v169 offset:6144
	v_cvt_pk_fp8_f32 v31, v38, v39 op_sel:[0,0,1]
	global_store_dwordx2 v[12:13], v[16:17], off offset:2560 nt
	s_waitcnt lgkmcnt(0)
	v_fma_f32 v26, v58, v26, v34
	v_fma_f32 v27, v59, v27, v35
	v_fma_f32 v28, v60, v28, v36
	v_fmac_f32_e32 v37, v61, v29
	global_store_dword v[14:15], v31, off offset:1280 nt
	v_cvt_pk_bf16_f32 v16, v26, v27
	v_cvt_pk_bf16_f32 v17, v28, v37
	v_med3_f32 v30, v26, s27, v25
	v_med3_f32 v31, v27, s27, v25
	v_med3_f32 v38, v28, s27, v25
	v_med3_f32 v39, v37, s27, v25
	ds_read_b128 v[26:29], v168 offset:7168
	ds_read_b128 v[34:37], v169 offset:7168
	v_cvt_pk_fp8_f32 v32, v30, v31
	global_store_dwordx2 v[12:13], v[16:17], off offset:3072 nt
	s_waitcnt lgkmcnt(0)
	v_fma_f32 v16, v62, v26, v34
	v_fma_f32 v17, v63, v27, v35
	v_fma_f32 v26, v64, v28, v36
	v_med3_f32 v27, v16, s27, v25
	v_med3_f32 v28, v17, s27, v25
	v_cvt_pk_fp8_f32 v33, v27, v28
	v_cvt_pk_fp8_f32 v32, v38, v39 op_sel:[0,0,1]
	v_fmac_f32_e32 v37, v65, v29
	v_med3_f32 v27, v26, s27, v25
	v_med3_f32 v28, v37, s27, v25
	v_cvt_pk_fp8_f32 v33, v27, v28 op_sel:[0,0,1]
	global_store_dword v[14:15], v32, off offset:1536 nt
	v_cvt_pk_bf16_f32 v16, v16, v17
	v_cvt_pk_bf16_f32 v17, v26, v37
	global_store_dwordx2 v[12:13], v[16:17], off offset:3584 nt
	global_store_dword v[14:15], v33, off offset:1792 nt
	s_cbranch_scc0 .LBB0_1411

.LBB0_1414:
	s_waitcnt vmcnt(3)
	v_mul_f32_e32 v4, 0x42800000, v4
	s_waitcnt vmcnt(2)
	v_mul_f32_e32 v8, 0x42800000, v8
	v_med3_f32 v4, v4, s67, v91
	v_med3_f32 v8, v8, s67, v91
	v_mov_b32_e32 v67, v69
	v_cvt_pk_fp8_f32 v67, v4, v8
	s_waitcnt vmcnt(1)
	v_mul_f32_e32 v12, 0x42800000, v12
	s_waitcnt vmcnt(0)
	v_mul_f32_e32 v0, 0x42800000, v0
	v_med3_f32 v4, v12, s67, v91
	v_med3_f32 v0, v0, s67, v91
	v_cvt_pk_fp8_f32 v67, v4, v0 op_sel:[0,0,1]
	v_mul_f32_e32 v0, 0x42800000, v57
	v_mul_f32_e32 v4, 0x42800000, v53
	v_med3_f32 v0, v0, s67, v91
	v_med3_f32 v4, v4, s67, v91
	v_mov_b32_e32 v98, v69
	v_cvt_pk_fp8_f32 v98, v0, v4
	v_mul_f32_e32 v8, 0x42800000, v61
	v_mul_f32_e32 v0, 0x42800000, v45
	v_med3_f32 v4, v8, s67, v91
	v_med3_f32 v0, v0, s67, v91
	v_cvt_pk_fp8_f32 v98, v4, v0 op_sel:[0,0,1]
	v_mul_f32_e32 v0, 0x42800000, v41
	v_mul_f32_e32 v4, 0x42800000, v37
	v_med3_f32 v0, v0, s67, v91
	v_med3_f32 v4, v4, s67, v91
	v_mov_b32_e32 v99, v69
	v_cvt_pk_fp8_f32 v99, v0, v4
	v_mul_f32_e32 v8, 0x42800000, v49
	v_mul_f32_e32 v0, 0x42800000, v33
	v_med3_f32 v4, v8, s67, v91
	v_med3_f32 v0, v0, s67, v91
	v_cvt_pk_fp8_f32 v99, v4, v0 op_sel:[0,0,1]
	v_mul_f32_e32 v0, 0x42800000, v21
	v_mul_f32_e32 v4, 0x42800000, v25
	v_med3_f32 v0, v0, s67, v91
	v_med3_f32 v4, v4, s67, v91
	v_mov_b32_e32 v100, v69
	v_cvt_pk_fp8_f32 v100, v0, v4
	v_mul_f32_e32 v8, 0x42800000, v29
	v_mul_f32_e32 v0, 0x42800000, v17
	v_med3_f32 v4, v8, s67, v91
	v_med3_f32 v0, v0, s67, v91
	v_cvt_pk_fp8_f32 v100, v4, v0 op_sel:[0,0,1]
	v_mul_f32_e32 v0, 0x42800000, v5
	v_mul_f32_e32 v4, 0x42800000, v9
	v_med3_f32 v0, v0, s67, v91
	v_med3_f32 v4, v4, s67, v91
	v_mov_b32_e32 v101, v69
	v_cvt_pk_fp8_f32 v101, v0, v4
	v_mul_f32_e32 v5, 0x42800000, v13
	v_mul_f32_e32 v0, 0x42800000, v1
	v_med3_f32 v1, v5, s67, v91
	v_med3_f32 v0, v0, s67, v91
	v_cvt_pk_fp8_f32 v101, v1, v0 op_sel:[0,0,1]
	v_mul_f32_e32 v0, 0x42800000, v58
	v_mul_f32_e32 v1, 0x42800000, v54
	v_med3_f32 v0, v0, s67, v91
	v_med3_f32 v1, v1, s67, v91
	v_mov_b32_e32 v102, v69
	v_cvt_pk_fp8_f32 v102, v0, v1
	v_mul_f32_e32 v4, 0x42800000, v62
	v_mul_f32_e32 v0, 0x42800000, v46
	v_med3_f32 v1, v4, s67, v91
	v_med3_f32 v0, v0, s67, v91
	v_cvt_pk_fp8_f32 v102, v1, v0 op_sel:[0,0,1]
	v_mul_f32_e32 v0, 0x42800000, v42
	v_mul_f32_e32 v1, 0x42800000, v38
	v_med3_f32 v0, v0, s67, v91
	v_med3_f32 v1, v1, s67, v91
	v_mov_b32_e32 v103, v69
	v_cvt_pk_fp8_f32 v103, v0, v1
	v_mul_f32_e32 v4, 0x42800000, v50
	v_mul_f32_e32 v0, 0x42800000, v34
	v_med3_f32 v1, v4, s67, v91
	v_med3_f32 v0, v0, s67, v91
	v_cvt_pk_fp8_f32 v103, v1, v0 op_sel:[0,0,1]
	v_mul_f32_e32 v0, 0x42800000, v22
	v_mul_f32_e32 v1, 0x42800000, v26
	v_med3_f32 v0, v0, s67, v91
	v_med3_f32 v1, v1, s67, v91
	v_mov_b32_e32 v104, v69
	v_cvt_pk_fp8_f32 v104, v0, v1
	v_mul_f32_e32 v4, 0x42800000, v30
	v_mul_f32_e32 v0, 0x42800000, v18
	v_med3_f32 v1, v4, s67, v91
	v_med3_f32 v0, v0, s67, v91
	v_cvt_pk_fp8_f32 v104, v1, v0 op_sel:[0,0,1]
	v_mul_f32_e32 v0, 0x42800000, v6
	v_mul_f32_e32 v1, 0x42800000, v10
	v_med3_f32 v0, v0, s67, v91
	v_med3_f32 v1, v1, s67, v91
	v_mov_b32_e32 v105, v69
	v_cvt_pk_fp8_f32 v105, v0, v1
	v_mul_f32_e32 v4, 0x42800000, v14
	v_mul_f32_e32 v0, 0x42800000, v2
	v_med3_f32 v1, v4, s67, v91
	v_med3_f32 v0, v0, s67, v91
	v_cvt_pk_fp8_f32 v105, v1, v0 op_sel:[0,0,1]
	v_mul_f32_e32 v0, 0x42800000, v59
	v_mul_f32_e32 v1, 0x42800000, v55
	v_med3_f32 v0, v0, s67, v91
	v_med3_f32 v1, v1, s67, v91
	v_mov_b32_e32 v4, v69
	v_cvt_pk_fp8_f32 v4, v0, v1
	v_mul_f32_e32 v2, 0x42800000, v63
	v_mul_f32_e32 v0, 0x42800000, v47
	v_med3_f32 v1, v2, s67, v91
	v_med3_f32 v0, v0, s67, v91
	v_cvt_pk_fp8_f32 v4, v1, v0 op_sel:[0,0,1]
	v_mul_f32_e32 v0, 0x42800000, v43
	v_mul_f32_e32 v1, 0x42800000, v39
	v_med3_f32 v0, v0, s67, v91
	v_med3_f32 v1, v1, s67, v91
	v_mov_b32_e32 v5, v69
	v_cvt_pk_fp8_f32 v5, v0, v1
	v_mul_f32_e32 v2, 0x42800000, v51
	v_mul_f32_e32 v0, 0x42800000, v35
	v_med3_f32 v1, v2, s67, v91
	v_med3_f32 v0, v0, s67, v91
	v_cvt_pk_fp8_f32 v5, v1, v0 op_sel:[0,0,1]
	v_mul_f32_e32 v0, 0x42800000, v23
	v_mul_f32_e32 v1, 0x42800000, v27
	v_mul_f32_e32 v56, 0x42800000, v56
	v_mul_f32_e32 v52, 0x42800000, v52
	v_med3_f32 v0, v0, s67, v91
	v_med3_f32 v1, v1, s67, v91
	v_mov_b32_e32 v6, v69
	v_med3_f32 v56, v56, s67, v91
	v_med3_f32 v52, v52, s67, v91
	v_mov_b32_e32 v64, v69
	v_cvt_pk_fp8_f32 v6, v0, v1
	v_cvt_pk_fp8_f32 v64, v56, v52
	v_mul_f32_e32 v40, 0x42800000, v40
	v_mul_f32_e32 v36, 0x42800000, v36
	v_mul_f32_e32 v20, 0x42800000, v20
	v_mul_f32_e32 v24, 0x42800000, v24
	v_med3_f32 v40, v40, s67, v91
	v_med3_f32 v36, v36, s67, v91
	v_mov_b32_e32 v65, v69
	v_med3_f32 v20, v20, s67, v91
	v_med3_f32 v24, v24, s67, v91
	v_mov_b32_e32 v66, v69
	v_mul_f32_e32 v2, 0x42800000, v31
	v_mul_f32_e32 v0, 0x42800000, v19
	v_mul_f32_e32 v60, 0x42800000, v60
	v_mul_f32_e32 v44, 0x42800000, v44
	v_cvt_pk_fp8_f32 v65, v40, v36
	v_cvt_pk_fp8_f32 v66, v20, v24
	v_med3_f32 v1, v2, s67, v91
	v_med3_f32 v0, v0, s67, v91
	v_med3_f32 v52, v60, s67, v91
	v_med3_f32 v44, v44, s67, v91
	v_cvt_pk_fp8_f32 v6, v1, v0 op_sel:[0,0,1]
	v_mul_f32_e32 v0, 0x42800000, v7
	v_mul_f32_e32 v1, 0x42800000, v11
	v_cvt_pk_fp8_f32 v64, v52, v44 op_sel:[0,0,1]
	v_mul_f32_e32 v44, 0x42800000, v48
	v_mul_f32_e32 v32, 0x42800000, v32
	v_mul_f32_e32 v28, 0x42800000, v28
	v_mul_f32_e32 v16, 0x42800000, v16
	v_med3_f32 v0, v0, s67, v91
	v_med3_f32 v1, v1, s67, v91
	v_mov_b32_e32 v7, v69
	v_med3_f32 v36, v44, s67, v91
	v_med3_f32 v32, v32, s67, v91
	v_med3_f32 v20, v28, s67, v91
	v_med3_f32 v16, v16, s67, v91
	v_cvt_pk_fp8_f32 v7, v0, v1
	v_cvt_pk_fp8_f32 v65, v36, v32 op_sel:[0,0,1]
	v_cvt_pk_fp8_f32 v66, v20, v16 op_sel:[0,0,1]
	v_mul_f32_e32 v2, 0x42800000, v15
	v_mul_f32_e32 v0, 0x42800000, v3
	v_med3_f32 v1, v2, s67, v91
	v_med3_f32 v0, v0, s67, v91
	v_cvt_pk_fp8_f32 v7, v1, v0 op_sel:[0,0,1]
	s_mul_hi_i32 s7, s6, 0x380000
	s_mul_i32 s6, s6, 0x380000
	ds_write_b128 v88, v[64:67] offset:40960
	ds_write_b128 v88, v[98:101] offset:41040
	ds_write_b128 v88, v[102:105] offset:41120
	ds_write_b128 v88, v[4:7] offset:41200
	s_add_u32 s6, s47, s6
	s_waitcnt lgkmcnt(0)
	s_addc_u32 s7, s48, s7
	s_add_i32 s17, s17, s4
	s_ashr_i32 s4, s24, 31
	ds_read_b128 v[0:3], v89 offset:40960
	s_add_u32 s6, s6, s24
	v_add_u32_e32 v4, s17, v76
	s_addc_u32 s7, s7, s4
	v_ashrrev_i32_e32 v5, 31, v4
	v_lshl_add_u64 v[8:9], s[6:7], 0, v[70:71]
	v_lshlrev_b64 v[4:5], 9, v[4:5]
	v_lshl_add_u64 v[10:11], v[8:9], 0, v[4:5]
	ds_read_b128 v[4:7], v89 offset:42240
	s_waitcnt lgkmcnt(1)
	global_store_dwordx4 v[10:11], v[0:3], off nt
	s_nop 1
	v_add_u32_e32 v0, s17, v77
	v_ashrrev_i32_e32 v1, 31, v0
	v_lshlrev_b64 v[0:1], 9, v[0:1]
	v_lshl_add_u64 v[0:1], v[8:9], 0, v[0:1]
	s_waitcnt lgkmcnt(0)
	global_store_dwordx4 v[0:1], v[4:7], off nt
	ds_read_b128 v[0:3], v89 offset:43520
	s_nop 0
	v_add_u32_e32 v4, s17, v78
	v_ashrrev_i32_e32 v5, 31, v4
	v_lshlrev_b64 v[4:5], 9, v[4:5]
	v_lshl_add_u64 v[10:11], v[8:9], 0, v[4:5]
	ds_read_b128 v[4:7], v89 offset:44800
	s_waitcnt lgkmcnt(1)
	global_store_dwordx4 v[10:11], v[0:3], off nt
	s_nop 1
	v_add_u32_e32 v0, s17, v79
	v_ashrrev_i32_e32 v1, 31, v0
	v_lshlrev_b64 v[0:1], 9, v[0:1]
	v_lshl_add_u64 v[0:1], v[8:9], 0, v[0:1]
	s_waitcnt lgkmcnt(0)
	global_store_dwordx4 v[0:1], v[4:7], off nt
	s_waitcnt lgkmcnt(0)

.LBB0_1416:
	s_add_i32 s4, s57, 0xffff8341
	s_mul_hi_i32 s6, s4, 0x20d56b39
	s_lshr_b32 s7, s6, 31
	s_ashr_i32 s6, s6, 12
	s_add_i32 s6, s6, s7
	s_mul_i32 s7, s6, 0x7cc0
	s_sub_i32 s38, s4, s7
	s_cmpk_gt_i32 s38, 0x1cbf
	s_mov_b64 s[8:9], -1
	s_cbranch_scc0 .LBB0_1422
	s_add_i32 s11, s38, 0xffffe340
	s_and_b32 s10, s11, 0xff
	s_cmpk_gt_u32 s38, 0x5cbf
	s_cbranch_scc0 .LBB0_1419
	v_mov_b32_e32 v0, s58
	s_add_i32 s4, s38, 0xffffa340
	s_ashr_i32 s7, s6, 31
	ds_read_b64 v[0:1], v0
	s_lshr_b32 s4, s4, 8
	s_lshl_b64 s[8:9], s[6:7], 26
	s_add_u32 s12, s3, s8
	s_addc_u32 s13, s40, s9
	s_lshl_b64 s[8:9], s[4:5], 20
	s_add_u32 s8, s12, s8
	s_addc_u32 s9, s13, s9
	s_waitcnt lgkmcnt(0)
	v_readfirstlane_b32 s16, v0
	s_lshl_b64 s[12:13], s[6:7], 27
	v_readfirstlane_b32 s17, v1
	s_add_u32 s7, s16, s12
	s_addc_u32 s17, s17, s13
	s_lshl_b64 s[12:13], s[4:5], 22
	s_add_u32 s16, s7, s12
	s_addc_u32 s17, s17, s13
	s_lshl_b32 s4, s10, 3
	s_and_b32 s7, s4, 0x7c0
	s_lshl_b32 s4, s38, 6
	s_and_b32 s12, s4, 0x1c0
	v_or_b32_e32 v0, s12, v75
	v_lshlrev_b32_e32 v0, 13, v0
	v_mov_b32_e32 v1, v69
	v_lshl_add_u64 v[0:1], s[16:17], 0, v[0:1]
	s_lshl_b32 s4, s7, 2
	v_lshl_add_u64 v[0:1], v[0:1], 0, s[4:5]
	v_mov_b32_e32 v73, v69
	v_lshl_add_u64 v[60:61], v[0:1], 0, v[72:73]
	v_add_co_u32_e32 v4, vcc, s59, v60
	s_mov_b32 s4, 0x8000
	s_nop 0
	v_addc_co_u32_e32 v5, vcc, 0, v61, vcc
	v_add_co_u32_e32 v8, vcc, s60, v60
	global_load_dwordx4 v[0:3], v[60:61], off nt
	s_nop 0
	global_load_dwordx4 v[4:7], v[4:5], off nt
	v_addc_co_u32_e32 v9, vcc, 0, v61, vcc
	v_add_co_u32_e32 v10, vcc, s61, v60
	v_mov_b32_e32 v64, v69
	s_nop 0
	v_addc_co_u32_e32 v11, vcc, 0, v61, vcc
	v_add_co_u32_e32 v16, vcc, s4, v60
	s_mov_b32 s4, 0xa000
	s_nop 0
	v_addc_co_u32_e32 v17, vcc, 0, v61, vcc
	v_add_co_u32_e32 v20, vcc, s4, v60
	s_mov_b32 s4, 0xc000
	s_nop 0
	v_addc_co_u32_e32 v21, vcc, 0, v61, vcc
	v_add_co_u32_e32 v24, vcc, s4, v60
	s_mov_b32 s4, 0xe000
	s_nop 0
	v_addc_co_u32_e32 v25, vcc, 0, v61, vcc
	global_load_dwordx4 v[12:15], v[8:9], off nt
	s_nop 0
	global_load_dwordx4 v[8:11], v[10:11], off nt
	v_add_co_u32_e32 v26, vcc, s4, v60
	s_mov_b32 s4, 0x10000
	s_nop 0
	v_addc_co_u32_e32 v27, vcc, 0, v61, vcc
	global_load_dwordx4 v[16:19], v[16:17], off nt
	s_nop 0
	global_load_dwordx4 v[20:23], v[20:21], off nt
	v_add_co_u32_e32 v28, vcc, s4, v60
	s_mov_b32 s4, 0x14000
	s_nop 0
	v_addc_co_u32_e32 v29, vcc, 0, v61, vcc
	v_add_co_u32_e32 v36, vcc, s62, v60
	global_load_dwordx4 v[32:35], v[24:25], off nt
	s_nop 0
	global_load_dwordx4 v[24:27], v[26:27], off nt
	v_addc_co_u32_e32 v37, vcc, 0, v61, vcc
	v_add_co_u32_e32 v40, vcc, s4, v60
	s_mov_b32 s4, 0x16000
	s_nop 0
	v_addc_co_u32_e32 v41, vcc, 0, v61, vcc
	global_load_dwordx4 v[28:31], v[28:29], off nt
	s_nop 0
	global_load_dwordx4 v[36:39], v[36:37], off nt
	v_add_co_u32_e32 v42, vcc, s4, v60
	v_mov_b32_e32 v65, v69
	s_nop 0
	v_addc_co_u32_e32 v43, vcc, 0, v61, vcc
	v_add_co_u32_e32 v44, vcc, s63, v60
	global_load_dwordx4 v[48:51], v[40:41], off nt
	s_nop 0
	global_load_dwordx4 v[40:43], v[42:43], off nt
	v_addc_co_u32_e32 v45, vcc, 0, v61, vcc
	v_add_co_u32_e32 v52, vcc, s64, v60
	v_mov_b32_e32 v66, v69
	s_nop 0
	v_addc_co_u32_e32 v53, vcc, 0, v61, vcc
	global_load_dwordx4 v[44:47], v[44:45], off nt
	s_nop 0
	global_load_dwordx4 v[52:55], v[52:53], off nt
	v_add_co_u32_e32 v56, vcc, s65, v60
	v_mov_b32_e32 v67, v69
	s_nop 0
	v_addc_co_u32_e32 v57, vcc, 0, v61, vcc
	v_add_co_u32_e32 v60, vcc, s66, v60
	global_load_dwordx4 v[56:59], v[56:57], off nt
	s_nop 0
	v_addc_co_u32_e32 v61, vcc, 0, v61, vcc
	global_load_dwordx4 v[60:63], v[60:61], off nt
	v_mov_b32_e32 v98, v69
	v_mov_b32_e32 v99, v69
	v_mov_b32_e32 v100, v69
	v_mov_b32_e32 v101, v69
	v_mov_b32_e32 v102, v69
	v_mov_b32_e32 v103, v69
	s_waitcnt vmcnt(15)
	v_mul_f32_e32 v0, 0x42000000, v0
	s_waitcnt vmcnt(14)
	v_mul_f32_e32 v4, 0x42000000, v4
	v_med3_f32 v0, v0, s67, v91
	v_med3_f32 v4, v4, s67, v91
	v_cvt_pk_fp8_f32 v64, v0, v4
	v_mov_b32_e32 v104, v69
	v_mov_b32_e32 v105, v69
	s_add_u32 s8, s8, s12
	s_addc_u32 s9, s9, 0
	s_waitcnt vmcnt(13)
	v_mul_f32_e32 v12, 0x42000000, v12
	s_waitcnt vmcnt(12)
	v_mul_f32_e32 v0, 0x42000000, v8
	v_med3_f32 v4, v12, s67, v91
	v_med3_f32 v0, v0, s67, v91
	v_cvt_pk_fp8_f32 v64, v4, v0 op_sel:[0,0,1]
	s_waitcnt vmcnt(11)
	v_mul_f32_e32 v0, 0x42000000, v16
	s_waitcnt vmcnt(10)
	v_mul_f32_e32 v4, 0x42000000, v20
	v_med3_f32 v0, v0, s67, v91
	v_med3_f32 v4, v4, s67, v91
	v_cvt_pk_fp8_f32 v65, v0, v4
	s_waitcnt vmcnt(9)
	v_mul_f32_e32 v8, 0x42000000, v32
	s_waitcnt vmcnt(8)
	v_mul_f32_e32 v0, 0x42000000, v24
	v_med3_f32 v4, v8, s67, v91
	v_med3_f32 v0, v0, s67, v91
	v_cvt_pk_fp8_f32 v65, v4, v0 op_sel:[0,0,1]
	s_waitcnt vmcnt(7)
	v_mul_f32_e32 v0, 0x42000000, v28
	s_waitcnt vmcnt(6)
	v_mul_f32_e32 v4, 0x42000000, v36
	v_med3_f32 v0, v0, s67, v91
	v_med3_f32 v4, v4, s67, v91
	v_cvt_pk_fp8_f32 v66, v0, v4
	s_waitcnt vmcnt(5)
	v_mul_f32_e32 v8, 0x42000000, v48
	s_waitcnt vmcnt(4)
	v_mul_f32_e32 v0, 0x42000000, v40
	v_med3_f32 v4, v8, s67, v91
	v_med3_f32 v0, v0, s67, v91
	v_cvt_pk_fp8_f32 v66, v4, v0 op_sel:[0,0,1]
	s_waitcnt vmcnt(3)
	v_mul_f32_e32 v0, 0x42000000, v44
	s_waitcnt vmcnt(2)
	v_mul_f32_e32 v4, 0x42000000, v52
	v_med3_f32 v0, v0, s67, v91
	v_med3_f32 v4, v4, s67, v91
	v_cvt_pk_fp8_f32 v67, v0, v4
	s_waitcnt vmcnt(1)
	v_mul_f32_e32 v8, 0x42000000, v56
	v_med3_f32 v4, v8, s67, v91
	s_waitcnt vmcnt(0)
	v_mul_f32_e32 v0, 0x42000000, v60
	v_med3_f32 v0, v0, s67, v91
	v_cvt_pk_fp8_f32 v67, v4, v0 op_sel:[0,0,1]
	v_mul_f32_e32 v0, 0x42000000, v1
	v_mul_f32_e32 v1, 0x42000000, v5
	v_med3_f32 v0, v0, s67, v91
	v_med3_f32 v1, v1, s67, v91
	v_cvt_pk_fp8_f32 v98, v0, v1
	v_mul_f32_e32 v4, 0x42000000, v13
	v_mul_f32_e32 v0, 0x42000000, v9
	v_med3_f32 v1, v4, s67, v91
	v_med3_f32 v0, v0, s67, v91
	v_cvt_pk_fp8_f32 v98, v1, v0 op_sel:[0,0,1]
	v_mul_f32_e32 v0, 0x42000000, v17
	v_mul_f32_e32 v1, 0x42000000, v21
	v_med3_f32 v0, v0, s67, v91
	v_med3_f32 v1, v1, s67, v91
	v_cvt_pk_fp8_f32 v99, v0, v1
	v_mul_f32_e32 v4, 0x42000000, v33
	v_mul_f32_e32 v0, 0x42000000, v25
	v_med3_f32 v1, v4, s67, v91
	v_med3_f32 v0, v0, s67, v91
	v_cvt_pk_fp8_f32 v99, v1, v0 op_sel:[0,0,1]
	v_mul_f32_e32 v0, 0x42000000, v29
	v_mul_f32_e32 v1, 0x42000000, v37
	v_med3_f32 v0, v0, s67, v91
	v_med3_f32 v1, v1, s67, v91
	v_cvt_pk_fp8_f32 v100, v0, v1
	v_mul_f32_e32 v4, 0x42000000, v49
	v_mul_f32_e32 v0, 0x42000000, v41
	v_med3_f32 v1, v4, s67, v91
	v_med3_f32 v0, v0, s67, v91
	v_cvt_pk_fp8_f32 v100, v1, v0 op_sel:[0,0,1]
	v_mul_f32_e32 v0, 0x42000000, v45
	v_mul_f32_e32 v1, 0x42000000, v53
	v_med3_f32 v0, v0, s67, v91
	v_med3_f32 v1, v1, s67, v91
	v_cvt_pk_fp8_f32 v101, v0, v1
	v_mul_f32_e32 v4, 0x42000000, v57
	v_mul_f32_e32 v0, 0x42000000, v61
	v_med3_f32 v1, v4, s67, v91
	v_med3_f32 v0, v0, s67, v91
	v_cvt_pk_fp8_f32 v101, v1, v0 op_sel:[0,0,1]
	v_mul_f32_e32 v0, 0x42000000, v2
	v_mul_f32_e32 v1, 0x42000000, v6
	v_med3_f32 v0, v0, s67, v91
	v_med3_f32 v1, v1, s67, v91
	v_cvt_pk_fp8_f32 v102, v0, v1
	v_mul_f32_e32 v2, 0x42000000, v14
	v_mul_f32_e32 v0, 0x42000000, v10
	v_med3_f32 v1, v2, s67, v91
	v_med3_f32 v0, v0, s67, v91
	v_cvt_pk_fp8_f32 v102, v1, v0 op_sel:[0,0,1]
	v_mul_f32_e32 v0, 0x42000000, v18
	v_mul_f32_e32 v1, 0x42000000, v22
	v_med3_f32 v0, v0, s67, v91
	v_med3_f32 v1, v1, s67, v91
	v_cvt_pk_fp8_f32 v103, v0, v1
	v_mul_f32_e32 v2, 0x42000000, v34
	v_mul_f32_e32 v0, 0x42000000, v26
	v_med3_f32 v1, v2, s67, v91
	v_med3_f32 v0, v0, s67, v91
	v_cvt_pk_fp8_f32 v103, v1, v0 op_sel:[0,0,1]
	v_mul_f32_e32 v0, 0x42000000, v30
	v_mul_f32_e32 v1, 0x42000000, v38
	v_med3_f32 v0, v0, s67, v91
	v_med3_f32 v1, v1, s67, v91
	v_cvt_pk_fp8_f32 v104, v0, v1
	v_mul_f32_e32 v2, 0x42000000, v50
	v_mul_f32_e32 v0, 0x42000000, v42
	v_med3_f32 v1, v2, s67, v91
	v_med3_f32 v0, v0, s67, v91
	v_cvt_pk_fp8_f32 v104, v1, v0 op_sel:[0,0,1]
	v_mul_f32_e32 v0, 0x42000000, v46
	v_mul_f32_e32 v1, 0x42000000, v54
	v_med3_f32 v0, v0, s67, v91
	v_med3_f32 v1, v1, s67, v91
	v_cvt_pk_fp8_f32 v105, v0, v1
	v_mul_f32_e32 v2, 0x42000000, v58
	v_mul_f32_e32 v0, 0x42000000, v62
	v_med3_f32 v1, v2, s67, v91
	v_med3_f32 v0, v0, s67, v91
	v_cvt_pk_fp8_f32 v105, v1, v0 op_sel:[0,0,1]
	v_mul_f32_e32 v0, 0x42000000, v3
	v_mul_f32_e32 v1, 0x42000000, v7
	v_med3_f32 v3, v0, s67, v91
	v_med3_f32 v1, v1, s67, v91
	v_mov_b32_e32 v0, v69
	v_cvt_pk_fp8_f32 v0, v3, v1
	v_mul_f32_e32 v2, 0x42000000, v15
	v_mul_f32_e32 v1, 0x42000000, v11
	v_med3_f32 v2, v2, s67, v91
	v_med3_f32 v1, v1, s67, v91
	v_cvt_pk_fp8_f32 v0, v2, v1 op_sel:[0,0,1]
	v_mul_f32_e32 v1, 0x42000000, v19
	v_mul_f32_e32 v2, 0x42000000, v23
	v_med3_f32 v4, v1, s67, v91
	v_med3_f32 v2, v2, s67, v91
	v_mov_b32_e32 v1, v69
	v_cvt_pk_fp8_f32 v1, v4, v2
	v_mul_f32_e32 v3, 0x42000000, v35
	v_mul_f32_e32 v2, 0x42000000, v27
	v_med3_f32 v3, v3, s67, v91
	v_med3_f32 v2, v2, s67, v91
	v_cvt_pk_fp8_f32 v1, v3, v2 op_sel:[0,0,1]
	v_mul_f32_e32 v2, 0x42000000, v31
	v_mul_f32_e32 v3, 0x42000000, v39
	v_med3_f32 v5, v2, s67, v91
	v_med3_f32 v3, v3, s67, v91
	v_mov_b32_e32 v2, v69
	v_cvt_pk_fp8_f32 v2, v5, v3
	v_mul_f32_e32 v4, 0x42000000, v51
	v_mul_f32_e32 v3, 0x42000000, v43
	v_med3_f32 v4, v4, s67, v91
	v_med3_f32 v3, v3, s67, v91
	v_cvt_pk_fp8_f32 v2, v4, v3 op_sel:[0,0,1]
	v_mul_f32_e32 v3, 0x42000000, v47
	v_mul_f32_e32 v4, 0x42000000, v55
	v_med3_f32 v6, v3, s67, v91
	v_med3_f32 v4, v4, s67, v91
	v_mov_b32_e32 v3, v69
	v_cvt_pk_fp8_f32 v3, v6, v4
	v_mul_f32_e32 v5, 0x42000000, v59
	v_mul_f32_e32 v4, 0x42000000, v63
	v_med3_f32 v5, v5, s67, v91
	v_med3_f32 v4, v4, s67, v91
	v_cvt_pk_fp8_f32 v3, v5, v4 op_sel:[0,0,1]
	ds_write_b128 v88, v[64:67] offset:40960
	ds_write_b128 v88, v[98:101] offset:41040
	ds_write_b128 v88, v[102:105] offset:41120
	ds_write_b128 v88, v[0:3] offset:41200
	s_waitcnt lgkmcnt(0)
	ds_read_b128 v[0:3], v89 offset:40960
	v_or_b32_e32 v4, s7, v76
	v_lshl_add_u64 v[8:9], s[8:9], 0, v[70:71]
	v_lshlrev_b32_e32 v4, 9, v4
	v_mov_b32_e32 v5, v69
	v_lshl_add_u64 v[10:11], v[8:9], 0, v[4:5]
	ds_read_b128 v[4:7], v89 offset:42240
	s_waitcnt lgkmcnt(1)
	global_store_dwordx4 v[10:11], v[0:3], off nt
	s_mov_b64 s[8:9], 0
	s_nop 0
	v_or_b32_e32 v0, s7, v77
	v_lshlrev_b32_e32 v0, 9, v0
	v_mov_b32_e32 v1, v69
	v_lshl_add_u64 v[0:1], v[8:9], 0, v[0:1]
	s_waitcnt lgkmcnt(0)
	global_store_dwordx4 v[0:1], v[4:7], off nt
	ds_read_b128 v[0:3], v89 offset:43520
	s_nop 0
	v_or_b32_e32 v4, s7, v78
	v_lshlrev_b32_e32 v4, 9, v4
	v_mov_b32_e32 v5, v69
	v_lshl_add_u64 v[10:11], v[8:9], 0, v[4:5]
	ds_read_b128 v[4:7], v89 offset:44800
	s_waitcnt lgkmcnt(1)
	global_store_dwordx4 v[10:11], v[0:3], off nt
	s_nop 1
	v_or_b32_e32 v0, s7, v79
	v_lshlrev_b32_e32 v0, 9, v0
	v_mov_b32_e32 v1, v69
	v_lshl_add_u64 v[0:1], v[8:9], 0, v[0:1]
	s_waitcnt lgkmcnt(0)
	global_store_dwordx4 v[0:1], v[4:7], off nt
	s_waitcnt lgkmcnt(0)
.LBB0_1419:
	s_andn2_b64 vcc, exec, s[8:9]
	s_cbranch_vccnz .LBB0_1421
	s_ashr_i32 s7, s6, 31
	s_lshr_b32 s4, s11, 9
	s_bfe_u32 s11, s11, 0x10008
	s_lshl_b64 s[12:13], s[6:7], 27
	s_add_u32 s7, s41, s12
	s_addc_u32 s16, s42, s13
	s_lshl_b32 s17, s11, 18
	s_lshl_b64 s[8:9], s[4:5], 21
	s_add_u32 s7, s7, s8
	s_addc_u32 s8, s16, s9
	s_add_u32 s7, s7, s17
	s_addc_u32 s8, s8, 0
	s_lshl_b32 s9, s11, 3
	s_add_i32 s9, s9, 0
	s_add_i32 s9, s9, 0x204e8
	v_mov_b32_e32 v0, s9
	ds_read_b64 v[0:1], v0
	v_mov_b32_e32 v73, v69
	v_mov_b32_e32 v12, v69
	v_mov_b32_e32 v14, v69
	v_mov_b32_e32 v13, v69
	s_waitcnt lgkmcnt(0)
	v_readfirstlane_b32 s9, v0
	v_readfirstlane_b32 s11, v1
	s_add_u32 s9, s9, s12
	s_addc_u32 s11, s11, s13
	s_lshl_b64 s[12:13], s[4:5], 22
	s_add_u32 s12, s9, s12
	s_addc_u32 s13, s11, s13
	s_lshl_b32 s4, s38, 6
	s_and_b32 s9, s4, 0x7c0
	v_or_b32_e32 v0, s9, v75
	v_lshlrev_b32_e32 v0, 11, v0
	v_mov_b32_e32 v1, v69
	s_lshl_b32 s4, s10, 3
	v_lshl_add_u64 v[0:1], s[12:13], 0, v[0:1]
	s_and_b32 s4, s4, 0x700
	v_lshl_add_u64 v[0:1], v[0:1], 0, s[4:5]
	v_lshl_add_u64 v[0:1], v[0:1], 0, v[72:73]
	v_add_co_u32_e32 v2, vcc, s68, v0
	global_load_dwordx4 v[40:43], v[0:1], off nt
	global_load_dwordx4 v[44:47], v[0:1], off offset:2048 nt
	v_addc_co_u32_e32 v3, vcc, 0, v1, vcc
	v_add_co_u32_e32 v4, vcc, s59, v0
	v_mov_b32_e32 v98, v69
	s_nop 0
	v_addc_co_u32_e32 v5, vcc, 0, v1, vcc
	global_load_dwordx4 v[56:59], v[4:5], off offset:-4096 nt
	global_load_dwordx4 v[20:23], v[4:5], off nt
	global_load_dwordx4 v[24:27], v[4:5], off offset:2048 nt
	v_add_co_u32_e32 v4, vcc, s69, v0
	v_mov_b32_e32 v99, v69
	s_nop 0
	v_addc_co_u32_e32 v5, vcc, 0, v1, vcc
	v_add_co_u32_e32 v6, vcc, s60, v0
	v_mov_b32_e32 v100, v69
	s_nop 0
	v_addc_co_u32_e32 v7, vcc, 0, v1, vcc
	global_load_dwordx4 v[64:67], v[2:3], off offset:2048 nt
	global_load_dwordx4 v[36:39], v[4:5], off offset:2048 nt
	global_load_dwordx4 v[60:63], v[6:7], off offset:-4096 nt
	global_load_dwordx4 v[16:19], v[6:7], off nt
	v_add_co_u32_e32 v2, vcc, s70, v0
	v_mov_b32_e32 v101, v69
	s_nop 0
	v_addc_co_u32_e32 v3, vcc, 0, v1, vcc
	v_add_co_u32_e32 v8, vcc, s61, v0
	v_mov_b32_e32 v102, v69
	s_nop 0
	v_addc_co_u32_e32 v9, vcc, 0, v1, vcc
	global_load_dwordx4 v[48:51], v[6:7], off offset:2048 nt
	global_load_dwordx4 v[52:55], v[8:9], off offset:-4096 nt
	global_load_dwordx4 v[28:31], v[2:3], off offset:2048 nt
	s_nop 0
	global_load_dwordx4 v[4:7], v[8:9], off nt
	s_nop 0
	global_load_dwordx4 v[8:11], v[8:9], off offset:2048 nt
	v_add_co_u32_e32 v0, vcc, s71, v0
	v_mov_b32_e32 v103, v69
	s_nop 0
	v_addc_co_u32_e32 v1, vcc, 0, v1, vcc
	global_load_dwordx4 v[32:35], v[0:1], off nt
	s_nop 0
	global_load_dwordx4 v[0:3], v[0:1], off offset:2048 nt
	v_mov_b32_e32 v104, v69
	v_mov_b32_e32 v105, v69
	s_lshl_b32 s4, s10, 1
	s_add_u32 s12, s7, s9
	s_addc_u32 s13, s8, 0
	s_lshl_b32 s7, s10, 2
	s_and_b32 s7, s7, 0x300
	s_and_b32 s4, s4, 64
	s_or_b32 s4, s4, s7
	s_waitcnt vmcnt(15)
	v_mul_f32_e32 v15, 0x42800000, v40
	s_waitcnt vmcnt(14)
	v_mul_f32_e32 v40, 0x42800000, v44
	v_med3_f32 v15, v15, s67, v91
	v_med3_f32 v40, v40, s67, v91
	v_cvt_pk_fp8_f32 v12, v15, v40
	s_waitcnt vmcnt(13)
	v_mul_f32_e32 v44, 0x42800000, v56
	s_waitcnt vmcnt(12)
	v_mul_f32_e32 v20, 0x42800000, v20
	s_waitcnt vmcnt(11)
	v_mul_f32_e32 v24, 0x42800000, v24
	v_med3_f32 v15, v20, s67, v91
	v_med3_f32 v20, v24, s67, v91
	v_cvt_pk_fp8_f32 v13, v15, v20
	v_med3_f32 v44, v44, s67, v91
	s_waitcnt vmcnt(10)
	v_mul_f32_e32 v56, 0x42800000, v64
	s_waitcnt vmcnt(9)
	v_mul_f32_e32 v36, 0x42800000, v36
	s_waitcnt vmcnt(8)
	v_mul_f32_e32 v60, 0x42800000, v60
	s_waitcnt vmcnt(7)
	v_mul_f32_e32 v16, 0x42800000, v16
	v_med3_f32 v16, v16, s67, v91
	v_med3_f32 v56, v56, s67, v91
	v_med3_f32 v24, v60, s67, v91
	v_med3_f32 v36, v36, s67, v91
	v_cvt_pk_fp8_f32 v12, v44, v56 op_sel:[0,0,1]
	v_cvt_pk_fp8_f32 v13, v24, v36 op_sel:[0,0,1]
	s_waitcnt vmcnt(6)
	v_mul_f32_e32 v48, 0x42800000, v48
	v_med3_f32 v40, v48, s67, v91
	v_cvt_pk_fp8_f32 v14, v16, v40
	s_waitcnt vmcnt(5)
	v_mul_f32_e32 v52, 0x42800000, v52
	s_waitcnt vmcnt(4)
	v_mul_f32_e32 v28, 0x42800000, v28
	s_waitcnt vmcnt(3)
	v_mul_f32_e32 v4, 0x42800000, v4
	s_waitcnt vmcnt(2)
	v_mul_f32_e32 v8, 0x42800000, v8
	v_med3_f32 v48, v52, s67, v91
	v_med3_f32 v15, v28, s67, v91
	v_cvt_pk_fp8_f32 v14, v48, v15 op_sel:[0,0,1]
	v_med3_f32 v4, v4, s67, v91
	v_med3_f32 v8, v8, s67, v91
	v_mov_b32_e32 v15, v69
	v_cvt_pk_fp8_f32 v15, v4, v8
	s_waitcnt vmcnt(1)
	v_mul_f32_e32 v16, 0x42800000, v32
	s_waitcnt vmcnt(0)
	v_mul_f32_e32 v0, 0x42800000, v0
	v_med3_f32 v4, v16, s67, v91
	v_med3_f32 v0, v0, s67, v91
	v_cvt_pk_fp8_f32 v15, v4, v0 op_sel:[0,0,1]
	v_mul_f32_e32 v0, 0x42800000, v41
	v_mul_f32_e32 v4, 0x42800000, v45
	v_med3_f32 v0, v0, s67, v91
	v_med3_f32 v4, v4, s67, v91
	v_cvt_pk_fp8_f32 v98, v0, v4
	v_mul_f32_e32 v8, 0x42800000, v57
	v_mul_f32_e32 v0, 0x42800000, v65
	v_med3_f32 v4, v8, s67, v91
	v_med3_f32 v0, v0, s67, v91
	v_cvt_pk_fp8_f32 v98, v4, v0 op_sel:[0,0,1]
	v_mul_f32_e32 v0, 0x42800000, v21
	v_mul_f32_e32 v4, 0x42800000, v25
	v_med3_f32 v0, v0, s67, v91
	v_med3_f32 v4, v4, s67, v91
	v_cvt_pk_fp8_f32 v99, v0, v4
	v_mul_f32_e32 v8, 0x42800000, v61
	v_mul_f32_e32 v0, 0x42800000, v37
	v_med3_f32 v4, v8, s67, v91
	v_med3_f32 v0, v0, s67, v91
	v_cvt_pk_fp8_f32 v99, v4, v0 op_sel:[0,0,1]
	v_mul_f32_e32 v0, 0x42800000, v17
	v_mul_f32_e32 v4, 0x42800000, v49
	v_med3_f32 v0, v0, s67, v91
	v_med3_f32 v4, v4, s67, v91
	v_cvt_pk_fp8_f32 v100, v0, v4
	v_mul_f32_e32 v8, 0x42800000, v53
	v_mul_f32_e32 v0, 0x42800000, v29
	v_med3_f32 v4, v8, s67, v91
	v_med3_f32 v0, v0, s67, v91
	v_cvt_pk_fp8_f32 v100, v4, v0 op_sel:[0,0,1]
	v_mul_f32_e32 v0, 0x42800000, v5
	v_mul_f32_e32 v4, 0x42800000, v9
	v_med3_f32 v0, v0, s67, v91
	v_med3_f32 v4, v4, s67, v91
	v_cvt_pk_fp8_f32 v101, v0, v4
	v_mul_f32_e32 v5, 0x42800000, v33
	v_mul_f32_e32 v0, 0x42800000, v1
	v_med3_f32 v1, v5, s67, v91
	v_med3_f32 v0, v0, s67, v91
	v_cvt_pk_fp8_f32 v101, v1, v0 op_sel:[0,0,1]
	v_mul_f32_e32 v0, 0x42800000, v42
	v_mul_f32_e32 v1, 0x42800000, v46
	v_med3_f32 v0, v0, s67, v91
	v_med3_f32 v1, v1, s67, v91
	v_cvt_pk_fp8_f32 v102, v0, v1
	v_mul_f32_e32 v4, 0x42800000, v58
	v_mul_f32_e32 v0, 0x42800000, v66
	v_med3_f32 v1, v4, s67, v91
	v_med3_f32 v0, v0, s67, v91
	v_cvt_pk_fp8_f32 v102, v1, v0 op_sel:[0,0,1]
	v_mul_f32_e32 v0, 0x42800000, v22
	v_mul_f32_e32 v1, 0x42800000, v26
	v_med3_f32 v0, v0, s67, v91
	v_med3_f32 v1, v1, s67, v91
	v_cvt_pk_fp8_f32 v103, v0, v1
	v_mul_f32_e32 v4, 0x42800000, v62
	v_mul_f32_e32 v0, 0x42800000, v38
	v_med3_f32 v1, v4, s67, v91
	v_med3_f32 v0, v0, s67, v91
	v_cvt_pk_fp8_f32 v103, v1, v0 op_sel:[0,0,1]
	v_mul_f32_e32 v0, 0x42800000, v18
	v_mul_f32_e32 v1, 0x42800000, v50
	v_med3_f32 v0, v0, s67, v91
	v_med3_f32 v1, v1, s67, v91
	v_cvt_pk_fp8_f32 v104, v0, v1
	v_mul_f32_e32 v4, 0x42800000, v54
	v_mul_f32_e32 v0, 0x42800000, v30
	v_med3_f32 v1, v4, s67, v91
	v_med3_f32 v0, v0, s67, v91
	v_cvt_pk_fp8_f32 v104, v1, v0 op_sel:[0,0,1]
	v_mul_f32_e32 v0, 0x42800000, v6
	v_mul_f32_e32 v1, 0x42800000, v10
	v_med3_f32 v0, v0, s67, v91
	v_med3_f32 v1, v1, s67, v91
	v_cvt_pk_fp8_f32 v105, v0, v1
	v_mul_f32_e32 v4, 0x42800000, v34
	v_mul_f32_e32 v0, 0x42800000, v2
	v_med3_f32 v1, v4, s67, v91
	v_med3_f32 v0, v0, s67, v91
	v_cvt_pk_fp8_f32 v105, v1, v0 op_sel:[0,0,1]
	v_mul_f32_e32 v0, 0x42800000, v43
	v_mul_f32_e32 v1, 0x42800000, v47
	v_med3_f32 v0, v0, s67, v91
	v_med3_f32 v1, v1, s67, v91
	v_mov_b32_e32 v4, v69
	v_cvt_pk_fp8_f32 v4, v0, v1
	v_mul_f32_e32 v2, 0x42800000, v59
	v_mul_f32_e32 v0, 0x42800000, v67
	v_med3_f32 v1, v2, s67, v91
	v_med3_f32 v0, v0, s67, v91
	v_cvt_pk_fp8_f32 v4, v1, v0 op_sel:[0,0,1]
	v_mul_f32_e32 v0, 0x42800000, v23
	v_mul_f32_e32 v1, 0x42800000, v27
	v_med3_f32 v0, v0, s67, v91
	v_med3_f32 v1, v1, s67, v91
	v_mov_b32_e32 v5, v69
	v_cvt_pk_fp8_f32 v5, v0, v1
	v_mul_f32_e32 v2, 0x42800000, v63
	v_mul_f32_e32 v0, 0x42800000, v39
	v_med3_f32 v1, v2, s67, v91
	v_med3_f32 v0, v0, s67, v91
	v_cvt_pk_fp8_f32 v5, v1, v0 op_sel:[0,0,1]
	v_mul_f32_e32 v0, 0x42800000, v19
	v_mul_f32_e32 v1, 0x42800000, v51
	v_med3_f32 v0, v0, s67, v91
	v_med3_f32 v1, v1, s67, v91
	v_mov_b32_e32 v6, v69
	v_cvt_pk_fp8_f32 v6, v0, v1
	v_mul_f32_e32 v2, 0x42800000, v55
	v_mul_f32_e32 v0, 0x42800000, v31
	v_med3_f32 v1, v2, s67, v91
	v_med3_f32 v0, v0, s67, v91
	v_cvt_pk_fp8_f32 v6, v1, v0 op_sel:[0,0,1]
	v_mul_f32_e32 v0, 0x42800000, v7
	v_mul_f32_e32 v1, 0x42800000, v11
	v_med3_f32 v0, v0, s67, v91
	v_med3_f32 v1, v1, s67, v91
	v_mov_b32_e32 v7, v69
	v_cvt_pk_fp8_f32 v7, v0, v1
	v_mul_f32_e32 v2, 0x42800000, v35
	v_mul_f32_e32 v0, 0x42800000, v3
	v_med3_f32 v1, v2, s67, v91
	v_med3_f32 v0, v0, s67, v91
	v_cvt_pk_fp8_f32 v7, v1, v0 op_sel:[0,0,1]
	ds_write_b128 v88, v[12:15] offset:40960
	ds_write_b128 v88, v[98:101] offset:41040
	ds_write_b128 v88, v[102:105] offset:41120
	ds_write_b128 v88, v[4:7] offset:41200
	s_waitcnt lgkmcnt(0)
	ds_read_b128 v[0:3], v89 offset:40960
	v_or_b32_e32 v4, s4, v76
	v_lshl_add_u64 v[8:9], s[12:13], 0, v[70:71]
	v_lshlrev_b32_e32 v4, 11, v4
	v_mov_b32_e32 v5, v69
	v_lshl_add_u64 v[10:11], v[8:9], 0, v[4:5]
	ds_read_b128 v[4:7], v89 offset:42240
	s_waitcnt lgkmcnt(1)
	global_store_dwordx4 v[10:11], v[0:3], off nt
	s_nop 1
	v_or_b32_e32 v0, s4, v77
	v_lshlrev_b32_e32 v0, 11, v0
	v_mov_b32_e32 v1, v69
	v_lshl_add_u64 v[0:1], v[8:9], 0, v[0:1]
	s_waitcnt lgkmcnt(0)
	global_store_dwordx4 v[0:1], v[4:7], off nt
	ds_read_b128 v[0:3], v89 offset:43520
	s_nop 0
	v_or_b32_e32 v4, s4, v78
	v_lshlrev_b32_e32 v4, 11, v4
	v_mov_b32_e32 v5, v69
	v_lshl_add_u64 v[10:11], v[8:9], 0, v[4:5]
	ds_read_b128 v[4:7], v89 offset:44800
	s_waitcnt lgkmcnt(1)
	global_store_dwordx4 v[10:11], v[0:3], off nt
	s_nop 1
	v_or_b32_e32 v0, s4, v79
	v_lshlrev_b32_e32 v0, 11, v0
	v_mov_b32_e32 v1, v69
	v_lshl_add_u64 v[0:1], v[8:9], 0, v[0:1]
	s_waitcnt lgkmcnt(0)
	global_store_dwordx4 v[0:1], v[4:7], off nt
	s_waitcnt lgkmcnt(0)

.LBB0_1451:
	s_cmpk_gt_i32 s94, 0x93
	s_cbranch_scc1 .LBB0_1453
	s_lshl_b32 s30, s7, 6
	s_mul_i32 s31, s6, 0x1280000
	v_or_b32_e32 v0, s30, v75
	s_mul_hi_i32 s23, s6, 0x1280000
	s_add_u32 s31, s51, s31
	v_mul_hi_i32_i24_e32 v1, 0x9500, v0
	v_mul_i32_i24_e32 v0, 0x9500, v0
	s_addc_u32 s38, s52, s23
	v_lshl_add_u64 v[0:1], s[8:9], 0, v[0:1]
	s_ashr_i32 s23, s22, 31
	v_lshl_add_u64 v[0:1], s[22:23], 2, v[0:1]
	v_mov_b32_e32 v73, v69
	v_lshl_add_u64 v[56:57], v[0:1], 0, v[72:73]
	v_add_co_u32_e32 v4, vcc, s79, v56
	global_load_dwordx4 v[0:3], v[56:57], off nt
	s_nop 0
	v_addc_co_u32_e32 v5, vcc, 0, v57, vcc
	global_load_dwordx4 v[16:19], v[4:5], off offset:1280 nt
	v_add_co_u32_e32 v4, vcc, s62, v56
	v_mov_b32_e32 v64, v69
	s_nop 0
	v_addc_co_u32_e32 v5, vcc, 0, v57, vcc
	global_load_dwordx4 v[20:23], v[4:5], off offset:2560 nt
	v_add_co_u32_e32 v4, vcc, s80, v56
	v_mov_b32_e32 v65, v69
	s_nop 0
	v_addc_co_u32_e32 v5, vcc, 0, v57, vcc
	global_load_dwordx4 v[44:47], v[4:5], off offset:3840 nt
	v_add_co_u32_e32 v4, vcc, s81, v56
	v_mov_b32_e32 v66, v69
	s_nop 0
	v_addc_co_u32_e32 v5, vcc, 0, v57, vcc
	v_add_co_u32_e32 v8, vcc, s82, v56
	global_load_dwordx4 v[4:7], v[4:5], off offset:1024 nt
	s_nop 0
	v_addc_co_u32_e32 v9, vcc, 0, v57, vcc
	global_load_dwordx4 v[24:27], v[8:9], off offset:2304 nt
	v_add_co_u32_e32 v8, vcc, s83, v56
	v_mov_b32_e32 v67, v69
	s_nop 0
	v_addc_co_u32_e32 v9, vcc, 0, v57, vcc
	global_load_dwordx4 v[28:31], v[8:9], off offset:3584 nt
	v_add_co_u32_e32 v8, vcc, s84, v56
	s_ashr_i32 s23, s30, 31
	s_nop 0
	v_addc_co_u32_e32 v9, vcc, 0, v57, vcc
	global_load_dwordx4 v[52:55], v[8:9], off offset:768 nt
	v_add_co_u32_e32 v8, vcc, s85, v56
	s_add_u32 s30, s31, s30
	s_nop 0
	v_addc_co_u32_e32 v9, vcc, 0, v57, vcc
	v_add_co_u32_e32 v12, vcc, s86, v56
	global_load_dwordx4 v[8:11], v[8:9], off offset:2048 nt
	s_nop 0
	v_addc_co_u32_e32 v13, vcc, 0, v57, vcc
	global_load_dwordx4 v[32:35], v[12:13], off offset:3328 nt
	v_add_co_u32_e32 v12, vcc, s87, v56
	s_addc_u32 s31, s38, s23
	s_nop 0
	v_addc_co_u32_e32 v13, vcc, 0, v57, vcc
	global_load_dwordx4 v[36:39], v[12:13], off offset:512 nt
	v_add_co_u32_e32 v12, vcc, s88, v56
	s_mov_b64 s[38:39], 0
	s_nop 0
	v_addc_co_u32_e32 v13, vcc, 0, v57, vcc
	global_load_dwordx4 v[60:63], v[12:13], off offset:1792 nt
	v_add_co_u32_e32 v12, vcc, s89, v56
	s_waitcnt vmcnt(11)
	v_mul_f32_e32 v0, 0x42800000, v0
	v_addc_co_u32_e32 v13, vcc, 0, v57, vcc
	v_add_co_u32_e32 v40, vcc, s90, v56
	global_load_dwordx4 v[12:15], v[12:13], off offset:3072 nt
	s_nop 0
	v_addc_co_u32_e32 v41, vcc, 0, v57, vcc
	global_load_dwordx4 v[40:43], v[40:41], off offset:256 nt
	v_add_co_u32_e32 v48, vcc, s91, v56
	s_waitcnt vmcnt(12)
	v_mul_f32_e32 v16, 0x42800000, v16
	v_addc_co_u32_e32 v49, vcc, 0, v57, vcc
	v_add_co_u32_e32 v56, vcc, s92, v56
	global_load_dwordx4 v[48:51], v[48:49], off offset:1536 nt
	s_nop 0
	v_addc_co_u32_e32 v57, vcc, 0, v57, vcc
	global_load_dwordx4 v[56:59], v[56:57], off offset:2816 nt
	v_med3_f32 v0, v0, s67, v91
	v_med3_f32 v16, v16, s67, v91
	v_cvt_pk_fp8_f32 v64, v0, v16
	s_waitcnt vmcnt(11)
	v_mul_f32_e32 v0, 0x42800000, v4
	v_med3_f32 v0, v0, s67, v91
	v_mul_f32_e32 v20, 0x42800000, v20
	s_waitcnt vmcnt(10)
	v_mul_f32_e32 v4, 0x42800000, v24
	v_med3_f32 v4, v4, s67, v91
	v_mul_f32_e32 v44, 0x42800000, v44
	v_cvt_pk_fp8_f32 v65, v0, v4
	v_med3_f32 v20, v20, s67, v91
	v_med3_f32 v44, v44, s67, v91
	v_cvt_pk_fp8_f32 v64, v20, v44 op_sel:[0,0,1]
	s_waitcnt vmcnt(9)
	v_mul_f32_e32 v16, 0x42800000, v28
	v_med3_f32 v16, v16, s67, v91
	s_waitcnt vmcnt(8)
	v_mul_f32_e32 v20, 0x42800000, v52
	v_med3_f32 v20, v20, s67, v91
	v_cvt_pk_fp8_f32 v65, v16, v20 op_sel:[0,0,1]
	s_waitcnt vmcnt(7)
	v_mul_f32_e32 v0, 0x42800000, v8
	v_med3_f32 v0, v0, s67, v91
	s_waitcnt vmcnt(6)
	v_mul_f32_e32 v4, 0x42800000, v32
	v_med3_f32 v4, v4, s67, v91
	v_cvt_pk_fp8_f32 v66, v0, v4
	s_waitcnt vmcnt(5)
	v_mul_f32_e32 v8, 0x42800000, v36
	v_med3_f32 v8, v8, s67, v91
	s_waitcnt vmcnt(4)
	v_mul_f32_e32 v16, 0x42800000, v60
	v_med3_f32 v16, v16, s67, v91
	v_cvt_pk_fp8_f32 v66, v8, v16 op_sel:[0,0,1]
	s_waitcnt vmcnt(3)
	v_mul_f32_e32 v0, 0x42800000, v12
	v_med3_f32 v0, v0, s67, v91
	s_waitcnt vmcnt(2)
	v_mul_f32_e32 v4, 0x42800000, v40
	v_med3_f32 v4, v4, s67, v91
	v_cvt_pk_fp8_f32 v67, v0, v4
	v_mul_f32_e32 v0, 0x42800000, v1
	v_mul_f32_e32 v1, 0x42800000, v17
	v_med3_f32 v0, v0, s67, v91
	v_med3_f32 v1, v1, s67, v91
	v_mul_f32_e32 v4, 0x42800000, v21
	s_waitcnt vmcnt(1)
	v_mul_f32_e32 v8, 0x42800000, v48
	v_med3_f32 v8, v8, s67, v91
	v_med3_f32 v4, v4, s67, v91
	s_waitcnt vmcnt(0)
	v_mul_f32_e32 v12, 0x42800000, v56
	v_med3_f32 v12, v12, s67, v91
	v_cvt_pk_fp8_f32 v67, v8, v12 op_sel:[0,0,1]
	v_mul_f32_e32 v8, 0x42800000, v45
	v_med3_f32 v8, v8, s67, v91
	ds_write_b128 v88, v[64:67] offset:40960
	v_mov_b32_e32 v64, v69
	v_cvt_pk_fp8_f32 v64, v0, v1
	v_mul_f32_e32 v0, 0x42800000, v5
	v_mul_f32_e32 v1, 0x42800000, v25
	v_med3_f32 v0, v0, s67, v91
	v_med3_f32 v1, v1, s67, v91
	v_mov_b32_e32 v65, v69
	v_cvt_pk_fp8_f32 v65, v0, v1
	v_mul_f32_e32 v0, 0x42800000, v9
	v_mul_f32_e32 v1, 0x42800000, v33
	v_med3_f32 v0, v0, s67, v91
	v_med3_f32 v1, v1, s67, v91
	v_mov_b32_e32 v66, v69
	v_cvt_pk_fp8_f32 v64, v4, v8 op_sel:[0,0,1]
	v_mul_f32_e32 v4, 0x42800000, v29
	v_mul_f32_e32 v5, 0x42800000, v53
	v_cvt_pk_fp8_f32 v66, v0, v1
	v_mul_f32_e32 v0, 0x42800000, v13
	v_mul_f32_e32 v1, 0x42800000, v41
	v_med3_f32 v4, v4, s67, v91
	v_med3_f32 v5, v5, s67, v91
	v_med3_f32 v0, v0, s67, v91
	v_med3_f32 v1, v1, s67, v91
	v_mov_b32_e32 v67, v69
	v_cvt_pk_fp8_f32 v65, v4, v5 op_sel:[0,0,1]
	v_mul_f32_e32 v4, 0x42800000, v37
	v_mul_f32_e32 v5, 0x42800000, v61
	v_cvt_pk_fp8_f32 v67, v0, v1
	v_med3_f32 v4, v4, s67, v91
	v_med3_f32 v5, v5, s67, v91
	v_cvt_pk_fp8_f32 v66, v4, v5 op_sel:[0,0,1]
	v_mul_f32_e32 v4, 0x42800000, v49
	v_mul_f32_e32 v5, 0x42800000, v57
	v_med3_f32 v4, v4, s67, v91
	v_med3_f32 v5, v5, s67, v91
	v_cvt_pk_fp8_f32 v67, v4, v5 op_sel:[0,0,1]
	v_mul_f32_e32 v0, 0x42800000, v2
	v_mul_f32_e32 v1, 0x42800000, v18
	v_med3_f32 v0, v0, s67, v91
	ds_write_b128 v88, v[64:67] offset:41040
	v_med3_f32 v1, v1, s67, v91
	v_mov_b32_e32 v64, v69
	v_cvt_pk_fp8_f32 v64, v0, v1
	v_mul_f32_e32 v0, 0x42800000, v6
	v_mul_f32_e32 v1, 0x42800000, v26
	v_med3_f32 v0, v0, s67, v91
	v_med3_f32 v1, v1, s67, v91
	v_mov_b32_e32 v65, v69
	v_mul_f32_e32 v2, 0x42800000, v22
	v_mul_f32_e32 v4, 0x42800000, v46
	v_cvt_pk_fp8_f32 v65, v0, v1
	v_mul_f32_e32 v0, 0x42800000, v10
	v_mul_f32_e32 v1, 0x42800000, v34
	v_med3_f32 v2, v2, s67, v91
	v_med3_f32 v4, v4, s67, v91
	v_med3_f32 v0, v0, s67, v91
	v_med3_f32 v1, v1, s67, v91
	v_mov_b32_e32 v66, v69
	v_cvt_pk_fp8_f32 v64, v2, v4 op_sel:[0,0,1]
	v_mul_f32_e32 v2, 0x42800000, v30
	v_mul_f32_e32 v4, 0x42800000, v54
	v_cvt_pk_fp8_f32 v66, v0, v1
	v_mul_f32_e32 v0, 0x42800000, v14
	v_mul_f32_e32 v1, 0x42800000, v42
	v_med3_f32 v2, v2, s67, v91
	v_med3_f32 v4, v4, s67, v91
	v_med3_f32 v0, v0, s67, v91
	v_med3_f32 v1, v1, s67, v91
	v_mov_b32_e32 v67, v69
	v_cvt_pk_fp8_f32 v65, v2, v4 op_sel:[0,0,1]
	v_mul_f32_e32 v2, 0x42800000, v38
	v_mul_f32_e32 v4, 0x42800000, v62
	v_cvt_pk_fp8_f32 v67, v0, v1
	v_med3_f32 v2, v2, s67, v91
	v_med3_f32 v4, v4, s67, v91
	v_cvt_pk_fp8_f32 v66, v2, v4 op_sel:[0,0,1]
	v_mul_f32_e32 v2, 0x42800000, v50
	v_mul_f32_e32 v4, 0x42800000, v58
	v_med3_f32 v2, v2, s67, v91
	v_med3_f32 v4, v4, s67, v91
	v_mul_f32_e32 v0, 0x42800000, v3
	v_mul_f32_e32 v1, 0x42800000, v19
	v_cvt_pk_fp8_f32 v67, v2, v4 op_sel:[0,0,1]
	v_med3_f32 v4, v0, s67, v91
	v_med3_f32 v1, v1, s67, v91
	v_mov_b32_e32 v0, v69
	v_cvt_pk_fp8_f32 v0, v4, v1
	v_mul_f32_e32 v2, 0x42800000, v23
	v_mul_f32_e32 v3, 0x42800000, v47
	v_med3_f32 v2, v2, s67, v91
	v_med3_f32 v3, v3, s67, v91
	v_cvt_pk_fp8_f32 v0, v2, v3 op_sel:[0,0,1]
	v_mul_f32_e32 v1, 0x42800000, v7
	v_mul_f32_e32 v2, 0x42800000, v27
	v_med3_f32 v5, v1, s67, v91
	v_med3_f32 v2, v2, s67, v91
	v_mov_b32_e32 v1, v69
	v_cvt_pk_fp8_f32 v1, v5, v2
	v_mul_f32_e32 v3, 0x42800000, v31
	v_mul_f32_e32 v4, 0x42800000, v55
	v_med3_f32 v3, v3, s67, v91
	v_med3_f32 v4, v4, s67, v91
	v_cvt_pk_fp8_f32 v1, v3, v4 op_sel:[0,0,1]
	v_mul_f32_e32 v2, 0x42800000, v11
	v_mul_f32_e32 v3, 0x42800000, v35
	v_med3_f32 v6, v2, s67, v91
	v_med3_f32 v3, v3, s67, v91
	v_mov_b32_e32 v2, v69
	v_cvt_pk_fp8_f32 v2, v6, v3
	v_mul_f32_e32 v4, 0x42800000, v39
	v_mul_f32_e32 v5, 0x42800000, v63
	v_med3_f32 v4, v4, s67, v91
	v_med3_f32 v5, v5, s67, v91
	v_cvt_pk_fp8_f32 v2, v4, v5 op_sel:[0,0,1]
	v_mul_f32_e32 v3, 0x42800000, v15
	v_mul_f32_e32 v4, 0x42800000, v43
	v_med3_f32 v7, v3, s67, v91
	v_med3_f32 v4, v4, s67, v91
	v_mov_b32_e32 v3, v69
	v_cvt_pk_fp8_f32 v3, v7, v4
	v_mul_f32_e32 v5, 0x42800000, v51
	v_mul_f32_e32 v6, 0x42800000, v59
	v_med3_f32 v5, v5, s67, v91
	v_med3_f32 v6, v6, s67, v91
	v_cvt_pk_fp8_f32 v3, v5, v6 op_sel:[0,0,1]
	ds_write_b128 v88, v[64:67] offset:41120
	v_or_b32_e32 v6, s17, v76
	v_ashrrev_i32_e32 v7, 31, v6
	ds_write_b128 v88, v[0:3] offset:41200
	s_waitcnt lgkmcnt(0)
	ds_read_b128 v[0:3], v89 offset:40960
	v_lshl_add_u64 v[4:5], s[30:31], 0, v[70:71]
	v_lshlrev_b64 v[6:7], 11, v[6:7]
	v_lshl_add_u64 v[6:7], v[4:5], 0, v[6:7]
	s_waitcnt lgkmcnt(0)
	global_store_dwordx4 v[6:7], v[0:3], off nt
	ds_read_b128 v[0:3], v89 offset:42240
	v_or_b32_e32 v6, s17, v77
	v_ashrrev_i32_e32 v7, 31, v6
	v_lshlrev_b64 v[6:7], 11, v[6:7]
	v_lshl_add_u64 v[6:7], v[4:5], 0, v[6:7]
	s_waitcnt lgkmcnt(0)
	global_store_dwordx4 v[6:7], v[0:3], off nt
	ds_read_b128 v[0:3], v89 offset:43520
	v_or_b32_e32 v6, s17, v78
	v_ashrrev_i32_e32 v7, 31, v6
	v_lshlrev_b64 v[6:7], 11, v[6:7]
	v_lshl_add_u64 v[6:7], v[4:5], 0, v[6:7]
	s_waitcnt lgkmcnt(0)
	global_store_dwordx4 v[6:7], v[0:3], off nt
	ds_read_b128 v[0:3], v89 offset:44800
	v_or_b32_e32 v6, s17, v79
	v_ashrrev_i32_e32 v7, 31, v6
	v_lshlrev_b64 v[6:7], 11, v[6:7]
	v_lshl_add_u64 v[4:5], v[4:5], 0, v[6:7]
	s_waitcnt lgkmcnt(0)
	global_store_dwordx4 v[4:5], v[0:3], off nt
	s_waitcnt lgkmcnt(0)
.LBB0_1453:
	s_and_b64 vcc, exec, s[38:39]
	s_cbranch_vccz .LBB0_1415
	s_xor_b64 s[38:39], s[24:25], -1
	s_lshl_b32 s24, s7, 6
	s_mov_b64 s[30:31], -1
	s_and_b64 vcc, exec, s[38:39]
	s_cbranch_vccz .LBB0_1484
	s_andn2_b64 vcc, exec, s[28:29]
	s_cbranch_vccnz .LBB0_1458
	s_ashr_i32 s7, s6, 31
	s_lshl_b64 s[28:29], s[6:7], 22
	v_or_b32_e32 v0, s24, v75
	s_add_u32 s7, s53, s28
	v_mul_hi_i32_i24_e32 v1, s18, v0
	v_mul_i32_i24_e32 v0, s18, v0
	s_addc_u32 s25, s54, s29
	v_lshl_add_u64 v[0:1], v[0:1], 2, s[8:9]
	s_ashr_i32 s23, s22, 31
	v_lshl_add_u64 v[0:1], s[22:23], 2, v[0:1]
	v_mov_b32_e32 v73, v69
	v_lshl_add_u64 v[0:1], v[0:1], 0, v[72:73]
	s_lshl_b64 s[28:29], s[18:19], 2
	global_load_dwordx4 v[56:59], v[0:1], off nt
	v_lshl_add_u64 v[0:1], v[0:1], 0, s[28:29]
	global_load_dwordx4 v[60:63], v[0:1], off nt
	v_lshl_add_u64 v[0:1], v[0:1], 0, s[28:29]
	global_load_dwordx4 v[64:67], v[0:1], off nt
	v_lshl_add_u64 v[0:1], v[0:1], 0, s[28:29]
	global_load_dwordx4 v[52:55], v[0:1], off nt
	v_lshl_add_u64 v[0:1], v[0:1], 0, s[28:29]
	global_load_dwordx4 v[40:43], v[0:1], off nt
	v_lshl_add_u64 v[0:1], v[0:1], 0, s[28:29]
	global_load_dwordx4 v[44:47], v[0:1], off nt
	v_lshl_add_u64 v[0:1], v[0:1], 0, s[28:29]
	global_load_dwordx4 v[48:51], v[0:1], off nt
	v_lshl_add_u64 v[0:1], v[0:1], 0, s[28:29]
	global_load_dwordx4 v[36:39], v[0:1], off nt
	v_lshl_add_u64 v[0:1], v[0:1], 0, s[28:29]
	global_load_dwordx4 v[24:27], v[0:1], off nt
	v_lshl_add_u64 v[0:1], v[0:1], 0, s[28:29]
	global_load_dwordx4 v[28:31], v[0:1], off nt
	v_lshl_add_u64 v[0:1], v[0:1], 0, s[28:29]
	global_load_dwordx4 v[32:35], v[0:1], off nt
	v_lshl_add_u64 v[0:1], v[0:1], 0, s[28:29]
	global_load_dwordx4 v[20:23], v[0:1], off nt
	v_lshl_add_u64 v[0:1], v[0:1], 0, s[28:29]
	global_load_dwordx4 v[4:7], v[0:1], off nt
	v_lshl_add_u64 v[0:1], v[0:1], 0, s[28:29]
	global_load_dwordx4 v[12:15], v[0:1], off nt
	v_lshl_add_u64 v[0:1], v[0:1], 0, s[28:29]
	global_load_dwordx4 v[16:19], v[0:1], off nt
	v_lshl_add_u64 v[0:1], v[0:1], 0, s[28:29]
	global_load_dwordx4 v[0:3], v[0:1], off nt
	v_mov_b32_e32 v11, v69
	v_mov_b32_e32 v99, v69
	v_mov_b32_e32 v100, v69
	v_mov_b32_e32 v101, v69
	v_mov_b32_e32 v102, v69
	v_mov_b32_e32 v103, v69
	v_mov_b32_e32 v104, v69
	v_mov_b32_e32 v105, v69
	v_mov_b32_e32 v8, v69
	v_mov_b32_e32 v9, v69
	v_mov_b32_e32 v10, v69
	v_mov_b32_e32 v98, v69
	s_ashr_i32 s23, s24, 31
	s_add_u32 s28, s7, s24
	s_addc_u32 s29, s25, s23
	s_cmpk_lt_u32 s57, 0xf97f
	s_waitcnt vmcnt(15)
	v_mul_f32_e32 v56, 0x42800000, v56
	v_mul_f32_e32 v57, 0x42800000, v57
	s_waitcnt vmcnt(14)
	v_mul_f32_e32 v60, 0x42800000, v60
	v_med3_f32 v56, v56, s67, v91
	v_mul_f32_e32 v61, 0x42800000, v61
	v_med3_f32 v60, v60, s67, v91
	v_med3_f32 v57, v57, s67, v91
	v_med3_f32 v61, v61, s67, v91
	s_waitcnt vmcnt(11)
	v_mul_f32_e32 v41, 0x42800000, v41
	v_med3_f32 v41, v41, s67, v91
	s_waitcnt vmcnt(10)
	v_mul_f32_e32 v45, 0x42800000, v45
	v_med3_f32 v45, v45, s67, v91
	v_cvt_pk_fp8_f32 v99, v41, v45
	s_waitcnt vmcnt(9)
	v_mul_f32_e32 v49, 0x42800000, v49
	v_mul_f32_e32 v40, 0x42800000, v40
	v_mul_f32_e32 v44, 0x42800000, v44
	s_waitcnt vmcnt(7)
	v_mul_f32_e32 v24, 0x42800000, v24
	v_med3_f32 v40, v40, s67, v91
	s_waitcnt vmcnt(6)
	v_mul_f32_e32 v28, 0x42800000, v28
	v_med3_f32 v44, v44, s67, v91
	v_med3_f32 v24, v24, s67, v91
	v_med3_f32 v28, v28, s67, v91
	v_cvt_pk_fp8_f32 v8, v56, v60
	v_cvt_pk_fp8_f32 v9, v40, v44
	s_waitcnt vmcnt(3)
	v_mul_f32_e32 v4, 0x42800000, v4
	v_med3_f32 v4, v4, s67, v91
	s_waitcnt vmcnt(2)
	v_mul_f32_e32 v12, 0x42800000, v12
	v_med3_f32 v12, v12, s67, v91
	v_cvt_pk_fp8_f32 v11, v4, v12
	s_waitcnt vmcnt(1)
	v_mul_f32_e32 v16, 0x42800000, v16
	s_waitcnt vmcnt(0)
	v_mul_f32_e32 v0, 0x42800000, v0
	v_med3_f32 v4, v16, s67, v91
	v_med3_f32 v0, v0, s67, v91
	v_cvt_pk_fp8_f32 v11, v4, v0 op_sel:[0,0,1]
	v_mul_f32_e32 v0, 0x42800000, v37
	v_med3_f32 v4, v49, s67, v91
	v_med3_f32 v0, v0, s67, v91
	v_cvt_pk_fp8_f32 v99, v4, v0 op_sel:[0,0,1]
	v_mul_f32_e32 v0, 0x42800000, v25
	v_mul_f32_e32 v4, 0x42800000, v29
	v_med3_f32 v0, v0, s67, v91
	v_med3_f32 v4, v4, s67, v91
	v_cvt_pk_fp8_f32 v100, v0, v4
	v_mul_f32_e32 v12, 0x42800000, v33
	v_mul_f32_e32 v0, 0x42800000, v21
	v_med3_f32 v4, v12, s67, v91
	v_med3_f32 v0, v0, s67, v91
	v_cvt_pk_fp8_f32 v100, v4, v0 op_sel:[0,0,1]
	v_mul_f32_e32 v0, 0x42800000, v5
	v_mul_f32_e32 v4, 0x42800000, v13
	v_med3_f32 v0, v0, s67, v91
	v_med3_f32 v4, v4, s67, v91
	v_cvt_pk_fp8_f32 v101, v0, v4
	v_mul_f32_e32 v5, 0x42800000, v17
	v_mul_f32_e32 v0, 0x42800000, v1
	v_med3_f32 v1, v5, s67, v91
	v_med3_f32 v0, v0, s67, v91
	v_cvt_pk_fp8_f32 v101, v1, v0 op_sel:[0,0,1]
	v_mul_f32_e32 v0, 0x42800000, v58
	v_mul_f32_e32 v1, 0x42800000, v62
	v_med3_f32 v0, v0, s67, v91
	v_med3_f32 v1, v1, s67, v91
	v_cvt_pk_fp8_f32 v102, v0, v1
	v_mul_f32_e32 v4, 0x42800000, v66
	v_mul_f32_e32 v0, 0x42800000, v54
	v_med3_f32 v1, v4, s67, v91
	v_med3_f32 v0, v0, s67, v91
	v_cvt_pk_fp8_f32 v102, v1, v0 op_sel:[0,0,1]
	v_mul_f32_e32 v0, 0x42800000, v42
	v_mul_f32_e32 v1, 0x42800000, v46
	v_med3_f32 v0, v0, s67, v91
	v_med3_f32 v1, v1, s67, v91
	v_cvt_pk_fp8_f32 v103, v0, v1
	v_mul_f32_e32 v4, 0x42800000, v50
	v_mul_f32_e32 v0, 0x42800000, v38
	v_med3_f32 v1, v4, s67, v91
	v_med3_f32 v0, v0, s67, v91
	v_cvt_pk_fp8_f32 v103, v1, v0 op_sel:[0,0,1]
	v_mul_f32_e32 v0, 0x42800000, v26
	v_mul_f32_e32 v1, 0x42800000, v30
	v_med3_f32 v0, v0, s67, v91
	v_med3_f32 v1, v1, s67, v91
	v_cvt_pk_fp8_f32 v104, v0, v1
	v_mul_f32_e32 v4, 0x42800000, v34
	v_mul_f32_e32 v0, 0x42800000, v22
	v_med3_f32 v1, v4, s67, v91
	v_med3_f32 v0, v0, s67, v91
	v_cvt_pk_fp8_f32 v104, v1, v0 op_sel:[0,0,1]
	v_mul_f32_e32 v0, 0x42800000, v6
	v_mul_f32_e32 v1, 0x42800000, v14
	v_med3_f32 v0, v0, s67, v91
	v_med3_f32 v1, v1, s67, v91
	v_cvt_pk_fp8_f32 v105, v0, v1
	v_mul_f32_e32 v4, 0x42800000, v18
	v_mul_f32_e32 v0, 0x42800000, v2
	v_med3_f32 v1, v4, s67, v91
	v_med3_f32 v0, v0, s67, v91
	v_cvt_pk_fp8_f32 v105, v1, v0 op_sel:[0,0,1]
	v_mul_f32_e32 v0, 0x42800000, v59
	v_mul_f32_e32 v1, 0x42800000, v63
	v_med3_f32 v0, v0, s67, v91
	v_med3_f32 v1, v1, s67, v91
	v_mov_b32_e32 v4, v69
	v_cvt_pk_fp8_f32 v4, v0, v1
	v_mul_f32_e32 v2, 0x42800000, v67
	v_mul_f32_e32 v0, 0x42800000, v55
	v_med3_f32 v1, v2, s67, v91
	v_med3_f32 v0, v0, s67, v91
	v_cvt_pk_fp8_f32 v4, v1, v0 op_sel:[0,0,1]
	v_mul_f32_e32 v0, 0x42800000, v43
	v_mul_f32_e32 v1, 0x42800000, v47
	v_med3_f32 v0, v0, s67, v91
	v_med3_f32 v1, v1, s67, v91
	v_mov_b32_e32 v5, v69
	v_cvt_pk_fp8_f32 v5, v0, v1
	v_mul_f32_e32 v2, 0x42800000, v51
	v_mul_f32_e32 v0, 0x42800000, v39
	v_med3_f32 v1, v2, s67, v91
	v_med3_f32 v0, v0, s67, v91
	v_cvt_pk_fp8_f32 v5, v1, v0 op_sel:[0,0,1]
	v_mul_f32_e32 v0, 0x42800000, v27
	v_mul_f32_e32 v1, 0x42800000, v31
	v_med3_f32 v0, v0, s67, v91
	v_med3_f32 v1, v1, s67, v91
	v_mov_b32_e32 v6, v69
	v_cvt_pk_fp8_f32 v6, v0, v1
	v_mul_f32_e32 v2, 0x42800000, v35
	v_mul_f32_e32 v0, 0x42800000, v23
	v_cvt_pk_fp8_f32 v10, v24, v28
	v_med3_f32 v1, v2, s67, v91
	v_med3_f32 v0, v0, s67, v91
	v_cvt_pk_fp8_f32 v98, v57, v61
	v_cvt_pk_fp8_f32 v6, v1, v0 op_sel:[0,0,1]
	v_mul_f32_e32 v0, 0x42800000, v7
	v_mul_f32_e32 v1, 0x42800000, v15
	v_mul_f32_e32 v64, 0x42800000, v64
	v_mul_f32_e32 v52, 0x42800000, v52
	v_mul_f32_e32 v48, 0x42800000, v48
	v_mul_f32_e32 v36, 0x42800000, v36
	v_mul_f32_e32 v32, 0x42800000, v32
	v_mul_f32_e32 v20, 0x42800000, v20
	v_med3_f32 v0, v0, s67, v91
	v_med3_f32 v1, v1, s67, v91
	v_mov_b32_e32 v7, v69
	v_mul_f32_e32 v65, 0x42800000, v65
	v_med3_f32 v64, v64, s67, v91
	v_mul_f32_e32 v53, 0x42800000, v53
	v_med3_f32 v52, v52, s67, v91
	v_med3_f32 v48, v48, s67, v91
	v_med3_f32 v36, v36, s67, v91
	v_med3_f32 v32, v32, s67, v91
	v_med3_f32 v20, v20, s67, v91
	v_cvt_pk_fp8_f32 v7, v0, v1
	v_med3_f32 v56, v65, s67, v91
	v_med3_f32 v53, v53, s67, v91
	v_cvt_pk_fp8_f32 v8, v64, v52 op_sel:[0,0,1]
	v_cvt_pk_fp8_f32 v9, v48, v36 op_sel:[0,0,1]
	v_cvt_pk_fp8_f32 v10, v32, v20 op_sel:[0,0,1]
	v_cvt_pk_fp8_f32 v98, v56, v53 op_sel:[0,0,1]
	v_mul_f32_e32 v2, 0x42800000, v19
	v_mul_f32_e32 v0, 0x42800000, v3
	v_med3_f32 v1, v2, s67, v91
	v_med3_f32 v0, v0, s67, v91
	v_cvt_pk_fp8_f32 v7, v1, v0 op_sel:[0,0,1]
	ds_write_b128 v88, v[8:11] offset:40960
	ds_write_b128 v88, v[98:101] offset:41040
	ds_write_b128 v88, v[102:105] offset:41120
	ds_write_b128 v88, v[4:7] offset:41200
	s_waitcnt lgkmcnt(0)
	ds_read_b128 v[0:3], v89 offset:40960
	v_or_b32_e32 v4, s17, v76
	v_ashrrev_i32_e32 v5, 31, v4
	v_lshl_add_u64 v[8:9], s[28:29], 0, v[70:71]
	v_lshlrev_b64 v[4:5], 11, v[4:5]
	v_lshl_add_u64 v[10:11], v[8:9], 0, v[4:5]
	ds_read_b128 v[4:7], v89 offset:42240
	s_waitcnt lgkmcnt(1)
	global_store_dwordx4 v[10:11], v[0:3], off nt
	s_cselect_b64 s[28:29], -1, 0
	s_nop 0
	v_or_b32_e32 v0, s17, v77
	v_ashrrev_i32_e32 v1, 31, v0
	v_lshlrev_b64 v[0:1], 11, v[0:1]
	v_lshl_add_u64 v[0:1], v[8:9], 0, v[0:1]
	s_waitcnt lgkmcnt(0)
	global_store_dwordx4 v[0:1], v[4:7], off nt
	ds_read_b128 v[0:3], v89 offset:43520
	s_nop 0
	v_or_b32_e32 v4, s17, v78
	v_ashrrev_i32_e32 v5, 31, v4
	v_lshlrev_b64 v[4:5], 11, v[4:5]
	v_lshl_add_u64 v[10:11], v[8:9], 0, v[4:5]
	ds_read_b128 v[4:7], v89 offset:44800
	s_waitcnt lgkmcnt(1)
	global_store_dwordx4 v[10:11], v[0:3], off nt
	s_nop 1
	v_or_b32_e32 v0, s17, v79
	v_ashrrev_i32_e32 v1, 31, v0
	v_lshlrev_b64 v[0:1], 11, v[0:1]
	v_lshl_add_u64 v[0:1], v[8:9], 0, v[0:1]
	s_waitcnt lgkmcnt(0)
	global_store_dwordx4 v[0:1], v[4:7], off nt
	s_waitcnt lgkmcnt(0)
	s_andn2_b64 vcc, exec, s[28:29]
	s_cbranch_vccz .LBB0_1459
	s_branch .LBB0_1483

.LBB0_1459:
	s_andn2_b64 vcc, exec, s[26:27]
	s_cbranch_vccnz .LBB0_1461
	s_ashr_i32 s7, s6, 31
	s_lshl_b64 s[26:27], s[6:7], 22
	s_add_u32 s7, s55, s26
	s_addc_u32 s23, s56, s27
	v_or_b32_e32 v0, s24, v75
	s_add_u32 s7, s7, s20
	v_mul_hi_i32_i24_e32 v1, s18, v0
	v_mul_i32_i24_e32 v0, s18, v0
	s_addc_u32 s25, s23, s21
	v_lshl_add_u64 v[0:1], v[0:1], 2, s[8:9]
	s_ashr_i32 s23, s22, 31
	v_lshl_add_u64 v[0:1], s[22:23], 2, v[0:1]
	v_mov_b32_e32 v73, v69
	v_lshl_add_u64 v[0:1], v[0:1], 0, v[72:73]
	s_lshl_b64 s[26:27], s[18:19], 2
	global_load_dwordx4 v[56:59], v[0:1], off nt
	v_lshl_add_u64 v[0:1], v[0:1], 0, s[26:27]
	global_load_dwordx4 v[60:63], v[0:1], off nt
	v_lshl_add_u64 v[0:1], v[0:1], 0, s[26:27]
	global_load_dwordx4 v[64:67], v[0:1], off nt
	v_lshl_add_u64 v[0:1], v[0:1], 0, s[26:27]
	global_load_dwordx4 v[52:55], v[0:1], off nt
	v_lshl_add_u64 v[0:1], v[0:1], 0, s[26:27]
	global_load_dwordx4 v[40:43], v[0:1], off nt
	v_lshl_add_u64 v[0:1], v[0:1], 0, s[26:27]
	global_load_dwordx4 v[44:47], v[0:1], off nt
	v_lshl_add_u64 v[0:1], v[0:1], 0, s[26:27]
	global_load_dwordx4 v[48:51], v[0:1], off nt
	v_lshl_add_u64 v[0:1], v[0:1], 0, s[26:27]
	global_load_dwordx4 v[36:39], v[0:1], off nt
	v_lshl_add_u64 v[0:1], v[0:1], 0, s[26:27]
	global_load_dwordx4 v[24:27], v[0:1], off nt
	v_lshl_add_u64 v[0:1], v[0:1], 0, s[26:27]
	global_load_dwordx4 v[28:31], v[0:1], off nt
	v_lshl_add_u64 v[0:1], v[0:1], 0, s[26:27]
	global_load_dwordx4 v[32:35], v[0:1], off nt
	v_lshl_add_u64 v[0:1], v[0:1], 0, s[26:27]
	global_load_dwordx4 v[20:23], v[0:1], off nt
	v_lshl_add_u64 v[0:1], v[0:1], 0, s[26:27]
	global_load_dwordx4 v[4:7], v[0:1], off nt
	v_lshl_add_u64 v[0:1], v[0:1], 0, s[26:27]
	global_load_dwordx4 v[12:15], v[0:1], off nt
	v_lshl_add_u64 v[0:1], v[0:1], 0, s[26:27]
	global_load_dwordx4 v[16:19], v[0:1], off nt
	v_lshl_add_u64 v[0:1], v[0:1], 0, s[26:27]
	global_load_dwordx4 v[0:3], v[0:1], off nt
	v_mov_b32_e32 v11, v69
	v_mov_b32_e32 v99, v69
	v_mov_b32_e32 v100, v69
	v_mov_b32_e32 v101, v69
	v_mov_b32_e32 v102, v69
	v_mov_b32_e32 v103, v69
	v_mov_b32_e32 v104, v69
	v_mov_b32_e32 v105, v69
	v_mov_b32_e32 v8, v69
	v_mov_b32_e32 v9, v69
	v_mov_b32_e32 v10, v69
	v_mov_b32_e32 v98, v69
	s_ashr_i32 s23, s24, 31
	s_add_u32 s26, s7, s24
	s_addc_u32 s27, s25, s23
	s_cmpk_lt_u32 s57, 0xf97f
	s_waitcnt vmcnt(15)
	v_mul_f32_e32 v56, 0x42800000, v56
	v_mul_f32_e32 v57, 0x42800000, v57
	s_waitcnt vmcnt(14)
	v_mul_f32_e32 v60, 0x42800000, v60
	v_med3_f32 v56, v56, s67, v91
	v_mul_f32_e32 v61, 0x42800000, v61
	v_med3_f32 v60, v60, s67, v91
	v_med3_f32 v57, v57, s67, v91
	v_med3_f32 v61, v61, s67, v91
	s_waitcnt vmcnt(11)
	v_mul_f32_e32 v41, 0x42800000, v41
	v_med3_f32 v41, v41, s67, v91
	s_waitcnt vmcnt(10)
	v_mul_f32_e32 v45, 0x42800000, v45
	v_med3_f32 v45, v45, s67, v91
	v_cvt_pk_fp8_f32 v99, v41, v45
	s_waitcnt vmcnt(9)
	v_mul_f32_e32 v49, 0x42800000, v49
	v_mul_f32_e32 v40, 0x42800000, v40
	v_mul_f32_e32 v44, 0x42800000, v44
	s_waitcnt vmcnt(7)
	v_mul_f32_e32 v24, 0x42800000, v24
	v_med3_f32 v40, v40, s67, v91
	s_waitcnt vmcnt(6)
	v_mul_f32_e32 v28, 0x42800000, v28
	v_med3_f32 v44, v44, s67, v91
	v_med3_f32 v24, v24, s67, v91
	v_med3_f32 v28, v28, s67, v91
	v_cvt_pk_fp8_f32 v8, v56, v60
	v_cvt_pk_fp8_f32 v9, v40, v44
	s_waitcnt vmcnt(3)
	v_mul_f32_e32 v4, 0x42800000, v4
	v_med3_f32 v4, v4, s67, v91
	s_waitcnt vmcnt(2)
	v_mul_f32_e32 v12, 0x42800000, v12
	v_med3_f32 v12, v12, s67, v91
	v_cvt_pk_fp8_f32 v11, v4, v12
	s_waitcnt vmcnt(1)
	v_mul_f32_e32 v16, 0x42800000, v16
	s_waitcnt vmcnt(0)
	v_mul_f32_e32 v0, 0x42800000, v0
	v_med3_f32 v4, v16, s67, v91
	v_med3_f32 v0, v0, s67, v91
	v_cvt_pk_fp8_f32 v11, v4, v0 op_sel:[0,0,1]
	v_mul_f32_e32 v0, 0x42800000, v37
	v_med3_f32 v4, v49, s67, v91
	v_med3_f32 v0, v0, s67, v91
	v_cvt_pk_fp8_f32 v99, v4, v0 op_sel:[0,0,1]
	v_mul_f32_e32 v0, 0x42800000, v25
	v_mul_f32_e32 v4, 0x42800000, v29
	v_med3_f32 v0, v0, s67, v91
	v_med3_f32 v4, v4, s67, v91
	v_cvt_pk_fp8_f32 v100, v0, v4
	v_mul_f32_e32 v12, 0x42800000, v33
	v_mul_f32_e32 v0, 0x42800000, v21
	v_med3_f32 v4, v12, s67, v91
	v_med3_f32 v0, v0, s67, v91
	v_cvt_pk_fp8_f32 v100, v4, v0 op_sel:[0,0,1]
	v_mul_f32_e32 v0, 0x42800000, v5
	v_mul_f32_e32 v4, 0x42800000, v13
	v_med3_f32 v0, v0, s67, v91
	v_med3_f32 v4, v4, s67, v91
	v_cvt_pk_fp8_f32 v101, v0, v4
	v_mul_f32_e32 v5, 0x42800000, v17
	v_mul_f32_e32 v0, 0x42800000, v1
	v_med3_f32 v1, v5, s67, v91
	v_med3_f32 v0, v0, s67, v91
	v_cvt_pk_fp8_f32 v101, v1, v0 op_sel:[0,0,1]
	v_mul_f32_e32 v0, 0x42800000, v58
	v_mul_f32_e32 v1, 0x42800000, v62
	v_med3_f32 v0, v0, s67, v91
	v_med3_f32 v1, v1, s67, v91
	v_cvt_pk_fp8_f32 v102, v0, v1
	v_mul_f32_e32 v4, 0x42800000, v66
	v_mul_f32_e32 v0, 0x42800000, v54
	v_med3_f32 v1, v4, s67, v91
	v_med3_f32 v0, v0, s67, v91
	v_cvt_pk_fp8_f32 v102, v1, v0 op_sel:[0,0,1]
	v_mul_f32_e32 v0, 0x42800000, v42
	v_mul_f32_e32 v1, 0x42800000, v46
	v_med3_f32 v0, v0, s67, v91
	v_med3_f32 v1, v1, s67, v91
	v_cvt_pk_fp8_f32 v103, v0, v1
	v_mul_f32_e32 v4, 0x42800000, v50
	v_mul_f32_e32 v0, 0x42800000, v38
	v_med3_f32 v1, v4, s67, v91
	v_med3_f32 v0, v0, s67, v91
	v_cvt_pk_fp8_f32 v103, v1, v0 op_sel:[0,0,1]
	v_mul_f32_e32 v0, 0x42800000, v26
	v_mul_f32_e32 v1, 0x42800000, v30
	v_med3_f32 v0, v0, s67, v91
	v_med3_f32 v1, v1, s67, v91
	v_cvt_pk_fp8_f32 v104, v0, v1
	v_mul_f32_e32 v4, 0x42800000, v34
	v_mul_f32_e32 v0, 0x42800000, v22
	v_med3_f32 v1, v4, s67, v91
	v_med3_f32 v0, v0, s67, v91
	v_cvt_pk_fp8_f32 v104, v1, v0 op_sel:[0,0,1]
	v_mul_f32_e32 v0, 0x42800000, v6
	v_mul_f32_e32 v1, 0x42800000, v14
	v_med3_f32 v0, v0, s67, v91
	v_med3_f32 v1, v1, s67, v91
	v_cvt_pk_fp8_f32 v105, v0, v1
	v_mul_f32_e32 v4, 0x42800000, v18
	v_mul_f32_e32 v0, 0x42800000, v2
	v_med3_f32 v1, v4, s67, v91
	v_med3_f32 v0, v0, s67, v91
	v_cvt_pk_fp8_f32 v105, v1, v0 op_sel:[0,0,1]
	v_mul_f32_e32 v0, 0x42800000, v59
	v_mul_f32_e32 v1, 0x42800000, v63
	v_med3_f32 v0, v0, s67, v91
	v_med3_f32 v1, v1, s67, v91
	v_mov_b32_e32 v4, v69
	v_cvt_pk_fp8_f32 v4, v0, v1
	v_mul_f32_e32 v2, 0x42800000, v67
	v_mul_f32_e32 v0, 0x42800000, v55
	v_med3_f32 v1, v2, s67, v91
	v_med3_f32 v0, v0, s67, v91
	v_cvt_pk_fp8_f32 v4, v1, v0 op_sel:[0,0,1]
	v_mul_f32_e32 v0, 0x42800000, v43
	v_mul_f32_e32 v1, 0x42800000, v47
	v_med3_f32 v0, v0, s67, v91
	v_med3_f32 v1, v1, s67, v91
	v_mov_b32_e32 v5, v69
	v_cvt_pk_fp8_f32 v5, v0, v1
	v_mul_f32_e32 v2, 0x42800000, v51
	v_mul_f32_e32 v0, 0x42800000, v39
	v_med3_f32 v1, v2, s67, v91
	v_med3_f32 v0, v0, s67, v91
	v_cvt_pk_fp8_f32 v5, v1, v0 op_sel:[0,0,1]
	v_mul_f32_e32 v0, 0x42800000, v27
	v_mul_f32_e32 v1, 0x42800000, v31
	v_med3_f32 v0, v0, s67, v91
	v_med3_f32 v1, v1, s67, v91
	v_mov_b32_e32 v6, v69
	v_cvt_pk_fp8_f32 v6, v0, v1
	v_mul_f32_e32 v2, 0x42800000, v35
	v_mul_f32_e32 v0, 0x42800000, v23
	v_cvt_pk_fp8_f32 v10, v24, v28
	v_med3_f32 v1, v2, s67, v91
	v_med3_f32 v0, v0, s67, v91
	v_cvt_pk_fp8_f32 v98, v57, v61
	v_cvt_pk_fp8_f32 v6, v1, v0 op_sel:[0,0,1]
	v_mul_f32_e32 v0, 0x42800000, v7
	v_mul_f32_e32 v1, 0x42800000, v15
	v_mul_f32_e32 v64, 0x42800000, v64
	v_mul_f32_e32 v52, 0x42800000, v52
	v_mul_f32_e32 v48, 0x42800000, v48
	v_mul_f32_e32 v36, 0x42800000, v36
	v_mul_f32_e32 v32, 0x42800000, v32
	v_mul_f32_e32 v20, 0x42800000, v20
	v_med3_f32 v0, v0, s67, v91
	v_med3_f32 v1, v1, s67, v91
	v_mov_b32_e32 v7, v69
	v_mul_f32_e32 v65, 0x42800000, v65
	v_med3_f32 v64, v64, s67, v91
	v_mul_f32_e32 v53, 0x42800000, v53
	v_med3_f32 v52, v52, s67, v91
	v_med3_f32 v48, v48, s67, v91
	v_med3_f32 v36, v36, s67, v91
	v_med3_f32 v32, v32, s67, v91
	v_med3_f32 v20, v20, s67, v91
	v_cvt_pk_fp8_f32 v7, v0, v1
	v_med3_f32 v56, v65, s67, v91
	v_med3_f32 v53, v53, s67, v91
	v_cvt_pk_fp8_f32 v8, v64, v52 op_sel:[0,0,1]
	v_cvt_pk_fp8_f32 v9, v48, v36 op_sel:[0,0,1]
	v_cvt_pk_fp8_f32 v10, v32, v20 op_sel:[0,0,1]
	v_cvt_pk_fp8_f32 v98, v56, v53 op_sel:[0,0,1]
	v_mul_f32_e32 v2, 0x42800000, v19
	v_mul_f32_e32 v0, 0x42800000, v3
	v_med3_f32 v1, v2, s67, v91
	v_med3_f32 v0, v0, s67, v91
	v_cvt_pk_fp8_f32 v7, v1, v0 op_sel:[0,0,1]
	ds_write_b128 v88, v[8:11] offset:40960
	ds_write_b128 v88, v[98:101] offset:41040
	ds_write_b128 v88, v[102:105] offset:41120
	ds_write_b128 v88, v[4:7] offset:41200
	s_waitcnt lgkmcnt(0)
	ds_read_b128 v[0:3], v89 offset:40960
	v_or_b32_e32 v4, s17, v76
	v_ashrrev_i32_e32 v5, 31, v4
	v_lshl_add_u64 v[8:9], s[26:27], 0, v[70:71]
	v_lshlrev_b64 v[4:5], 11, v[4:5]
	v_lshl_add_u64 v[10:11], v[8:9], 0, v[4:5]
	ds_read_b128 v[4:7], v89 offset:42240
	s_waitcnt lgkmcnt(1)
	global_store_dwordx4 v[10:11], v[0:3], off nt
	s_cselect_b64 s[26:27], -1, 0
	s_nop 0
	v_or_b32_e32 v0, s17, v77
	v_ashrrev_i32_e32 v1, 31, v0
	v_lshlrev_b64 v[0:1], 11, v[0:1]
	v_lshl_add_u64 v[0:1], v[8:9], 0, v[0:1]
	s_waitcnt lgkmcnt(0)
	global_store_dwordx4 v[0:1], v[4:7], off nt
	ds_read_b128 v[0:3], v89 offset:43520
	s_nop 0
	v_or_b32_e32 v4, s17, v78
	v_ashrrev_i32_e32 v5, 31, v4
	v_lshlrev_b64 v[4:5], 11, v[4:5]
	v_lshl_add_u64 v[10:11], v[8:9], 0, v[4:5]
	ds_read_b128 v[4:7], v89 offset:44800
	s_waitcnt lgkmcnt(1)
	global_store_dwordx4 v[10:11], v[0:3], off nt
	s_nop 1
	v_or_b32_e32 v0, s17, v79
	v_ashrrev_i32_e32 v1, 31, v0
	v_lshlrev_b64 v[0:1], 11, v[0:1]
	v_lshl_add_u64 v[0:1], v[8:9], 0, v[0:1]
	s_waitcnt lgkmcnt(0)
	global_store_dwordx4 v[0:1], v[4:7], off nt
	s_waitcnt lgkmcnt(0)
	s_andn2_b64 vcc, exec, s[26:27]
	s_cbranch_vccz .LBB0_1462
	s_branch .LBB0_1483

.LBB0_1466:
	s_lshl_b64 s[20:21], s[20:21], 1
	s_add_u32 s7, s12, s20
	s_addc_u32 s20, s13, s21
	s_ashr_i32 s25, s24, 31
	s_lshl_b64 s[12:13], s[24:25], 1
	s_waitcnt lgkmcnt(0)
	s_add_u32 s12, s7, s12
	s_addc_u32 s13, s20, s13
	v_or_b32_e32 v0, s17, v80
	v_lshl_add_u64 v[4:5], s[12:13], 0, v[68:69]
	s_mov_b64 s[12:13], -1
	s_and_b64 vcc, exec, s[26:27]
	v_mul_hi_i32_i24_e32 v7, s16, v0
	v_mul_i32_i24_e32 v6, s16, v0
	s_cbranch_vccz .LBB0_1468
	v_lshl_add_u64 v[0:1], v[6:7], 1, v[4:5]
	global_store_dwordx4 v[0:1], v[94:97], off nt
	s_mov_b64 s[12:13], 0
.LBB0_1468:
	v_mov_b32_e32 v0, 0
	s_andn2_b64 vcc, exec, s[12:13]
	v_mov_b32_e32 v1, 0
	v_mov_b32_e32 v2, 0
	v_mov_b32_e32 v3, 0
	s_cbranch_vccnz .LBB0_1470
	ds_read_b128 v[8:11], v92 offset:40960
	ds_read_b128 v[0:3], v92 offset:42112
	v_lshl_add_u64 v[6:7], v[6:7], 1, v[4:5]
	s_waitcnt lgkmcnt(1)
	global_store_dwordx4 v[6:7], v[8:11], off nt
.LBB0_1470:
	v_or_b32_e32 v6, s17, v81
	v_mul_hi_i32_i24_e32 v7, s16, v6
	v_mul_i32_i24_e32 v6, s16, v6
	v_lshl_add_u64 v[6:7], v[6:7], 1, v[4:5]
	s_waitcnt lgkmcnt(0)
	global_store_dwordx4 v[6:7], v[0:3], off nt
	s_mov_b64 s[12:13], -1
	s_and_b64 vcc, exec, s[26:27]
	v_or_b32_e32 v0, s17, v82
	v_mul_hi_i32_i24_e32 v7, s16, v0
	v_mul_i32_i24_e32 v6, s16, v0
	s_cbranch_vccz .LBB0_1472
	v_lshl_add_u64 v[0:1], v[6:7], 1, v[4:5]
	global_store_dwordx4 v[0:1], v[94:97], off nt
	s_mov_b64 s[12:13], 0
.LBB0_1472:
	v_mov_b32_e32 v0, 0
	s_andn2_b64 vcc, exec, s[12:13]
	v_mov_b32_e32 v1, 0
	v_mov_b32_e32 v2, 0
	v_mov_b32_e32 v3, 0
	s_cbranch_vccnz .LBB0_1474
	ds_read_b128 v[8:11], v92 offset:43264
	ds_read_b128 v[0:3], v92 offset:44416
	v_lshl_add_u64 v[6:7], v[6:7], 1, v[4:5]
	s_waitcnt lgkmcnt(1)
	global_store_dwordx4 v[6:7], v[8:11], off nt
.LBB0_1474:
	v_or_b32_e32 v6, s17, v83
	v_mul_hi_i32_i24_e32 v7, s16, v6
	v_mul_i32_i24_e32 v6, s16, v6
	v_lshl_add_u64 v[6:7], v[6:7], 1, v[4:5]
	s_waitcnt lgkmcnt(0)
	global_store_dwordx4 v[6:7], v[0:3], off nt
	s_mov_b64 s[12:13], -1
	s_and_b64 vcc, exec, s[26:27]
	v_or_b32_e32 v0, s17, v84
	v_mul_hi_i32_i24_e32 v7, s16, v0
	v_mul_i32_i24_e32 v6, s16, v0
	s_cbranch_vccz .LBB0_1476
	v_lshl_add_u64 v[0:1], v[6:7], 1, v[4:5]
	global_store_dwordx4 v[0:1], v[94:97], off nt
	s_mov_b64 s[12:13], 0
.LBB0_1476:
	v_mov_b32_e32 v0, 0
	s_andn2_b64 vcc, exec, s[12:13]
	v_mov_b32_e32 v1, 0
	v_mov_b32_e32 v2, 0
	v_mov_b32_e32 v3, 0
	s_cbranch_vccnz .LBB0_1478
	ds_read_b128 v[8:11], v92 offset:45568
	ds_read_b128 v[0:3], v92 offset:46720
	v_lshl_add_u64 v[6:7], v[6:7], 1, v[4:5]
	s_waitcnt lgkmcnt(1)
	global_store_dwordx4 v[6:7], v[8:11], off nt
.LBB0_1478:
	v_or_b32_e32 v6, s17, v85
	v_mul_hi_i32_i24_e32 v7, s16, v6
	v_mul_i32_i24_e32 v6, s16, v6
	v_lshl_add_u64 v[6:7], v[6:7], 1, v[4:5]
	s_waitcnt lgkmcnt(0)
	global_store_dwordx4 v[6:7], v[0:3], off nt
	s_mov_b64 s[12:13], -1
	s_and_b64 vcc, exec, s[26:27]
	v_or_b32_e32 v0, s17, v86
	v_mul_hi_i32_i24_e32 v7, s16, v0
	v_mul_i32_i24_e32 v6, s16, v0
	s_cbranch_vccz .LBB0_1480
	v_lshl_add_u64 v[0:1], v[6:7], 1, v[4:5]
	global_store_dwordx4 v[0:1], v[94:97], off nt
	s_mov_b64 s[12:13], 0
.LBB0_1480:
	v_mov_b32_e32 v0, 0
	s_andn2_b64 vcc, exec, s[12:13]
	v_mov_b32_e32 v1, 0
	v_mov_b32_e32 v2, 0
	v_mov_b32_e32 v3, 0
	s_cbranch_vccnz .LBB0_1482
	ds_read_b128 v[8:11], v92 offset:47872
	ds_read_b128 v[0:3], v92 offset:49024
	v_lshl_add_u64 v[6:7], v[6:7], 1, v[4:5]
	s_waitcnt lgkmcnt(1)
	global_store_dwordx4 v[6:7], v[8:11], off nt
.LBB0_1482:
	v_or_b32_e32 v6, s17, v87
	v_mul_hi_i32_i24_e32 v7, s16, v6
	v_mul_i32_i24_e32 v6, s16, v6
	v_lshl_add_u64 v[4:5], v[6:7], 1, v[4:5]
	s_waitcnt lgkmcnt(0)
	global_store_dwordx4 v[4:5], v[0:3], off nt
	s_waitcnt lgkmcnt(0)
